# GEMM tile loops: first K-loop iteration of tiles 2.. peeled; its first two counted waits no longer wait for the previous tile's epilogue stores (vmcnt is in-order)
# speedup vs baseline: 1.0116x; 1.0060x over previous
; #define PG8_STAGE(bufoff, gbase, voff) do { _Pragma("unroll") for (int _i = 0; _i < 2; ++_i) \
;         __builtin_amdgcn_global_load_lds((const unsigned*)((const char*)(gbase) + (voff)[_i]), (LAS unsigned*)(lds + (bufoff) + ldsw + _i * 8192), 16, 0, 0); } while (0)
; #define PG8_LDA(dst, b, h) do { _Pragma("unroll") for (int m = 0; m < 4; ++m) _Pragma("unroll") for (int k = 0; k < 2; ++k) dst[m][k] = *(const LAS bf16x8*)(lds + PG8_SA(b, h) + aoff + m * 2048 + k * 1024); } while (0)
; #define PG8_LDB(dst, b, h) do { _Pragma("unroll") for (int n = 0; n < 2; ++n) _Pragma("unroll") for (int k = 0; k < 2; ++k) dst[n][k] = *(const LAS bf16x8*)(lds + PG8_SB(b, h) + boff + n * 2048 + k * 1024); } while (0)
; #define PG8_MMA(ai, bj, At, Bt) do { __builtin_amdgcn_s_setprio(1); _Pragma("unroll") for (int m = 0; m < 4; ++m) _Pragma("unroll") for (int n = 0; n < 2; ++n) _Pragma("unroll") for (int k = 0; k < 2; ++k) \
;         acc[ai][bj][m][n] = __builtin_amdgcn_mfma_f32_16x16x32_bf16(Bt[n][k], At[m][k], acc[ai][bj][m][n], 0, 0, 0); __builtin_amdgcn_s_setprio(0); } while (0)
; #define PG8_WAIT_V(n) asm volatile("s_waitcnt vmcnt(" #n ")" ::: "memory")
; #define PG8_WAIT_L(n) asm volatile("s_waitcnt lgkmcnt(" #n ")" ::: "memory")
; template <class Epi, class Sched>
; __device__ __forceinline__ void gemm_phase(LAS unsigned char* lds, const Gemm g, const Sched& S, const Epi& E, const int tid, unsigned* last_sig = nullptr) {
;     ...
;         for (int t = 0; t < nt; t += 2) {
;             const bool last = (t == nt - 2);
;             const char* a1 = cA + (size_t)(t + 1) * kstep;
;             const char* a2 = last ? nA : cA + (size_t)(t + 2) * kstep; const char* b2 = last ? nB : cB + (size_t)(t + 2) * kstep;
;             const char* a3 = a2 + kstep; const char* b3 = b2 + kstep;
;             PG8_LDB(B0, 0, 0); PG8_LDB(B1, 0, 1); PG8_SCHED; PG8_LDA(At, 0, 0); PG8_STAGE(PG8_SA(1, 1), a1 + hstep, voffA);
;             PG8_WAIT_V(8); PG8_WAIT_L(0); PG8_BAR; PG8_MMA(0, 0, At, B0); PG8_MMA(0, 1, At, B1); PG8_BAR; PG8_SCHED;
;     ...
; #pragma unroll
;         for (int a = 0; a < 2; ++a)
; #pragma unroll
;             for (int b = 0; b < 2; ++b)
; #pragma unroll
;                 for (int m = 0; m < 4; ++m)
; #pragma unroll
;                     for (int n = 0; n < 2; ++n) acc[a][b][m][n] = (f32x4){0.f, 0.f, 0.f, 0.f};
;         cur = nxt; cA = nA; cB = nB; ++ui;
.LBB0_171:
	s_ashr_i32 s13, s12, 31
	s_lshl_b64 s[16:17], s[12:13], 20
	v_readlane_b32 s14, v253, 46
	v_readlane_b32 s15, v253, 47
	s_add_u32 s16, s14, s16
	s_addc_u32 s17, s15, s17
	s_and_b64 s[18:19], s[38:39], exec
	s_cselect_b32 s13, s17, s21
	s_cselect_b32 s28, s16, s20
	s_ashr_i32 s11, s10, 31
	s_lshl_b64 s[18:19], s[10:11], 20
	s_add_u32 s18, s31, s18
	s_addc_u32 s19, s42, s19
	s_and_b64 s[40:41], s[38:39], exec
	s_cselect_b32 s11, s19, s23
	s_cselect_b32 s56, s18, s22
	s_add_u32 s20, s20, 0x80080
	s_addc_u32 s21, s21, 0
	s_add_u32 s57, s22, 0x100
	v_mov_b32_e32 v2, 0
	s_addc_u32 s58, s23, 0
	s_mov_b32 s59, -2
	v_mov_b32_e32 v3, v2
	v_mov_b32_e32 v4, v2
	v_mov_b32_e32 v5, v2
	v_mov_b32_e32 v6, v2
	v_mov_b32_e32 v7, v2
	v_mov_b32_e32 v8, v2
	v_mov_b32_e32 v9, v2
	v_mov_b32_e32 v10, v2
	v_mov_b32_e32 v11, v2
	v_mov_b32_e32 v12, v2
	v_mov_b32_e32 v13, v2
	v_mov_b32_e32 v18, v2
	v_mov_b32_e32 v19, v2
	v_mov_b32_e32 v20, v2
	v_mov_b32_e32 v21, v2
	v_mov_b32_e32 v26, v2
	v_mov_b32_e32 v27, v2
	v_mov_b32_e32 v28, v2
	v_mov_b32_e32 v29, v2
	v_mov_b32_e32 v34, v2
	v_mov_b32_e32 v35, v2
	v_mov_b32_e32 v36, v2
	v_mov_b32_e32 v37, v2
	v_mov_b32_e32 v42, v2
	v_mov_b32_e32 v43, v2
	v_mov_b32_e32 v44, v2
	v_mov_b32_e32 v45, v2
	v_mov_b32_e32 v50, v2
	v_mov_b32_e32 v51, v2
	v_mov_b32_e32 v52, v2
	v_mov_b32_e32 v53, v2
	v_mov_b32_e32 v14, v2
	v_mov_b32_e32 v15, v2
	v_mov_b32_e32 v16, v2
	v_mov_b32_e32 v17, v2
	v_mov_b32_e32 v22, v2
	v_mov_b32_e32 v23, v2
	v_mov_b32_e32 v24, v2
	v_mov_b32_e32 v25, v2
	v_mov_b32_e32 v30, v2
	v_mov_b32_e32 v31, v2
	v_mov_b32_e32 v32, v2
	v_mov_b32_e32 v33, v2
	v_mov_b32_e32 v38, v2
	v_mov_b32_e32 v39, v2
	v_mov_b32_e32 v40, v2
	v_mov_b32_e32 v41, v2
	v_mov_b32_e32 v46, v2
	v_mov_b32_e32 v47, v2
	v_mov_b32_e32 v48, v2
	v_mov_b32_e32 v49, v2
	v_mov_b32_e32 v54, v2
	v_mov_b32_e32 v55, v2
	v_mov_b32_e32 v56, v2
	v_mov_b32_e32 v57, v2
	v_mov_b32_e32 v58, v2
	v_mov_b32_e32 v59, v2
	v_mov_b32_e32 v60, v2
	v_mov_b32_e32 v61, v2
	v_mov_b32_e32 v62, v2
	v_mov_b32_e32 v63, v2
	v_mov_b32_e32 v64, v2
	v_mov_b32_e32 v65, v2
	v_mov_b32_e32 v66, v2
	v_mov_b32_e32 v67, v2
	v_mov_b32_e32 v68, v2
	v_mov_b32_e32 v69, v2
	v_mov_b32_e32 v70, v2
	v_mov_b32_e32 v71, v2
	v_mov_b32_e32 v72, v2
	v_mov_b32_e32 v73, v2
	v_mov_b32_e32 v74, v2
	v_mov_b32_e32 v75, v2
	v_mov_b32_e32 v76, v2
	v_mov_b32_e32 v77, v2
	v_mov_b32_e32 v82, v2
	v_mov_b32_e32 v83, v2
	v_mov_b32_e32 v84, v2
	v_mov_b32_e32 v85, v2
	v_mov_b32_e32 v90, v2
	v_mov_b32_e32 v91, v2
	v_mov_b32_e32 v92, v2
	v_mov_b32_e32 v93, v2
	v_mov_b32_e32 v98, v2
	v_mov_b32_e32 v99, v2
	v_mov_b32_e32 v100, v2
	v_mov_b32_e32 v101, v2
	v_mov_b32_e32 v106, v2
	v_mov_b32_e32 v107, v2
	v_mov_b32_e32 v108, v2
	v_mov_b32_e32 v109, v2
	v_mov_b32_e32 v114, v2
	v_mov_b32_e32 v115, v2
	v_mov_b32_e32 v116, v2
	v_mov_b32_e32 v117, v2
	v_mov_b32_e32 v78, v2
	v_mov_b32_e32 v79, v2
	v_mov_b32_e32 v80, v2
	v_mov_b32_e32 v81, v2
	v_mov_b32_e32 v86, v2
	v_mov_b32_e32 v87, v2
	v_mov_b32_e32 v88, v2
	v_mov_b32_e32 v89, v2
	v_mov_b32_e32 v94, v2
	v_mov_b32_e32 v95, v2
	v_mov_b32_e32 v96, v2
	v_mov_b32_e32 v97, v2
	v_mov_b32_e32 v102, v2
	v_mov_b32_e32 v103, v2
	v_mov_b32_e32 v104, v2
	v_mov_b32_e32 v105, v2
	v_mov_b32_e32 v110, v2
	v_mov_b32_e32 v111, v2
	v_mov_b32_e32 v112, v2
	v_mov_b32_e32 v113, v2
	v_mov_b32_e32 v118, v2
	v_mov_b32_e32 v119, v2
	v_mov_b32_e32 v120, v2
	v_mov_b32_e32 v121, v2
	v_mov_b32_e32 v122, v2
	v_mov_b32_e32 v123, v2
	v_mov_b32_e32 v124, v2
	v_mov_b32_e32 v125, v2
	v_mov_b32_e32 v126, v2
	v_mov_b32_e32 v127, v2
	v_mov_b32_e32 v128, v2
	v_mov_b32_e32 v129, v2
	s_cmp_eq_u32 s53, 1
	s_cbranch_scc1 .LBB0_172
	s_add_u32 s14, s20, 0xfff80080
	s_addc_u32 s15, s21, -1
	s_add_i32 s60, 0, 0x10000
	s_cmp_eq_u32 s59, 28
	s_cselect_b32 s41, s13, s15
	s_cselect_b32 s40, s28, s14
	s_cselect_b32 s23, s11, s58
	s_cselect_b32 s22, s56, s57
	s_add_i32 s14, 0, 0x14000
	v_add_u32_e32 v160, s60, v145
	v_add_u32_e32 v176, s14, v145
	ds_read_b128 v[130:133], v160
	ds_read_b128 v[152:155], v160 offset:1024
	ds_read_b128 v[156:159], v160 offset:2048
	ds_read_b128 v[160:163], v160 offset:3072
	ds_read_b128 v[164:167], v176
	ds_read_b128 v[168:171], v176 offset:1024
	ds_read_b128 v[172:175], v176 offset:2048
	ds_read_b128 v[176:179], v176 offset:3072
	v_lshl_add_u64 v[184:185], s[20:21], 0, v[148:149]
	s_add_i32 m0, s44, 0xc000
	ds_read_b128 v[180:183], v147
	ds_read_b128 v[200:203], v147 offset:1024
	ds_read_b128 v[204:207], v147 offset:2048
	ds_read_b128 v[208:211], v147 offset:3072
	ds_read_b128 v[212:215], v147 offset:4096
	ds_read_b128 v[216:219], v147 offset:5120
	ds_read_b128 v[220:223], v147 offset:6144
	ds_read_b128 v[232:235], v147 offset:7168
	global_load_lds_dwordx4 v[184:185], off
	v_lshl_add_u64 v[184:185], s[20:21], 0, v[150:151]
	s_add_i32 m0, s44, 0xe000
	s_nop 0
	global_load_lds_dwordx4 v[184:185], off
	s_waitcnt vmcnt(24)
	s_waitcnt lgkmcnt(0)
	s_barrier
; #define PG8_STAGE(bufoff, gbase, voff) do { _Pragma("unroll") for (int _i = 0; _i < 2; ++_i) \
;         __builtin_amdgcn_global_load_lds((const unsigned*)((const char*)(gbase) + (voff)[_i]), (LAS unsigned*)(lds + (bufoff) + ldsw + _i * 8192), 16, 0, 0); } while (0)
; #define PG8_LDA(dst, b, h) do { _Pragma("unroll") for (int m = 0; m < 4; ++m) _Pragma("unroll") for (int k = 0; k < 2; ++k) dst[m][k] = *(const LAS bf16x8*)(lds + PG8_SA(b, h) + aoff + m * 2048 + k * 1024); } while (0)
; #define PG8_LDB(dst, b, h) do { _Pragma("unroll") for (int n = 0; n < 2; ++n) _Pragma("unroll") for (int k = 0; k < 2; ++k) dst[n][k] = *(const LAS bf16x8*)(lds + PG8_SB(b, h) + boff + n * 2048 + k * 1024); } while (0)
; #define PG8_MMA(ai, bj, At, Bt) do { __builtin_amdgcn_s_setprio(1); _Pragma("unroll") for (int m = 0; m < 4; ++m) _Pragma("unroll") for (int n = 0; n < 2; ++n) _Pragma("unroll") for (int k = 0; k < 2; ++k) \
;         acc[ai][bj][m][n] = __builtin_amdgcn_mfma_f32_16x16x32_bf16(Bt[n][k], At[m][k], acc[ai][bj][m][n], 0, 0, 0); __builtin_amdgcn_s_setprio(0); } while (0)
; #define PG8_WAIT_V(n) asm volatile("s_waitcnt vmcnt(" #n ")" ::: "memory")
; #define PG8_WAIT_L(n) asm volatile("s_waitcnt lgkmcnt(" #n ")" ::: "memory")
; #define PG8_BAR __builtin_amdgcn_s_barrier()
; #define PG8_SCHED __builtin_amdgcn_sched_barrier(0)
; template <class Epi, class Sched>
; __device__ __forceinline__ void gemm_phase(LAS unsigned char* lds, const Gemm g, const Sched& S, const Epi& E, const int tid, unsigned* last_sig = nullptr) {
;     ...
;             PG8_LDB(B0, 0, 0); PG8_LDB(B1, 0, 1); PG8_SCHED; PG8_LDA(At, 0, 0); PG8_STAGE(PG8_SA(1, 1), a1 + hstep, voffA);
;             PG8_WAIT_V(8); PG8_WAIT_L(0); PG8_BAR; PG8_MMA(0, 0, At, B0); PG8_MMA(0, 1, At, B1); PG8_BAR; PG8_SCHED;
;             PG8_LDA(At, 0, 1); PG8_STAGE(PG8_SB(0, 0), b2, voffB); PG8_STAGE(PG8_SB(0, 1), b2 + hstep, voffB); PG8_STAGE(PG8_SA(0, 0), a2, voffA);
;             PG8_WAIT_V(8); PG8_WAIT_L(0); PG8_BAR; PG8_MMA(1, 0, At, B0); PG8_MMA(1, 1, At, B1); PG8_BAR; PG8_SCHED;
	s_setprio 1
	s_waitcnt lgkmcnt(0)
	v_mfma_f32_16x16x32_bf16 v[126:129], v[130:133], v[180:183], v[126:129]
	v_mfma_f32_16x16x32_bf16 v[122:125], v[156:159], v[180:183], v[122:125]
	v_mfma_f32_16x16x32_bf16 v[118:121], v[130:133], v[204:207], v[118:121]
	v_mfma_f32_16x16x32_bf16 v[110:113], v[156:159], v[204:207], v[110:113]
	v_mfma_f32_16x16x32_bf16 v[102:105], v[130:133], v[212:215], v[102:105]
	v_mfma_f32_16x16x32_bf16 v[94:97], v[156:159], v[212:215], v[94:97]
	v_mfma_f32_16x16x32_bf16 v[86:89], v[130:133], v[220:223], v[86:89]
	v_mfma_f32_16x16x32_bf16 v[78:81], v[156:159], v[220:223], v[78:81]
	v_mfma_f32_16x16x32_bf16 v[126:129], v[152:155], v[200:203], v[126:129]
	v_mfma_f32_16x16x32_bf16 v[122:125], v[160:163], v[200:203], v[122:125]
	v_mfma_f32_16x16x32_bf16 v[118:121], v[152:155], v[208:211], v[118:121]
	v_mfma_f32_16x16x32_bf16 v[110:113], v[160:163], v[208:211], v[110:113]
	v_mfma_f32_16x16x32_bf16 v[102:105], v[152:155], v[216:219], v[102:105]
	v_mfma_f32_16x16x32_bf16 v[94:97], v[160:163], v[216:219], v[94:97]
	v_mfma_f32_16x16x32_bf16 v[86:89], v[152:155], v[232:235], v[86:89]
	v_mfma_f32_16x16x32_bf16 v[78:81], v[160:163], v[232:235], v[78:81]
	s_setprio 0
	s_setprio 1
	v_mfma_f32_16x16x32_bf16 v[114:117], v[164:167], v[180:183], v[114:117]
	v_mfma_f32_16x16x32_bf16 v[106:109], v[172:175], v[180:183], v[106:109]
	v_mfma_f32_16x16x32_bf16 v[98:101], v[164:167], v[204:207], v[98:101]
	v_mfma_f32_16x16x32_bf16 v[90:93], v[172:175], v[204:207], v[90:93]
	v_mfma_f32_16x16x32_bf16 v[82:85], v[164:167], v[212:215], v[82:85]
	v_mfma_f32_16x16x32_bf16 v[74:77], v[172:175], v[212:215], v[74:77]
	v_mfma_f32_16x16x32_bf16 v[70:73], v[164:167], v[220:223], v[70:73]
	v_mfma_f32_16x16x32_bf16 v[66:69], v[172:175], v[220:223], v[66:69]
	v_mfma_f32_16x16x32_bf16 v[114:117], v[168:171], v[200:203], v[114:117]
	v_mfma_f32_16x16x32_bf16 v[106:109], v[176:179], v[200:203], v[106:109]
	v_mfma_f32_16x16x32_bf16 v[98:101], v[168:171], v[208:211], v[98:101]
	v_mfma_f32_16x16x32_bf16 v[90:93], v[176:179], v[208:211], v[90:93]
	v_mfma_f32_16x16x32_bf16 v[82:85], v[168:171], v[216:219], v[82:85]
	v_mfma_f32_16x16x32_bf16 v[74:77], v[176:179], v[216:219], v[74:77]
	v_mfma_f32_16x16x32_bf16 v[70:73], v[168:171], v[232:235], v[70:73]
	v_mfma_f32_16x16x32_bf16 v[66:69], v[176:179], v[232:235], v[66:69]
	s_setprio 0
	s_barrier
	s_add_i32 s15, s60, s43
	v_lshl_add_u64 v[184:185], s[22:23], 0, v[138:139]
	s_mov_b32 m0, s15
	ds_read_b128 v[180:183], v147 offset:16384
	ds_read_b128 v[200:203], v147 offset:17408
	ds_read_b128 v[204:207], v147 offset:18432
	ds_read_b128 v[208:211], v147 offset:19456
	ds_read_b128 v[212:215], v147 offset:20480
	ds_read_b128 v[216:219], v147 offset:21504
	ds_read_b128 v[220:223], v147 offset:22528
	ds_read_b128 v[232:235], v147 offset:23552
	global_load_lds_dwordx4 v[184:185], off
	s_add_i32 m0, s15, 0x2000
	s_add_u32 s60, s22, 0x80000
	v_lshl_add_u64 v[236:237], s[22:23], 0, v[134:135]
	s_addc_u32 s61, s23, 0
	s_add_i32 s14, s14, s43
	global_load_lds_dwordx4 v[236:237], off
	v_lshl_add_u64 v[238:239], s[60:61], 0, v[138:139]
	s_mov_b32 m0, s14
	v_lshl_add_u64 v[240:241], s[40:41], 0, v[136:137]
	global_load_lds_dwordx4 v[238:239], off
	v_lshl_add_u64 v[238:239], s[60:61], 0, v[134:135]
	s_add_i32 m0, s14, 0x2000
	s_nop 0
	global_load_lds_dwordx4 v[238:239], off
	v_lshl_add_u64 v[238:239], s[40:41], 0, v[140:141]
	s_mov_b32 m0, s44
	s_nop 0
	global_load_lds_dwordx4 v[238:239], off
	s_mov_b32 m0, s45
	s_nop 0
	global_load_lds_dwordx4 v[240:241], off
	s_waitcnt vmcnt(24)
	s_waitcnt lgkmcnt(0)
	s_barrier
	s_setprio 1
	s_waitcnt lgkmcnt(0)
	v_mfma_f32_16x16x32_bf16 v[62:65], v[130:133], v[180:183], v[62:65]
	v_mfma_f32_16x16x32_bf16 v[58:61], v[156:159], v[180:183], v[58:61]
	v_mfma_f32_16x16x32_bf16 v[54:57], v[130:133], v[204:207], v[54:57]
	v_mfma_f32_16x16x32_bf16 v[46:49], v[156:159], v[204:207], v[46:49]
	v_mfma_f32_16x16x32_bf16 v[38:41], v[130:133], v[212:215], v[38:41]
	v_mfma_f32_16x16x32_bf16 v[30:33], v[156:159], v[212:215], v[30:33]
	v_mfma_f32_16x16x32_bf16 v[22:25], v[130:133], v[220:223], v[22:25]
	v_mfma_f32_16x16x32_bf16 v[14:17], v[156:159], v[220:223], v[14:17]
	v_mfma_f32_16x16x32_bf16 v[62:65], v[152:155], v[200:203], v[62:65]
	v_mfma_f32_16x16x32_bf16 v[58:61], v[160:163], v[200:203], v[58:61]
	v_mfma_f32_16x16x32_bf16 v[54:57], v[152:155], v[208:211], v[54:57]
	v_mfma_f32_16x16x32_bf16 v[46:49], v[160:163], v[208:211], v[46:49]
	v_mfma_f32_16x16x32_bf16 v[38:41], v[152:155], v[216:219], v[38:41]
	v_mfma_f32_16x16x32_bf16 v[30:33], v[160:163], v[216:219], v[30:33]
	v_mfma_f32_16x16x32_bf16 v[22:25], v[152:155], v[232:235], v[22:25]
	v_mfma_f32_16x16x32_bf16 v[14:17], v[160:163], v[232:235], v[14:17]
	s_setprio 0
	s_setprio 1
	v_mfma_f32_16x16x32_bf16 v[50:53], v[164:167], v[180:183], v[50:53]
	v_mfma_f32_16x16x32_bf16 v[42:45], v[172:175], v[180:183], v[42:45]
	v_mfma_f32_16x16x32_bf16 v[34:37], v[164:167], v[204:207], v[34:37]
	v_mfma_f32_16x16x32_bf16 v[26:29], v[172:175], v[204:207], v[26:29]
	v_mfma_f32_16x16x32_bf16 v[18:21], v[164:167], v[212:215], v[18:21]
	v_mfma_f32_16x16x32_bf16 v[10:13], v[172:175], v[212:215], v[10:13]
	v_mfma_f32_16x16x32_bf16 v[6:9], v[164:167], v[220:223], v[6:9]
	v_mfma_f32_16x16x32_bf16 v[2:5], v[172:175], v[220:223], v[2:5]
	v_mfma_f32_16x16x32_bf16 v[50:53], v[168:171], v[200:203], v[50:53]
	v_mfma_f32_16x16x32_bf16 v[42:45], v[176:179], v[200:203], v[42:45]
	v_mfma_f32_16x16x32_bf16 v[34:37], v[168:171], v[208:211], v[34:37]
	v_mfma_f32_16x16x32_bf16 v[26:29], v[176:179], v[208:211], v[26:29]
	v_mfma_f32_16x16x32_bf16 v[18:21], v[168:171], v[216:219], v[18:21]
	v_mfma_f32_16x16x32_bf16 v[10:13], v[176:179], v[216:219], v[10:13]
	v_mfma_f32_16x16x32_bf16 v[6:9], v[168:171], v[232:235], v[6:9]
	v_mfma_f32_16x16x32_bf16 v[2:5], v[176:179], v[232:235], v[2:5]
	s_setprio 0
	s_barrier
; #define PG8_STAGE(bufoff, gbase, voff) do { _Pragma("unroll") for (int _i = 0; _i < 2; ++_i) \
;         __builtin_amdgcn_global_load_lds((const unsigned*)((const char*)(gbase) + (voff)[_i]), (LAS unsigned*)(lds + (bufoff) + ldsw + _i * 8192), 16, 0, 0); } while (0)
; #define PG8_LDA(dst, b, h) do { _Pragma("unroll") for (int m = 0; m < 4; ++m) _Pragma("unroll") for (int k = 0; k < 2; ++k) dst[m][k] = *(const LAS bf16x8*)(lds + PG8_SA(b, h) + aoff + m * 2048 + k * 1024); } while (0)
; #define PG8_LDB(dst, b, h) do { _Pragma("unroll") for (int n = 0; n < 2; ++n) _Pragma("unroll") for (int k = 0; k < 2; ++k) dst[n][k] = *(const LAS bf16x8*)(lds + PG8_SB(b, h) + boff + n * 2048 + k * 1024); } while (0)
; #define PG8_MMA(ai, bj, At, Bt) do { __builtin_amdgcn_s_setprio(1); _Pragma("unroll") for (int m = 0; m < 4; ++m) _Pragma("unroll") for (int n = 0; n < 2; ++n) _Pragma("unroll") for (int k = 0; k < 2; ++k) \
;         acc[ai][bj][m][n] = __builtin_amdgcn_mfma_f32_16x16x32_bf16(Bt[n][k], At[m][k], acc[ai][bj][m][n], 0, 0, 0); __builtin_amdgcn_s_setprio(0); } while (0)
; #define PG8_WAIT_V(n) asm volatile("s_waitcnt vmcnt(" #n ")" ::: "memory")
; #define PG8_WAIT_L(n) asm volatile("s_waitcnt lgkmcnt(" #n ")" ::: "memory")
; #define PG8_BAR __builtin_amdgcn_s_barrier()
; #define PG8_SCHED __builtin_amdgcn_sched_barrier(0)
; template <class Epi, class Sched>
; __device__ __forceinline__ void gemm_phase(LAS unsigned char* lds, const Gemm g, const Sched& S, const Epi& E, const int tid, unsigned* last_sig = nullptr) {
;     ...
;             PG8_LDB(B0, 1, 0); PG8_LDB(B1, 1, 1); PG8_SCHED; PG8_LDA(At, 1, 0); PG8_STAGE(PG8_SA(0, 1), a2 + hstep, voffA);
;             PG8_WAIT_V(8); PG8_WAIT_L(0); PG8_BAR; PG8_MMA(0, 0, At, B0); PG8_MMA(0, 1, At, B1); PG8_BAR; PG8_SCHED;
	s_add_i32 s14, 0, 0x18000
	s_add_i32 s15, 0, 0x1c000
	v_add_u32_e32 v160, s14, v145
	v_add_u32_e32 v176, s15, v145
	ds_read_b128 v[130:133], v160
	ds_read_b128 v[152:155], v160 offset:1024
	ds_read_b128 v[156:159], v160 offset:2048
	ds_read_b128 v[160:163], v160 offset:3072
	ds_read_b128 v[164:167], v176
	ds_read_b128 v[168:171], v176 offset:1024
	ds_read_b128 v[172:175], v176 offset:2048
	ds_read_b128 v[176:179], v176 offset:3072
	s_add_u32 s40, s40, 0x80000
	s_addc_u32 s41, s41, 0
	s_mov_b32 m0, s46
	v_lshl_add_u64 v[242:243], s[40:41], 0, v[140:141]
	ds_read_b128 v[180:183], v147 offset:32768
	ds_read_b128 v[200:203], v147 offset:33792
	ds_read_b128 v[204:207], v147 offset:34816
	ds_read_b128 v[208:211], v147 offset:35840
	ds_read_b128 v[212:215], v147 offset:36864
	ds_read_b128 v[216:219], v147 offset:37888
	ds_read_b128 v[220:223], v147 offset:38912
	ds_read_b128 v[232:235], v147 offset:39936
	global_load_lds_dwordx4 v[242:243], off
	v_lshl_add_u64 v[242:243], s[40:41], 0, v[136:137]
	s_mov_b32 m0, s47
	s_nop 0
	global_load_lds_dwordx4 v[242:243], off
	s_waitcnt vmcnt(8)
	s_waitcnt lgkmcnt(0)
	s_barrier
	s_setprio 1
	s_waitcnt lgkmcnt(0)
	v_mfma_f32_16x16x32_bf16 v[126:129], v[130:133], v[180:183], v[126:129]
	v_mfma_f32_16x16x32_bf16 v[122:125], v[156:159], v[180:183], v[122:125]
	v_mfma_f32_16x16x32_bf16 v[118:121], v[130:133], v[204:207], v[118:121]
	v_mfma_f32_16x16x32_bf16 v[110:113], v[156:159], v[204:207], v[110:113]
	v_mfma_f32_16x16x32_bf16 v[102:105], v[130:133], v[212:215], v[102:105]
	v_mfma_f32_16x16x32_bf16 v[94:97], v[156:159], v[212:215], v[94:97]
	v_mfma_f32_16x16x32_bf16 v[86:89], v[130:133], v[220:223], v[86:89]
	v_mfma_f32_16x16x32_bf16 v[78:81], v[156:159], v[220:223], v[78:81]
	v_mfma_f32_16x16x32_bf16 v[126:129], v[152:155], v[200:203], v[126:129]
	v_mfma_f32_16x16x32_bf16 v[122:125], v[160:163], v[200:203], v[122:125]
	v_mfma_f32_16x16x32_bf16 v[118:121], v[152:155], v[208:211], v[118:121]
	v_mfma_f32_16x16x32_bf16 v[110:113], v[160:163], v[208:211], v[110:113]
	v_mfma_f32_16x16x32_bf16 v[102:105], v[152:155], v[216:219], v[102:105]
	v_mfma_f32_16x16x32_bf16 v[94:97], v[160:163], v[216:219], v[94:97]
	v_mfma_f32_16x16x32_bf16 v[86:89], v[152:155], v[232:235], v[86:89]
	v_mfma_f32_16x16x32_bf16 v[78:81], v[160:163], v[232:235], v[78:81]
	s_setprio 0
	s_setprio 1
	v_mfma_f32_16x16x32_bf16 v[114:117], v[164:167], v[180:183], v[114:117]
	v_mfma_f32_16x16x32_bf16 v[106:109], v[172:175], v[180:183], v[106:109]
	v_mfma_f32_16x16x32_bf16 v[98:101], v[164:167], v[204:207], v[98:101]
	v_mfma_f32_16x16x32_bf16 v[90:93], v[172:175], v[204:207], v[90:93]
	v_mfma_f32_16x16x32_bf16 v[82:85], v[164:167], v[212:215], v[82:85]
	v_mfma_f32_16x16x32_bf16 v[74:77], v[172:175], v[212:215], v[74:77]
	v_mfma_f32_16x16x32_bf16 v[70:73], v[164:167], v[220:223], v[70:73]
	v_mfma_f32_16x16x32_bf16 v[66:69], v[172:175], v[220:223], v[66:69]
	v_mfma_f32_16x16x32_bf16 v[114:117], v[168:171], v[200:203], v[114:117]
	v_mfma_f32_16x16x32_bf16 v[106:109], v[176:179], v[200:203], v[106:109]
	v_mfma_f32_16x16x32_bf16 v[98:101], v[168:171], v[208:211], v[98:101]
	v_mfma_f32_16x16x32_bf16 v[90:93], v[176:179], v[208:211], v[90:93]
	v_mfma_f32_16x16x32_bf16 v[82:85], v[168:171], v[216:219], v[82:85]
	v_mfma_f32_16x16x32_bf16 v[74:77], v[176:179], v[216:219], v[74:77]
	v_mfma_f32_16x16x32_bf16 v[70:73], v[168:171], v[232:235], v[70:73]
	v_mfma_f32_16x16x32_bf16 v[66:69], v[176:179], v[232:235], v[66:69]
	s_setprio 0
	s_barrier
; #define PG8_STAGE(bufoff, gbase, voff) do { _Pragma("unroll") for (int _i = 0; _i < 2; ++_i) \
;         __builtin_amdgcn_global_load_lds((const unsigned*)((const char*)(gbase) + (voff)[_i]), (LAS unsigned*)(lds + (bufoff) + ldsw + _i * 8192), 16, 0, 0); } while (0)
; #define PG8_LDA(dst, b, h) do { _Pragma("unroll") for (int m = 0; m < 4; ++m) _Pragma("unroll") for (int k = 0; k < 2; ++k) dst[m][k] = *(const LAS bf16x8*)(lds + PG8_SA(b, h) + aoff + m * 2048 + k * 1024); } while (0)
; #define PG8_MMA(ai, bj, At, Bt) do { __builtin_amdgcn_s_setprio(1); _Pragma("unroll") for (int m = 0; m < 4; ++m) _Pragma("unroll") for (int n = 0; n < 2; ++n) _Pragma("unroll") for (int k = 0; k < 2; ++k) \
;         acc[ai][bj][m][n] = __builtin_amdgcn_mfma_f32_16x16x32_bf16(Bt[n][k], At[m][k], acc[ai][bj][m][n], 0, 0, 0); __builtin_amdgcn_s_setprio(0); } while (0)
; #define PG8_WAIT_V(n) asm volatile("s_waitcnt vmcnt(" #n ")" ::: "memory")
; #define PG8_WAIT_L(n) asm volatile("s_waitcnt lgkmcnt(" #n ")" ::: "memory")
; #define PG8_BAR __builtin_amdgcn_s_barrier()
; #define PG8_SCHED __builtin_amdgcn_sched_barrier(0)
; template <class Epi, class Sched>
; __device__ __forceinline__ void gemm_phase(LAS unsigned char* lds, const Gemm g, const Sched& S, const Epi& E, const int tid, unsigned* last_sig = nullptr) {
;     ...
;             PG8_LDA(At, 1, 1); PG8_STAGE(PG8_SB(1, 0), b3, voffB); PG8_STAGE(PG8_SB(1, 1), b3 + hstep, voffB); PG8_STAGE(PG8_SA(1, 0), a3, voffA);
;             PG8_WAIT_V(8); PG8_WAIT_L(0); PG8_BAR; PG8_MMA(1, 0, At, B0); PG8_MMA(1, 1, At, B1); PG8_BAR; PG8_SCHED;
;         }
	s_add_i32 s14, s14, s43
	v_lshl_add_u64 v[184:185], v[184:185], 0, s[34:35]
	s_mov_b32 m0, s14
	ds_read_b128 v[180:183], v147 offset:49152
	ds_read_b128 v[200:203], v147 offset:50176
	ds_read_b128 v[204:207], v147 offset:51200
	ds_read_b128 v[208:211], v147 offset:52224
	ds_read_b128 v[212:215], v147 offset:53248
	ds_read_b128 v[216:219], v147 offset:54272
	ds_read_b128 v[220:223], v147 offset:55296
	ds_read_b128 v[232:235], v147 offset:56320
	global_load_lds_dwordx4 v[184:185], off
	s_add_i32 m0, s14, 0x2000
	s_add_u32 s22, s22, 0x80080
	v_lshl_add_u64 v[184:185], v[236:237], 0, s[34:35]
	s_addc_u32 s23, s23, 0
	s_add_i32 s14, s15, s43
	global_load_lds_dwordx4 v[184:185], off
	v_lshl_add_u64 v[184:185], s[22:23], 0, v[138:139]
	s_mov_b32 m0, s14
	s_nop 0
	global_load_lds_dwordx4 v[184:185], off
	v_lshl_add_u64 v[184:185], s[22:23], 0, v[134:135]
	s_add_i32 m0, s14, 0x2000
	s_nop 0
	global_load_lds_dwordx4 v[184:185], off
	v_lshl_add_u64 v[184:185], v[238:239], 0, s[34:35]
	s_mov_b32 m0, s49
	s_nop 0
	global_load_lds_dwordx4 v[184:185], off
	v_lshl_add_u64 v[184:185], v[240:241], 0, s[34:35]
	s_mov_b32 m0, s50
	s_nop 0
	global_load_lds_dwordx4 v[184:185], off
	s_waitcnt vmcnt(8)
	s_waitcnt lgkmcnt(0)
	s_barrier
	s_setprio 1
	s_waitcnt lgkmcnt(0)
	v_mfma_f32_16x16x32_bf16 v[62:65], v[130:133], v[180:183], v[62:65]
	v_mfma_f32_16x16x32_bf16 v[58:61], v[156:159], v[180:183], v[58:61]
	v_mfma_f32_16x16x32_bf16 v[54:57], v[130:133], v[204:207], v[54:57]
	v_mfma_f32_16x16x32_bf16 v[46:49], v[156:159], v[204:207], v[46:49]
	v_mfma_f32_16x16x32_bf16 v[38:41], v[130:133], v[212:215], v[38:41]
	v_mfma_f32_16x16x32_bf16 v[30:33], v[156:159], v[212:215], v[30:33]
	v_mfma_f32_16x16x32_bf16 v[22:25], v[130:133], v[220:223], v[22:25]
	v_mfma_f32_16x16x32_bf16 v[14:17], v[156:159], v[220:223], v[14:17]
	v_mfma_f32_16x16x32_bf16 v[62:65], v[152:155], v[200:203], v[62:65]
	v_mfma_f32_16x16x32_bf16 v[58:61], v[160:163], v[200:203], v[58:61]
	v_mfma_f32_16x16x32_bf16 v[54:57], v[152:155], v[208:211], v[54:57]
	v_mfma_f32_16x16x32_bf16 v[46:49], v[160:163], v[208:211], v[46:49]
	v_mfma_f32_16x16x32_bf16 v[38:41], v[152:155], v[216:219], v[38:41]
	v_mfma_f32_16x16x32_bf16 v[30:33], v[160:163], v[216:219], v[30:33]
	v_mfma_f32_16x16x32_bf16 v[22:25], v[152:155], v[232:235], v[22:25]
	v_mfma_f32_16x16x32_bf16 v[14:17], v[160:163], v[232:235], v[14:17]
	s_setprio 0
	s_setprio 1
	v_mfma_f32_16x16x32_bf16 v[50:53], v[164:167], v[180:183], v[50:53]
	v_mfma_f32_16x16x32_bf16 v[42:45], v[172:175], v[180:183], v[42:45]
	v_mfma_f32_16x16x32_bf16 v[34:37], v[164:167], v[204:207], v[34:37]
	v_mfma_f32_16x16x32_bf16 v[26:29], v[172:175], v[204:207], v[26:29]
	v_mfma_f32_16x16x32_bf16 v[18:21], v[164:167], v[212:215], v[18:21]
	v_mfma_f32_16x16x32_bf16 v[10:13], v[172:175], v[212:215], v[10:13]
	v_mfma_f32_16x16x32_bf16 v[6:9], v[164:167], v[220:223], v[6:9]
	v_mfma_f32_16x16x32_bf16 v[2:5], v[172:175], v[220:223], v[2:5]
	v_mfma_f32_16x16x32_bf16 v[50:53], v[168:171], v[200:203], v[50:53]
	v_mfma_f32_16x16x32_bf16 v[42:45], v[176:179], v[200:203], v[42:45]
	v_mfma_f32_16x16x32_bf16 v[34:37], v[168:171], v[208:211], v[34:37]
	v_mfma_f32_16x16x32_bf16 v[26:29], v[176:179], v[208:211], v[26:29]
	v_mfma_f32_16x16x32_bf16 v[18:21], v[168:171], v[216:219], v[18:21]
	v_mfma_f32_16x16x32_bf16 v[10:13], v[176:179], v[216:219], v[10:13]
	v_mfma_f32_16x16x32_bf16 v[6:9], v[168:171], v[232:235], v[6:9]
	v_mfma_f32_16x16x32_bf16 v[2:5], v[176:179], v[232:235], v[2:5]
	s_setprio 0
	s_barrier
	s_add_i32 s59, s59, 2
	s_add_u32 s20, s20, 0x100
	s_addc_u32 s21, s21, 0
	s_add_u32 s57, s57, 0x100
	s_addc_u32 s58, s58, 0
	s_cmp_gt_u32 s59, 29
	s_cbranch_scc1 .Lkpeel_exit_0

; #define PG8_BAR __builtin_amdgcn_s_barrier()
; template <class Epi, class Sched>
; __device__ __forceinline__ void gemm_phase(LAS unsigned char* lds, const Gemm g, const Sched& S, const Epi& E, const int tid, unsigned* last_sig = nullptr) {
;     ...
;         if (wr == 0) PG8_BAR;
;         E(acc, cur, wr, wc, fr, fq);
;     __device__ __forceinline__ void operator()(const f32x4 (&acc)[2][2][4][2], const Unit& u, int wr, int wc, int fr, int fq) const {
;         const int pn = u.pn;
;         if (pn < 4) run<1>(acc, u, wr, wc, fr, fq);
.Lkpeel_exit_0:
	s_and_b64 vcc, exec, s[8:9]
	s_cbranch_vccnz .LBB0_177
	s_cmp_gt_i32 s54, 3
	s_mov_b64 s[20:21], -1
	s_cbranch_scc1 .LBB0_178

; #define PG8_STAGE(bufoff, gbase, voff) do { _Pragma("unroll") for (int _i = 0; _i < 2; ++_i) \
;         __builtin_amdgcn_global_load_lds((const unsigned*)((const char*)(gbase) + (voff)[_i]), (LAS unsigned*)(lds + (bufoff) + ldsw + _i * 8192), 16, 0, 0); } while (0)
; #define PG8_LDA(dst, b, h) do { _Pragma("unroll") for (int m = 0; m < 4; ++m) _Pragma("unroll") for (int k = 0; k < 2; ++k) dst[m][k] = *(const LAS bf16x8*)(lds + PG8_SA(b, h) + aoff + m * 2048 + k * 1024); } while (0)
; #define PG8_LDB(dst, b, h) do { _Pragma("unroll") for (int n = 0; n < 2; ++n) _Pragma("unroll") for (int k = 0; k < 2; ++k) dst[n][k] = *(const LAS bf16x8*)(lds + PG8_SB(b, h) + boff + n * 2048 + k * 1024); } while (0)
; #define PG8_MMA(ai, bj, At, Bt) do { __builtin_amdgcn_s_setprio(1); _Pragma("unroll") for (int m = 0; m < 4; ++m) _Pragma("unroll") for (int n = 0; n < 2; ++n) _Pragma("unroll") for (int k = 0; k < 2; ++k) \
;         acc[ai][bj][m][n] = __builtin_amdgcn_mfma_f32_16x16x32_bf16(Bt[n][k], At[m][k], acc[ai][bj][m][n], 0, 0, 0); __builtin_amdgcn_s_setprio(0); } while (0)
; #define PG8_WAIT_V(n) asm volatile("s_waitcnt vmcnt(" #n ")" ::: "memory")
; #define PG8_WAIT_L(n) asm volatile("s_waitcnt lgkmcnt(" #n ")" ::: "memory")
; template <class Epi, class Sched>
; __device__ __forceinline__ void gemm_phase(LAS unsigned char* lds, const Gemm g, const Sched& S, const Epi& E, const int tid, unsigned* last_sig = nullptr) {
;     ...
;         for (int t = 0; t < nt; t += 2) {
;             const bool last = (t == nt - 2);
;             const char* a1 = cA + (size_t)(t + 1) * kstep;
;             const char* a2 = last ? nA : cA + (size_t)(t + 2) * kstep; const char* b2 = last ? nB : cB + (size_t)(t + 2) * kstep;
;             const char* a3 = a2 + kstep; const char* b3 = b2 + kstep;
;             PG8_LDB(B0, 0, 0); PG8_LDB(B1, 0, 1); PG8_SCHED; PG8_LDA(At, 0, 0); PG8_STAGE(PG8_SA(1, 1), a1 + hstep, voffA);
;             PG8_WAIT_V(8); PG8_WAIT_L(0); PG8_BAR; PG8_MMA(0, 0, At, B0); PG8_MMA(0, 1, At, B1); PG8_BAR; PG8_SCHED;
;     ...
; #pragma unroll
;         for (int a = 0; a < 2; ++a)
; #pragma unroll
;             for (int b = 0; b < 2; ++b)
; #pragma unroll
;                 for (int m = 0; m < 4; ++m)
; #pragma unroll
;                     for (int n = 0; n < 2; ++n) acc[a][b][m][n] = (f32x4){0.f, 0.f, 0.f, 0.f};
;         cur = nxt; cA = nA; cB = nB; ++ui;
.LBB0_597:
	s_ashr_i32 s13, s12, 31
	s_lshl_b64 s[14:15], s[12:13], 19
	v_readlane_b32 s16, v253, 56
	v_readlane_b32 s17, v253, 57
	s_add_u32 s16, s16, s14
	s_addc_u32 s17, s17, s15
	s_and_b64 s[14:15], s[4:5], exec
	s_cselect_b32 s13, s17, s21
	s_cselect_b32 s51, s16, s20
	s_ashr_i32 s11, s10, 31
	s_lshl_b64 s[14:15], s[10:11], 19
	s_add_u32 s18, s31, s14
	s_addc_u32 s19, s40, s15
	s_and_b64 s[14:15], s[4:5], exec
	s_cselect_b32 s11, s19, s23
	s_cselect_b32 s52, s18, s22
	s_add_u32 s20, s20, 0x40080
	s_addc_u32 s21, s21, 0
	s_add_u32 s53, s22, 0x100
	v_mov_b32_e32 v6, 0
	s_addc_u32 s54, s23, 0
	s_mov_b32 s55, -2
	v_mov_b32_e32 v7, v6
	v_mov_b32_e32 v8, v6
	v_mov_b32_e32 v9, v6
	v_mov_b32_e32 v2, v6
	v_mov_b32_e32 v3, v6
	v_mov_b32_e32 v4, v6
	v_mov_b32_e32 v5, v6
	v_mov_b32_e32 v22, v6
	v_mov_b32_e32 v23, v6
	v_mov_b32_e32 v24, v6
	v_mov_b32_e32 v25, v6
	v_mov_b32_e32 v18, v6
	v_mov_b32_e32 v19, v6
	v_mov_b32_e32 v20, v6
	v_mov_b32_e32 v21, v6
	v_mov_b32_e32 v38, v6
	v_mov_b32_e32 v39, v6
	v_mov_b32_e32 v40, v6
	v_mov_b32_e32 v41, v6
	v_mov_b32_e32 v34, v6
	v_mov_b32_e32 v35, v6
	v_mov_b32_e32 v36, v6
	v_mov_b32_e32 v37, v6
	v_mov_b32_e32 v54, v6
	v_mov_b32_e32 v55, v6
	v_mov_b32_e32 v56, v6
	v_mov_b32_e32 v57, v6
	v_mov_b32_e32 v50, v6
	v_mov_b32_e32 v51, v6
	v_mov_b32_e32 v52, v6
	v_mov_b32_e32 v53, v6
	v_mov_b32_e32 v14, v6
	v_mov_b32_e32 v15, v6
	v_mov_b32_e32 v16, v6
	v_mov_b32_e32 v17, v6
	v_mov_b32_e32 v10, v6
	v_mov_b32_e32 v11, v6
	v_mov_b32_e32 v12, v6
	v_mov_b32_e32 v13, v6
	v_mov_b32_e32 v30, v6
	v_mov_b32_e32 v31, v6
	v_mov_b32_e32 v32, v6
	v_mov_b32_e32 v33, v6
	v_mov_b32_e32 v26, v6
	v_mov_b32_e32 v27, v6
	v_mov_b32_e32 v28, v6
	v_mov_b32_e32 v29, v6
	v_mov_b32_e32 v46, v6
	v_mov_b32_e32 v47, v6
	v_mov_b32_e32 v48, v6
	v_mov_b32_e32 v49, v6
	v_mov_b32_e32 v42, v6
	v_mov_b32_e32 v43, v6
	v_mov_b32_e32 v44, v6
	v_mov_b32_e32 v45, v6
	v_mov_b32_e32 v62, v6
	v_mov_b32_e32 v63, v6
	v_mov_b32_e32 v64, v6
	v_mov_b32_e32 v65, v6
	v_mov_b32_e32 v58, v6
	v_mov_b32_e32 v59, v6
	v_mov_b32_e32 v60, v6
	v_mov_b32_e32 v61, v6
	v_mov_b32_e32 v70, v6
	v_mov_b32_e32 v71, v6
	v_mov_b32_e32 v72, v6
	v_mov_b32_e32 v73, v6
	v_mov_b32_e32 v66, v6
	v_mov_b32_e32 v67, v6
	v_mov_b32_e32 v68, v6
	v_mov_b32_e32 v69, v6
	v_mov_b32_e32 v86, v6
	v_mov_b32_e32 v87, v6
	v_mov_b32_e32 v88, v6
	v_mov_b32_e32 v89, v6
	v_mov_b32_e32 v82, v6
	v_mov_b32_e32 v83, v6
	v_mov_b32_e32 v84, v6
	v_mov_b32_e32 v85, v6
	v_mov_b32_e32 v102, v6
	v_mov_b32_e32 v103, v6
	v_mov_b32_e32 v104, v6
	v_mov_b32_e32 v105, v6
	v_mov_b32_e32 v98, v6
	v_mov_b32_e32 v99, v6
	v_mov_b32_e32 v100, v6
	v_mov_b32_e32 v101, v6
	v_mov_b32_e32 v118, v6
	v_mov_b32_e32 v119, v6
	v_mov_b32_e32 v120, v6
	v_mov_b32_e32 v121, v6
	v_mov_b32_e32 v114, v6
	v_mov_b32_e32 v115, v6
	v_mov_b32_e32 v116, v6
	v_mov_b32_e32 v117, v6
	v_mov_b32_e32 v78, v6
	v_mov_b32_e32 v79, v6
	v_mov_b32_e32 v80, v6
	v_mov_b32_e32 v81, v6
	v_mov_b32_e32 v74, v6
	v_mov_b32_e32 v75, v6
	v_mov_b32_e32 v76, v6
	v_mov_b32_e32 v77, v6
	v_mov_b32_e32 v94, v6
	v_mov_b32_e32 v95, v6
	v_mov_b32_e32 v96, v6
	v_mov_b32_e32 v97, v6
	v_mov_b32_e32 v90, v6
	v_mov_b32_e32 v91, v6
	v_mov_b32_e32 v92, v6
	v_mov_b32_e32 v93, v6
	v_mov_b32_e32 v110, v6
	v_mov_b32_e32 v111, v6
	v_mov_b32_e32 v112, v6
	v_mov_b32_e32 v113, v6
	v_mov_b32_e32 v106, v6
	v_mov_b32_e32 v107, v6
	v_mov_b32_e32 v108, v6
	v_mov_b32_e32 v109, v6
	v_mov_b32_e32 v126, v6
	v_mov_b32_e32 v127, v6
	v_mov_b32_e32 v128, v6
	v_mov_b32_e32 v129, v6
	v_mov_b32_e32 v122, v6
	v_mov_b32_e32 v123, v6
	v_mov_b32_e32 v124, v6
	v_mov_b32_e32 v125, v6
	s_cmp_eq_u32 s48, 1
	s_cbranch_scc1 .LBB0_598
	s_add_u32 s14, s20, 0xfffc0080
	s_addc_u32 s15, s21, -1
	s_add_i32 s56, 0, 0x10000
	s_cmp_eq_u32 s55, 12
	s_cselect_b32 s39, s13, s15
	s_cselect_b32 s38, s51, s14
	s_cselect_b32 s23, s11, s54
	s_cselect_b32 s22, s52, s53
	s_add_i32 s57, 0, 0x14000
	v_add_u32_e32 v142, s56, v185
	v_add_u32_e32 v162, s57, v185
	ds_read_b128 v[130:133], v142
	ds_read_b128 v[134:137], v142 offset:1024
	ds_read_b128 v[138:141], v142 offset:2048
	ds_read_b128 v[142:145], v142 offset:3072
	ds_read_b128 v[146:149], v162
	ds_read_b128 v[150:153], v162 offset:1024
	ds_read_b128 v[154:157], v162 offset:2048
	ds_read_b128 v[162:165], v162 offset:3072
	v_lshl_add_u64 v[240:241], s[20:21], 0, v[158:159]
	s_add_i32 m0, s42, 0xc000
	ds_read_b128 v[166:169], v207
	ds_read_b128 v[170:173], v207 offset:1024
	ds_read_b128 v[208:211], v207 offset:2048
	ds_read_b128 v[212:215], v207 offset:3072
	ds_read_b128 v[216:219], v207 offset:4096
	ds_read_b128 v[220:223], v207 offset:5120
	ds_read_b128 v[232:235], v207 offset:6144
	ds_read_b128 v[236:239], v207 offset:7168
	global_load_lds_dwordx4 v[240:241], off
	v_lshl_add_u64 v[240:241], s[20:21], 0, v[160:161]
	s_add_i32 m0, s42, 0xe000
	s_nop 0
	global_load_lds_dwordx4 v[240:241], off
	s_waitcnt vmcnt(24)
	s_waitcnt lgkmcnt(0)
	s_barrier
; #define PG8_STAGE(bufoff, gbase, voff) do { _Pragma("unroll") for (int _i = 0; _i < 2; ++_i) \
;         __builtin_amdgcn_global_load_lds((const unsigned*)((const char*)(gbase) + (voff)[_i]), (LAS unsigned*)(lds + (bufoff) + ldsw + _i * 8192), 16, 0, 0); } while (0)
; #define PG8_LDA(dst, b, h) do { _Pragma("unroll") for (int m = 0; m < 4; ++m) _Pragma("unroll") for (int k = 0; k < 2; ++k) dst[m][k] = *(const LAS bf16x8*)(lds + PG8_SA(b, h) + aoff + m * 2048 + k * 1024); } while (0)
; #define PG8_MMA(ai, bj, At, Bt) do { __builtin_amdgcn_s_setprio(1); _Pragma("unroll") for (int m = 0; m < 4; ++m) _Pragma("unroll") for (int n = 0; n < 2; ++n) _Pragma("unroll") for (int k = 0; k < 2; ++k) \
;         acc[ai][bj][m][n] = __builtin_amdgcn_mfma_f32_16x16x32_bf16(Bt[n][k], At[m][k], acc[ai][bj][m][n], 0, 0, 0); __builtin_amdgcn_s_setprio(0); } while (0)
; #define PG8_WAIT_V(n) asm volatile("s_waitcnt vmcnt(" #n ")" ::: "memory")
; #define PG8_WAIT_L(n) asm volatile("s_waitcnt lgkmcnt(" #n ")" ::: "memory")
; #define PG8_BAR __builtin_amdgcn_s_barrier()
; #define PG8_SCHED __builtin_amdgcn_sched_barrier(0)
; template <class Epi, class Sched>
; __device__ __forceinline__ void gemm_phase(LAS unsigned char* lds, const Gemm g, const Sched& S, const Epi& E, const int tid, unsigned* last_sig = nullptr) {
;     ...
;             PG8_WAIT_V(8); PG8_WAIT_L(0); PG8_BAR; PG8_MMA(0, 0, At, B0); PG8_MMA(0, 1, At, B1); PG8_BAR; PG8_SCHED;
;             PG8_LDA(At, 0, 1); PG8_STAGE(PG8_SB(0, 0), b2, voffB); PG8_STAGE(PG8_SB(0, 1), b2 + hstep, voffB); PG8_STAGE(PG8_SA(0, 0), a2, voffA);
;             PG8_WAIT_V(8); PG8_WAIT_L(0); PG8_BAR; PG8_MMA(1, 0, At, B0); PG8_MMA(1, 1, At, B1); PG8_BAR; PG8_SCHED;
	s_setprio 1
	s_waitcnt lgkmcnt(0)
	v_mfma_f32_16x16x32_bf16 v[122:125], v[130:133], v[166:169], v[122:125]
	v_mfma_f32_16x16x32_bf16 v[126:129], v[138:141], v[166:169], v[126:129]
	v_mfma_f32_16x16x32_bf16 v[106:109], v[130:133], v[208:211], v[106:109]
	v_mfma_f32_16x16x32_bf16 v[110:113], v[138:141], v[208:211], v[110:113]
	v_mfma_f32_16x16x32_bf16 v[90:93], v[130:133], v[216:219], v[90:93]
	v_mfma_f32_16x16x32_bf16 v[94:97], v[138:141], v[216:219], v[94:97]
	v_mfma_f32_16x16x32_bf16 v[74:77], v[130:133], v[232:235], v[74:77]
	v_mfma_f32_16x16x32_bf16 v[78:81], v[138:141], v[232:235], v[78:81]
	v_mfma_f32_16x16x32_bf16 v[122:125], v[134:137], v[170:173], v[122:125]
	v_mfma_f32_16x16x32_bf16 v[126:129], v[142:145], v[170:173], v[126:129]
	v_mfma_f32_16x16x32_bf16 v[106:109], v[134:137], v[212:215], v[106:109]
	v_mfma_f32_16x16x32_bf16 v[110:113], v[142:145], v[212:215], v[110:113]
	v_mfma_f32_16x16x32_bf16 v[90:93], v[134:137], v[220:223], v[90:93]
	v_mfma_f32_16x16x32_bf16 v[94:97], v[142:145], v[220:223], v[94:97]
	v_mfma_f32_16x16x32_bf16 v[74:77], v[134:137], v[236:239], v[74:77]
	v_mfma_f32_16x16x32_bf16 v[78:81], v[142:145], v[236:239], v[78:81]
	s_setprio 0
	s_setprio 1
	v_mfma_f32_16x16x32_bf16 v[114:117], v[146:149], v[166:169], v[114:117]
	v_mfma_f32_16x16x32_bf16 v[118:121], v[154:157], v[166:169], v[118:121]
	v_mfma_f32_16x16x32_bf16 v[98:101], v[146:149], v[208:211], v[98:101]
	v_mfma_f32_16x16x32_bf16 v[102:105], v[154:157], v[208:211], v[102:105]
	v_mfma_f32_16x16x32_bf16 v[82:85], v[146:149], v[216:219], v[82:85]
	v_mfma_f32_16x16x32_bf16 v[86:89], v[154:157], v[216:219], v[86:89]
	v_mfma_f32_16x16x32_bf16 v[66:69], v[146:149], v[232:235], v[66:69]
	v_mfma_f32_16x16x32_bf16 v[70:73], v[154:157], v[232:235], v[70:73]
	v_mfma_f32_16x16x32_bf16 v[114:117], v[150:153], v[170:173], v[114:117]
	v_mfma_f32_16x16x32_bf16 v[118:121], v[162:165], v[170:173], v[118:121]
	v_mfma_f32_16x16x32_bf16 v[98:101], v[150:153], v[212:215], v[98:101]
	v_mfma_f32_16x16x32_bf16 v[102:105], v[162:165], v[212:215], v[102:105]
	v_mfma_f32_16x16x32_bf16 v[82:85], v[150:153], v[220:223], v[82:85]
	v_mfma_f32_16x16x32_bf16 v[86:89], v[162:165], v[220:223], v[86:89]
	v_mfma_f32_16x16x32_bf16 v[66:69], v[150:153], v[236:239], v[66:69]
	v_mfma_f32_16x16x32_bf16 v[70:73], v[162:165], v[236:239], v[70:73]
	s_setprio 0
	s_barrier
	s_add_i32 s14, s56, s41
	v_lshl_add_u64 v[240:241], s[22:23], 0, v[186:187]
	s_mov_b32 m0, s14
	ds_read_b128 v[166:169], v207 offset:16384
	ds_read_b128 v[170:173], v207 offset:17408
	ds_read_b128 v[208:211], v207 offset:18432
	ds_read_b128 v[212:215], v207 offset:19456
	ds_read_b128 v[216:219], v207 offset:20480
	ds_read_b128 v[220:223], v207 offset:21504
	ds_read_b128 v[232:235], v207 offset:22528
	ds_read_b128 v[236:239], v207 offset:23552
	global_load_lds_dwordx4 v[240:241], off
	s_add_i32 m0, s14, 0x2000
	s_add_u32 s14, s22, 0x40000
	v_lshl_add_u64 v[242:243], s[22:23], 0, v[204:205]
	s_addc_u32 s15, s23, 0
	s_add_i32 s56, s57, s41
	global_load_lds_dwordx4 v[242:243], off
	v_lshl_add_u64 v[244:245], s[14:15], 0, v[186:187]
	s_mov_b32 m0, s56
	v_lshl_add_u64 v[246:247], s[38:39], 0, v[202:203]
	global_load_lds_dwordx4 v[244:245], off
	v_lshl_add_u64 v[244:245], s[14:15], 0, v[204:205]
	s_add_i32 m0, s56, 0x2000
	s_nop 0
	global_load_lds_dwordx4 v[244:245], off
	v_lshl_add_u64 v[244:245], s[38:39], 0, v[200:201]
	s_mov_b32 m0, s42
	s_nop 0
	global_load_lds_dwordx4 v[244:245], off
	s_mov_b32 m0, s43
	s_nop 0
	global_load_lds_dwordx4 v[246:247], off
	s_waitcnt vmcnt(24)
	s_waitcnt lgkmcnt(0)
	s_barrier
	s_setprio 1
	s_waitcnt lgkmcnt(0)
	v_mfma_f32_16x16x32_bf16 v[58:61], v[130:133], v[166:169], v[58:61]
	v_mfma_f32_16x16x32_bf16 v[62:65], v[138:141], v[166:169], v[62:65]
	v_mfma_f32_16x16x32_bf16 v[42:45], v[130:133], v[208:211], v[42:45]
	v_mfma_f32_16x16x32_bf16 v[46:49], v[138:141], v[208:211], v[46:49]
	v_mfma_f32_16x16x32_bf16 v[26:29], v[130:133], v[216:219], v[26:29]
	v_mfma_f32_16x16x32_bf16 v[30:33], v[138:141], v[216:219], v[30:33]
	v_mfma_f32_16x16x32_bf16 v[10:13], v[130:133], v[232:235], v[10:13]
	v_mfma_f32_16x16x32_bf16 v[14:17], v[138:141], v[232:235], v[14:17]
	v_mfma_f32_16x16x32_bf16 v[58:61], v[134:137], v[170:173], v[58:61]
	v_mfma_f32_16x16x32_bf16 v[62:65], v[142:145], v[170:173], v[62:65]
	v_mfma_f32_16x16x32_bf16 v[42:45], v[134:137], v[212:215], v[42:45]
	v_mfma_f32_16x16x32_bf16 v[46:49], v[142:145], v[212:215], v[46:49]
	v_mfma_f32_16x16x32_bf16 v[26:29], v[134:137], v[220:223], v[26:29]
	v_mfma_f32_16x16x32_bf16 v[30:33], v[142:145], v[220:223], v[30:33]
	v_mfma_f32_16x16x32_bf16 v[10:13], v[134:137], v[236:239], v[10:13]
	v_mfma_f32_16x16x32_bf16 v[14:17], v[142:145], v[236:239], v[14:17]
	s_setprio 0
	s_setprio 1
	v_mfma_f32_16x16x32_bf16 v[50:53], v[146:149], v[166:169], v[50:53]
	v_mfma_f32_16x16x32_bf16 v[54:57], v[154:157], v[166:169], v[54:57]
	v_mfma_f32_16x16x32_bf16 v[34:37], v[146:149], v[208:211], v[34:37]
	v_mfma_f32_16x16x32_bf16 v[38:41], v[154:157], v[208:211], v[38:41]
	v_mfma_f32_16x16x32_bf16 v[18:21], v[146:149], v[216:219], v[18:21]
	v_mfma_f32_16x16x32_bf16 v[22:25], v[154:157], v[216:219], v[22:25]
	v_mfma_f32_16x16x32_bf16 v[2:5], v[146:149], v[232:235], v[2:5]
	v_mfma_f32_16x16x32_bf16 v[6:9], v[154:157], v[232:235], v[6:9]
	v_mfma_f32_16x16x32_bf16 v[50:53], v[150:153], v[170:173], v[50:53]
	v_mfma_f32_16x16x32_bf16 v[54:57], v[162:165], v[170:173], v[54:57]
	v_mfma_f32_16x16x32_bf16 v[34:37], v[150:153], v[212:215], v[34:37]
	v_mfma_f32_16x16x32_bf16 v[38:41], v[162:165], v[212:215], v[38:41]
	v_mfma_f32_16x16x32_bf16 v[18:21], v[150:153], v[220:223], v[18:21]
	v_mfma_f32_16x16x32_bf16 v[22:25], v[162:165], v[220:223], v[22:25]
	v_mfma_f32_16x16x32_bf16 v[2:5], v[150:153], v[236:239], v[2:5]
	v_mfma_f32_16x16x32_bf16 v[6:9], v[162:165], v[236:239], v[6:9]
	s_setprio 0
	s_barrier
; #define PG8_STAGE(bufoff, gbase, voff) do { _Pragma("unroll") for (int _i = 0; _i < 2; ++_i) \
;         __builtin_amdgcn_global_load_lds((const unsigned*)((const char*)(gbase) + (voff)[_i]), (LAS unsigned*)(lds + (bufoff) + ldsw + _i * 8192), 16, 0, 0); } while (0)
; #define PG8_LDA(dst, b, h) do { _Pragma("unroll") for (int m = 0; m < 4; ++m) _Pragma("unroll") for (int k = 0; k < 2; ++k) dst[m][k] = *(const LAS bf16x8*)(lds + PG8_SA(b, h) + aoff + m * 2048 + k * 1024); } while (0)
; #define PG8_LDB(dst, b, h) do { _Pragma("unroll") for (int n = 0; n < 2; ++n) _Pragma("unroll") for (int k = 0; k < 2; ++k) dst[n][k] = *(const LAS bf16x8*)(lds + PG8_SB(b, h) + boff + n * 2048 + k * 1024); } while (0)
; #define PG8_MMA(ai, bj, At, Bt) do { __builtin_amdgcn_s_setprio(1); _Pragma("unroll") for (int m = 0; m < 4; ++m) _Pragma("unroll") for (int n = 0; n < 2; ++n) _Pragma("unroll") for (int k = 0; k < 2; ++k) \
;         acc[ai][bj][m][n] = __builtin_amdgcn_mfma_f32_16x16x32_bf16(Bt[n][k], At[m][k], acc[ai][bj][m][n], 0, 0, 0); __builtin_amdgcn_s_setprio(0); } while (0)
; #define PG8_WAIT_V(n) asm volatile("s_waitcnt vmcnt(" #n ")" ::: "memory")
; #define PG8_WAIT_L(n) asm volatile("s_waitcnt lgkmcnt(" #n ")" ::: "memory")
; #define PG8_BAR __builtin_amdgcn_s_barrier()
; #define PG8_SCHED __builtin_amdgcn_sched_barrier(0)
; template <class Epi, class Sched>
; __device__ __forceinline__ void gemm_phase(LAS unsigned char* lds, const Gemm g, const Sched& S, const Epi& E, const int tid, unsigned* last_sig = nullptr) {
;     ...
;             PG8_LDB(B0, 1, 0); PG8_LDB(B1, 1, 1); PG8_SCHED; PG8_LDA(At, 1, 0); PG8_STAGE(PG8_SA(0, 1), a2 + hstep, voffA);
;             PG8_WAIT_V(8); PG8_WAIT_L(0); PG8_BAR; PG8_MMA(0, 0, At, B0); PG8_MMA(0, 1, At, B1); PG8_BAR; PG8_SCHED;
	s_add_i32 s56, 0, 0x18000
	s_add_i32 s57, 0, 0x1c000
	v_add_u32_e32 v142, s56, v185
	v_add_u32_e32 v162, s57, v185
	ds_read_b128 v[130:133], v142
	ds_read_b128 v[134:137], v142 offset:1024
	ds_read_b128 v[138:141], v142 offset:2048
	ds_read_b128 v[142:145], v142 offset:3072
	ds_read_b128 v[146:149], v162
	ds_read_b128 v[150:153], v162 offset:1024
	ds_read_b128 v[154:157], v162 offset:2048
	ds_read_b128 v[162:165], v162 offset:3072
	s_add_u32 s14, s38, 0x40000
	s_addc_u32 s15, s39, 0
	s_mov_b32 m0, s44
	v_lshl_add_u64 v[248:249], s[14:15], 0, v[200:201]
	ds_read_b128 v[166:169], v207 offset:32768
	ds_read_b128 v[170:173], v207 offset:33792
	ds_read_b128 v[208:211], v207 offset:34816
	ds_read_b128 v[212:215], v207 offset:35840
	ds_read_b128 v[216:219], v207 offset:36864
	ds_read_b128 v[220:223], v207 offset:37888
	ds_read_b128 v[232:235], v207 offset:38912
	ds_read_b128 v[236:239], v207 offset:39936
	global_load_lds_dwordx4 v[248:249], off
	v_lshl_add_u64 v[248:249], s[14:15], 0, v[202:203]
	s_mov_b32 m0, s45
	s_nop 0
	global_load_lds_dwordx4 v[248:249], off
	s_waitcnt vmcnt(8)
	s_waitcnt lgkmcnt(0)
	s_barrier
	s_setprio 1
	s_waitcnt lgkmcnt(0)
	v_mfma_f32_16x16x32_bf16 v[122:125], v[130:133], v[166:169], v[122:125]
	v_mfma_f32_16x16x32_bf16 v[126:129], v[138:141], v[166:169], v[126:129]
	v_mfma_f32_16x16x32_bf16 v[106:109], v[130:133], v[208:211], v[106:109]
	v_mfma_f32_16x16x32_bf16 v[110:113], v[138:141], v[208:211], v[110:113]
	v_mfma_f32_16x16x32_bf16 v[90:93], v[130:133], v[216:219], v[90:93]
	v_mfma_f32_16x16x32_bf16 v[94:97], v[138:141], v[216:219], v[94:97]
	v_mfma_f32_16x16x32_bf16 v[74:77], v[130:133], v[232:235], v[74:77]
	v_mfma_f32_16x16x32_bf16 v[78:81], v[138:141], v[232:235], v[78:81]
	v_mfma_f32_16x16x32_bf16 v[122:125], v[134:137], v[170:173], v[122:125]
	v_mfma_f32_16x16x32_bf16 v[126:129], v[142:145], v[170:173], v[126:129]
	v_mfma_f32_16x16x32_bf16 v[106:109], v[134:137], v[212:215], v[106:109]
	v_mfma_f32_16x16x32_bf16 v[110:113], v[142:145], v[212:215], v[110:113]
	v_mfma_f32_16x16x32_bf16 v[90:93], v[134:137], v[220:223], v[90:93]
	v_mfma_f32_16x16x32_bf16 v[94:97], v[142:145], v[220:223], v[94:97]
	v_mfma_f32_16x16x32_bf16 v[74:77], v[134:137], v[236:239], v[74:77]
	v_mfma_f32_16x16x32_bf16 v[78:81], v[142:145], v[236:239], v[78:81]
	s_setprio 0
	s_setprio 1
	v_mfma_f32_16x16x32_bf16 v[114:117], v[146:149], v[166:169], v[114:117]
	v_mfma_f32_16x16x32_bf16 v[118:121], v[154:157], v[166:169], v[118:121]
	v_mfma_f32_16x16x32_bf16 v[98:101], v[146:149], v[208:211], v[98:101]
	v_mfma_f32_16x16x32_bf16 v[102:105], v[154:157], v[208:211], v[102:105]
	v_mfma_f32_16x16x32_bf16 v[82:85], v[146:149], v[216:219], v[82:85]
	v_mfma_f32_16x16x32_bf16 v[86:89], v[154:157], v[216:219], v[86:89]
	v_mfma_f32_16x16x32_bf16 v[66:69], v[146:149], v[232:235], v[66:69]
	v_mfma_f32_16x16x32_bf16 v[70:73], v[154:157], v[232:235], v[70:73]
	v_mfma_f32_16x16x32_bf16 v[114:117], v[150:153], v[170:173], v[114:117]
	v_mfma_f32_16x16x32_bf16 v[118:121], v[162:165], v[170:173], v[118:121]
	v_mfma_f32_16x16x32_bf16 v[98:101], v[150:153], v[212:215], v[98:101]
	v_mfma_f32_16x16x32_bf16 v[102:105], v[162:165], v[212:215], v[102:105]
	v_mfma_f32_16x16x32_bf16 v[82:85], v[150:153], v[220:223], v[82:85]
	v_mfma_f32_16x16x32_bf16 v[86:89], v[162:165], v[220:223], v[86:89]
	v_mfma_f32_16x16x32_bf16 v[66:69], v[150:153], v[236:239], v[66:69]
	v_mfma_f32_16x16x32_bf16 v[70:73], v[162:165], v[236:239], v[70:73]
	s_setprio 0
	s_barrier
; #define PG8_STAGE(bufoff, gbase, voff) do { _Pragma("unroll") for (int _i = 0; _i < 2; ++_i) \
;         __builtin_amdgcn_global_load_lds((const unsigned*)((const char*)(gbase) + (voff)[_i]), (LAS unsigned*)(lds + (bufoff) + ldsw + _i * 8192), 16, 0, 0); } while (0)
; #define PG8_LDA(dst, b, h) do { _Pragma("unroll") for (int m = 0; m < 4; ++m) _Pragma("unroll") for (int k = 0; k < 2; ++k) dst[m][k] = *(const LAS bf16x8*)(lds + PG8_SA(b, h) + aoff + m * 2048 + k * 1024); } while (0)
; #define PG8_MMA(ai, bj, At, Bt) do { __builtin_amdgcn_s_setprio(1); _Pragma("unroll") for (int m = 0; m < 4; ++m) _Pragma("unroll") for (int n = 0; n < 2; ++n) _Pragma("unroll") for (int k = 0; k < 2; ++k) \
;         acc[ai][bj][m][n] = __builtin_amdgcn_mfma_f32_16x16x32_bf16(Bt[n][k], At[m][k], acc[ai][bj][m][n], 0, 0, 0); __builtin_amdgcn_s_setprio(0); } while (0)
; #define PG8_WAIT_V(n) asm volatile("s_waitcnt vmcnt(" #n ")" ::: "memory")
; #define PG8_WAIT_L(n) asm volatile("s_waitcnt lgkmcnt(" #n ")" ::: "memory")
; #define PG8_BAR __builtin_amdgcn_s_barrier()
; #define PG8_SCHED __builtin_amdgcn_sched_barrier(0)
; template <class Epi, class Sched>
; __device__ __forceinline__ void gemm_phase(LAS unsigned char* lds, const Gemm g, const Sched& S, const Epi& E, const int tid, unsigned* last_sig = nullptr) {
;     ...
;             PG8_LDA(At, 1, 1); PG8_STAGE(PG8_SB(1, 0), b3, voffB); PG8_STAGE(PG8_SB(1, 1), b3 + hstep, voffB); PG8_STAGE(PG8_SA(1, 0), a3, voffA);
;             PG8_WAIT_V(8); PG8_WAIT_L(0); PG8_BAR; PG8_MMA(1, 0, At, B0); PG8_MMA(1, 1, At, B1); PG8_BAR; PG8_SCHED;
;         }
	s_add_i32 s14, s56, s41
	v_lshl_add_u64 v[240:241], v[240:241], 0, s[34:35]
	s_mov_b32 m0, s14
	ds_read_b128 v[166:169], v207 offset:49152
	ds_read_b128 v[170:173], v207 offset:50176
	ds_read_b128 v[208:211], v207 offset:51200
	ds_read_b128 v[212:215], v207 offset:52224
	ds_read_b128 v[216:219], v207 offset:53248
	ds_read_b128 v[220:223], v207 offset:54272
	ds_read_b128 v[232:235], v207 offset:55296
	ds_read_b128 v[236:239], v207 offset:56320
	global_load_lds_dwordx4 v[240:241], off
	s_add_i32 m0, s14, 0x2000
	s_add_u32 s14, s22, 0x40080
	v_lshl_add_u64 v[240:241], v[242:243], 0, s[34:35]
	s_addc_u32 s15, s23, 0
	s_add_i32 s22, s57, s41
	global_load_lds_dwordx4 v[240:241], off
	v_lshl_add_u64 v[240:241], s[14:15], 0, v[186:187]
	s_mov_b32 m0, s22
	s_nop 0
	global_load_lds_dwordx4 v[240:241], off
	v_lshl_add_u64 v[240:241], s[14:15], 0, v[204:205]
	s_add_i32 m0, s22, 0x2000
	s_nop 0
	global_load_lds_dwordx4 v[240:241], off
	v_lshl_add_u64 v[240:241], v[244:245], 0, s[34:35]
	s_mov_b32 m0, s46
	s_nop 0
	global_load_lds_dwordx4 v[240:241], off
	v_lshl_add_u64 v[240:241], v[246:247], 0, s[34:35]
	s_mov_b32 m0, s47
	s_nop 0
	global_load_lds_dwordx4 v[240:241], off
	s_waitcnt vmcnt(8)
	s_waitcnt lgkmcnt(0)
	s_barrier
	s_setprio 1
	s_waitcnt lgkmcnt(0)
	v_mfma_f32_16x16x32_bf16 v[58:61], v[130:133], v[166:169], v[58:61]
	v_mfma_f32_16x16x32_bf16 v[62:65], v[138:141], v[166:169], v[62:65]
	v_mfma_f32_16x16x32_bf16 v[42:45], v[130:133], v[208:211], v[42:45]
	v_mfma_f32_16x16x32_bf16 v[46:49], v[138:141], v[208:211], v[46:49]
	v_mfma_f32_16x16x32_bf16 v[26:29], v[130:133], v[216:219], v[26:29]
	v_mfma_f32_16x16x32_bf16 v[30:33], v[138:141], v[216:219], v[30:33]
	v_mfma_f32_16x16x32_bf16 v[10:13], v[130:133], v[232:235], v[10:13]
	v_mfma_f32_16x16x32_bf16 v[14:17], v[138:141], v[232:235], v[14:17]
	v_mfma_f32_16x16x32_bf16 v[58:61], v[134:137], v[170:173], v[58:61]
	v_mfma_f32_16x16x32_bf16 v[62:65], v[142:145], v[170:173], v[62:65]
	v_mfma_f32_16x16x32_bf16 v[42:45], v[134:137], v[212:215], v[42:45]
	v_mfma_f32_16x16x32_bf16 v[46:49], v[142:145], v[212:215], v[46:49]
	v_mfma_f32_16x16x32_bf16 v[26:29], v[134:137], v[220:223], v[26:29]
	v_mfma_f32_16x16x32_bf16 v[30:33], v[142:145], v[220:223], v[30:33]
	v_mfma_f32_16x16x32_bf16 v[10:13], v[134:137], v[236:239], v[10:13]
	v_mfma_f32_16x16x32_bf16 v[14:17], v[142:145], v[236:239], v[14:17]
	s_setprio 0
	s_setprio 1
	v_mfma_f32_16x16x32_bf16 v[50:53], v[146:149], v[166:169], v[50:53]
	v_mfma_f32_16x16x32_bf16 v[54:57], v[154:157], v[166:169], v[54:57]
	v_mfma_f32_16x16x32_bf16 v[34:37], v[146:149], v[208:211], v[34:37]
	v_mfma_f32_16x16x32_bf16 v[38:41], v[154:157], v[208:211], v[38:41]
	v_mfma_f32_16x16x32_bf16 v[18:21], v[146:149], v[216:219], v[18:21]
	v_mfma_f32_16x16x32_bf16 v[22:25], v[154:157], v[216:219], v[22:25]
	v_mfma_f32_16x16x32_bf16 v[2:5], v[146:149], v[232:235], v[2:5]
	v_mfma_f32_16x16x32_bf16 v[6:9], v[154:157], v[232:235], v[6:9]
	v_mfma_f32_16x16x32_bf16 v[50:53], v[150:153], v[170:173], v[50:53]
	v_mfma_f32_16x16x32_bf16 v[54:57], v[162:165], v[170:173], v[54:57]
	v_mfma_f32_16x16x32_bf16 v[34:37], v[150:153], v[212:215], v[34:37]
	v_mfma_f32_16x16x32_bf16 v[38:41], v[162:165], v[212:215], v[38:41]
	v_mfma_f32_16x16x32_bf16 v[18:21], v[150:153], v[220:223], v[18:21]
	v_mfma_f32_16x16x32_bf16 v[22:25], v[162:165], v[220:223], v[22:25]
	v_mfma_f32_16x16x32_bf16 v[2:5], v[150:153], v[236:239], v[2:5]
	v_mfma_f32_16x16x32_bf16 v[6:9], v[162:165], v[236:239], v[6:9]
	s_setprio 0
	s_barrier
	s_add_i32 s55, s55, 2
	s_add_u32 s20, s20, 0x100
	s_addc_u32 s21, s21, 0
	s_add_u32 s53, s53, 0x100
	s_addc_u32 s54, s54, 0
	s_cmp_gt_u32 s55, 13
	s_cbranch_scc1 .Lkpeel_exit_1

; #define PG8_BAR __builtin_amdgcn_s_barrier()
; template <class Epi, class Sched>
; __device__ __forceinline__ void gemm_phase(LAS unsigned char* lds, const Gemm g, const Sched& S, const Epi& E, const int tid, unsigned* last_sig = nullptr) {
;     ...
;         if (wr == 0) PG8_BAR;
.Lkpeel_exit_1:
	s_and_b64 vcc, exec, s[8:9]
	s_cbranch_vccz .LBB0_601
	s_barrier

; #define PG8_STAGE(bufoff, gbase, voff) do { _Pragma("unroll") for (int _i = 0; _i < 2; ++_i) \
;         __builtin_amdgcn_global_load_lds((const unsigned*)((const char*)(gbase) + (voff)[_i]), (LAS unsigned*)(lds + (bufoff) + ldsw + _i * 8192), 16, 0, 0); } while (0)
; #define PG8_LDA(dst, b, h) do { _Pragma("unroll") for (int m = 0; m < 4; ++m) _Pragma("unroll") for (int k = 0; k < 2; ++k) dst[m][k] = *(const LAS bf16x8*)(lds + PG8_SA(b, h) + aoff + m * 2048 + k * 1024); } while (0)
; #define PG8_LDB(dst, b, h) do { _Pragma("unroll") for (int n = 0; n < 2; ++n) _Pragma("unroll") for (int k = 0; k < 2; ++k) dst[n][k] = *(const LAS bf16x8*)(lds + PG8_SB(b, h) + boff + n * 2048 + k * 1024); } while (0)
; #define PG8_MMA(ai, bj, At, Bt) do { __builtin_amdgcn_s_setprio(1); _Pragma("unroll") for (int m = 0; m < 4; ++m) _Pragma("unroll") for (int n = 0; n < 2; ++n) _Pragma("unroll") for (int k = 0; k < 2; ++k) \
;         acc[ai][bj][m][n] = __builtin_amdgcn_mfma_f32_16x16x32_bf16(Bt[n][k], At[m][k], acc[ai][bj][m][n], 0, 0, 0); __builtin_amdgcn_s_setprio(0); } while (0)
; #define PG8_WAIT_V(n) asm volatile("s_waitcnt vmcnt(" #n ")" ::: "memory")
; #define PG8_WAIT_L(n) asm volatile("s_waitcnt lgkmcnt(" #n ")" ::: "memory")
; template <class Epi, class Sched>
; __device__ __forceinline__ void gemm_phase(LAS unsigned char* lds, const Gemm g, const Sched& S, const Epi& E, const int tid, unsigned* last_sig = nullptr) {
;     ...
;         for (int t = 0; t < nt; t += 2) {
;             const bool last = (t == nt - 2);
;             const char* a1 = cA + (size_t)(t + 1) * kstep;
;             const char* a2 = last ? nA : cA + (size_t)(t + 2) * kstep; const char* b2 = last ? nB : cB + (size_t)(t + 2) * kstep;
;             const char* a3 = a2 + kstep; const char* b3 = b2 + kstep;
;             PG8_LDB(B0, 0, 0); PG8_LDB(B1, 0, 1); PG8_SCHED; PG8_LDA(At, 0, 0); PG8_STAGE(PG8_SA(1, 1), a1 + hstep, voffA);
;             PG8_WAIT_V(8); PG8_WAIT_L(0); PG8_BAR; PG8_MMA(0, 0, At, B0); PG8_MMA(0, 1, At, B1); PG8_BAR; PG8_SCHED;
;     ...
; #pragma unroll
;         for (int a = 0; a < 2; ++a)
; #pragma unroll
;             for (int b = 0; b < 2; ++b)
; #pragma unroll
;                 for (int m = 0; m < 4; ++m)
; #pragma unroll
;                     for (int n = 0; n < 2; ++n) acc[a][b][m][n] = (f32x4){0.f, 0.f, 0.f, 0.f};
;         cur = nxt; cA = nA; cB = nB; ++ui;
.LBB0_617:
	s_ashr_i32 s11, s10, 31
	s_lshl_b64 s[12:13], s[10:11], 19
	v_readlane_b32 s14, v251, 47
	v_readlane_b32 s15, v251, 48
	s_add_u32 s12, s14, s12
	s_addc_u32 s13, s15, s13
	s_and_b64 s[14:15], s[0:1], exec
	s_cselect_b32 s11, s13, s23
	s_cselect_b32 s19, s12, s22
	s_ashr_i32 s9, s8, 31
	s_lshl_b64 s[14:15], s[8:9], 19
	s_add_u32 s16, s28, s14
	s_addc_u32 s17, s31, s15
	s_and_b64 s[14:15], s[0:1], exec
	s_cselect_b32 s9, s17, s39
	s_cselect_b32 s49, s16, s38
	s_add_u32 s22, s22, 0x40080
	s_addc_u32 s23, s23, 0
	s_add_u32 s50, s38, 0x100
	v_mov_b32_e32 v6, 0
	s_addc_u32 s51, s39, 0
	s_mov_b32 s52, -2
	v_mov_b32_e32 v7, v6
	v_mov_b32_e32 v8, v6
	v_mov_b32_e32 v9, v6
	v_mov_b32_e32 v2, v6
	v_mov_b32_e32 v3, v6
	v_mov_b32_e32 v4, v6
	v_mov_b32_e32 v5, v6
	v_mov_b32_e32 v22, v6
	v_mov_b32_e32 v23, v6
	v_mov_b32_e32 v24, v6
	v_mov_b32_e32 v25, v6
	v_mov_b32_e32 v18, v6
	v_mov_b32_e32 v19, v6
	v_mov_b32_e32 v20, v6
	v_mov_b32_e32 v21, v6
	v_mov_b32_e32 v38, v6
	v_mov_b32_e32 v39, v6
	v_mov_b32_e32 v40, v6
	v_mov_b32_e32 v41, v6
	v_mov_b32_e32 v34, v6
	v_mov_b32_e32 v35, v6
	v_mov_b32_e32 v36, v6
	v_mov_b32_e32 v37, v6
	v_mov_b32_e32 v54, v6
	v_mov_b32_e32 v55, v6
	v_mov_b32_e32 v56, v6
	v_mov_b32_e32 v57, v6
	v_mov_b32_e32 v50, v6
	v_mov_b32_e32 v51, v6
	v_mov_b32_e32 v52, v6
	v_mov_b32_e32 v53, v6
	v_mov_b32_e32 v14, v6
	v_mov_b32_e32 v15, v6
	v_mov_b32_e32 v16, v6
	v_mov_b32_e32 v17, v6
	v_mov_b32_e32 v10, v6
	v_mov_b32_e32 v11, v6
	v_mov_b32_e32 v12, v6
	v_mov_b32_e32 v13, v6
	v_mov_b32_e32 v30, v6
	v_mov_b32_e32 v31, v6
	v_mov_b32_e32 v32, v6
	v_mov_b32_e32 v33, v6
	v_mov_b32_e32 v26, v6
	v_mov_b32_e32 v27, v6
	v_mov_b32_e32 v28, v6
	v_mov_b32_e32 v29, v6
	v_mov_b32_e32 v46, v6
	v_mov_b32_e32 v47, v6
	v_mov_b32_e32 v48, v6
	v_mov_b32_e32 v49, v6
	v_mov_b32_e32 v42, v6
	v_mov_b32_e32 v43, v6
	v_mov_b32_e32 v44, v6
	v_mov_b32_e32 v45, v6
	v_mov_b32_e32 v62, v6
	v_mov_b32_e32 v63, v6
	v_mov_b32_e32 v64, v6
	v_mov_b32_e32 v65, v6
	v_mov_b32_e32 v58, v6
	v_mov_b32_e32 v59, v6
	v_mov_b32_e32 v60, v6
	v_mov_b32_e32 v61, v6
	v_mov_b32_e32 v70, v6
	v_mov_b32_e32 v71, v6
	v_mov_b32_e32 v72, v6
	v_mov_b32_e32 v73, v6
	v_mov_b32_e32 v66, v6
	v_mov_b32_e32 v67, v6
	v_mov_b32_e32 v68, v6
	v_mov_b32_e32 v69, v6
	v_mov_b32_e32 v86, v6
	v_mov_b32_e32 v87, v6
	v_mov_b32_e32 v88, v6
	v_mov_b32_e32 v89, v6
	v_mov_b32_e32 v82, v6
	v_mov_b32_e32 v83, v6
	v_mov_b32_e32 v84, v6
	v_mov_b32_e32 v85, v6
	v_mov_b32_e32 v102, v6
	v_mov_b32_e32 v103, v6
	v_mov_b32_e32 v104, v6
	v_mov_b32_e32 v105, v6
	v_mov_b32_e32 v98, v6
	v_mov_b32_e32 v99, v6
	v_mov_b32_e32 v100, v6
	v_mov_b32_e32 v101, v6
	v_mov_b32_e32 v118, v6
	v_mov_b32_e32 v119, v6
	v_mov_b32_e32 v120, v6
	v_mov_b32_e32 v121, v6
	v_mov_b32_e32 v114, v6
	v_mov_b32_e32 v115, v6
	v_mov_b32_e32 v116, v6
	v_mov_b32_e32 v117, v6
	v_mov_b32_e32 v78, v6
	v_mov_b32_e32 v79, v6
	v_mov_b32_e32 v80, v6
	v_mov_b32_e32 v81, v6
	v_mov_b32_e32 v74, v6
	v_mov_b32_e32 v75, v6
	v_mov_b32_e32 v76, v6
	v_mov_b32_e32 v77, v6
	v_mov_b32_e32 v94, v6
	v_mov_b32_e32 v95, v6
	v_mov_b32_e32 v96, v6
	v_mov_b32_e32 v97, v6
	v_mov_b32_e32 v90, v6
	v_mov_b32_e32 v91, v6
	v_mov_b32_e32 v92, v6
	v_mov_b32_e32 v93, v6
	v_mov_b32_e32 v110, v6
	v_mov_b32_e32 v111, v6
	v_mov_b32_e32 v112, v6
	v_mov_b32_e32 v113, v6
	v_mov_b32_e32 v106, v6
	v_mov_b32_e32 v107, v6
	v_mov_b32_e32 v108, v6
	v_mov_b32_e32 v109, v6
	v_mov_b32_e32 v126, v6
	v_mov_b32_e32 v127, v6
	v_mov_b32_e32 v128, v6
	v_mov_b32_e32 v129, v6
	v_mov_b32_e32 v122, v6
	v_mov_b32_e32 v123, v6
	v_mov_b32_e32 v124, v6
	v_mov_b32_e32 v125, v6
	s_cmp_eq_u32 s48, 1
	s_cbranch_scc1 .LBB0_618
	s_add_u32 s14, s22, 0xfffc0080
	s_addc_u32 s15, s23, -1
	s_add_i32 s53, 0, 0x10000
	s_cmp_eq_u32 s52, 12
	s_cselect_b32 s41, s11, s15
	s_cselect_b32 s40, s19, s14
	s_cselect_b32 s39, s9, s51
	s_cselect_b32 s38, s49, s50
	s_add_i32 s54, 0, 0x14000
	v_add_u32_e32 v142, s53, v232
	v_add_u32_e32 v158, s54, v232
	ds_read_b128 v[130:133], v142
	ds_read_b128 v[134:137], v142 offset:1024
	ds_read_b128 v[138:141], v142 offset:2048
	ds_read_b128 v[142:145], v142 offset:3072
	ds_read_b128 v[146:149], v158
	ds_read_b128 v[150:153], v158 offset:1024
	ds_read_b128 v[154:157], v158 offset:2048
	ds_read_b128 v[158:161], v158 offset:3072
	v_lshl_add_u64 v[218:219], s[22:23], 0, v[206:207]
	s_add_i32 m0, s21, 0xc000
	ds_read_b128 v[162:165], v234
	ds_read_b128 v[166:169], v234 offset:1024
	ds_read_b128 v[170:173], v234 offset:2048
	ds_read_b128 v[174:177], v234 offset:3072
	ds_read_b128 v[178:181], v234 offset:4096
	ds_read_b128 v[182:185], v234 offset:5120
	ds_read_b128 v[210:213], v234 offset:6144
	ds_read_b128 v[214:217], v234 offset:7168
	global_load_lds_dwordx4 v[218:219], off
	v_lshl_add_u64 v[218:219], s[22:23], 0, v[208:209]
	s_add_i32 m0, s21, 0xe000
	s_nop 0
	global_load_lds_dwordx4 v[218:219], off
	s_waitcnt vmcnt(24)
	s_waitcnt lgkmcnt(0)
	s_barrier
; #define PG8_STAGE(bufoff, gbase, voff) do { _Pragma("unroll") for (int _i = 0; _i < 2; ++_i) \
;         __builtin_amdgcn_global_load_lds((const unsigned*)((const char*)(gbase) + (voff)[_i]), (LAS unsigned*)(lds + (bufoff) + ldsw + _i * 8192), 16, 0, 0); } while (0)
; #define PG8_LDA(dst, b, h) do { _Pragma("unroll") for (int m = 0; m < 4; ++m) _Pragma("unroll") for (int k = 0; k < 2; ++k) dst[m][k] = *(const LAS bf16x8*)(lds + PG8_SA(b, h) + aoff + m * 2048 + k * 1024); } while (0)
; #define PG8_MMA(ai, bj, At, Bt) do { __builtin_amdgcn_s_setprio(1); _Pragma("unroll") for (int m = 0; m < 4; ++m) _Pragma("unroll") for (int n = 0; n < 2; ++n) _Pragma("unroll") for (int k = 0; k < 2; ++k) \
;         acc[ai][bj][m][n] = __builtin_amdgcn_mfma_f32_16x16x32_bf16(Bt[n][k], At[m][k], acc[ai][bj][m][n], 0, 0, 0); __builtin_amdgcn_s_setprio(0); } while (0)
; #define PG8_WAIT_V(n) asm volatile("s_waitcnt vmcnt(" #n ")" ::: "memory")
; #define PG8_WAIT_L(n) asm volatile("s_waitcnt lgkmcnt(" #n ")" ::: "memory")
; #define PG8_BAR __builtin_amdgcn_s_barrier()
; #define PG8_SCHED __builtin_amdgcn_sched_barrier(0)
; template <class Epi, class Sched>
; __device__ __forceinline__ void gemm_phase(LAS unsigned char* lds, const Gemm g, const Sched& S, const Epi& E, const int tid, unsigned* last_sig = nullptr) {
;     ...
;             PG8_WAIT_V(8); PG8_WAIT_L(0); PG8_BAR; PG8_MMA(0, 0, At, B0); PG8_MMA(0, 1, At, B1); PG8_BAR; PG8_SCHED;
;             PG8_LDA(At, 0, 1); PG8_STAGE(PG8_SB(0, 0), b2, voffB); PG8_STAGE(PG8_SB(0, 1), b2 + hstep, voffB); PG8_STAGE(PG8_SA(0, 0), a2, voffA);
;             PG8_WAIT_V(8); PG8_WAIT_L(0); PG8_BAR; PG8_MMA(1, 0, At, B0); PG8_MMA(1, 1, At, B1); PG8_BAR; PG8_SCHED;
	s_setprio 1
	s_waitcnt lgkmcnt(0)
	v_mfma_f32_16x16x32_bf16 v[122:125], v[130:133], v[162:165], v[122:125]
	v_mfma_f32_16x16x32_bf16 v[126:129], v[138:141], v[162:165], v[126:129]
	v_mfma_f32_16x16x32_bf16 v[106:109], v[130:133], v[170:173], v[106:109]
	v_mfma_f32_16x16x32_bf16 v[110:113], v[138:141], v[170:173], v[110:113]
	v_mfma_f32_16x16x32_bf16 v[90:93], v[130:133], v[178:181], v[90:93]
	v_mfma_f32_16x16x32_bf16 v[94:97], v[138:141], v[178:181], v[94:97]
	v_mfma_f32_16x16x32_bf16 v[74:77], v[130:133], v[210:213], v[74:77]
	v_mfma_f32_16x16x32_bf16 v[78:81], v[138:141], v[210:213], v[78:81]
	v_mfma_f32_16x16x32_bf16 v[122:125], v[134:137], v[166:169], v[122:125]
	v_mfma_f32_16x16x32_bf16 v[126:129], v[142:145], v[166:169], v[126:129]
	v_mfma_f32_16x16x32_bf16 v[106:109], v[134:137], v[174:177], v[106:109]
	v_mfma_f32_16x16x32_bf16 v[110:113], v[142:145], v[174:177], v[110:113]
	v_mfma_f32_16x16x32_bf16 v[90:93], v[134:137], v[182:185], v[90:93]
	v_mfma_f32_16x16x32_bf16 v[94:97], v[142:145], v[182:185], v[94:97]
	v_mfma_f32_16x16x32_bf16 v[74:77], v[134:137], v[214:217], v[74:77]
	v_mfma_f32_16x16x32_bf16 v[78:81], v[142:145], v[214:217], v[78:81]
	s_setprio 0
	s_setprio 1
	v_mfma_f32_16x16x32_bf16 v[114:117], v[146:149], v[162:165], v[114:117]
	v_mfma_f32_16x16x32_bf16 v[118:121], v[154:157], v[162:165], v[118:121]
	v_mfma_f32_16x16x32_bf16 v[98:101], v[146:149], v[170:173], v[98:101]
	v_mfma_f32_16x16x32_bf16 v[102:105], v[154:157], v[170:173], v[102:105]
	v_mfma_f32_16x16x32_bf16 v[82:85], v[146:149], v[178:181], v[82:85]
	v_mfma_f32_16x16x32_bf16 v[86:89], v[154:157], v[178:181], v[86:89]
	v_mfma_f32_16x16x32_bf16 v[66:69], v[146:149], v[210:213], v[66:69]
	v_mfma_f32_16x16x32_bf16 v[70:73], v[154:157], v[210:213], v[70:73]
	v_mfma_f32_16x16x32_bf16 v[114:117], v[150:153], v[166:169], v[114:117]
	v_mfma_f32_16x16x32_bf16 v[118:121], v[158:161], v[166:169], v[118:121]
	v_mfma_f32_16x16x32_bf16 v[98:101], v[150:153], v[174:177], v[98:101]
	v_mfma_f32_16x16x32_bf16 v[102:105], v[158:161], v[174:177], v[102:105]
	v_mfma_f32_16x16x32_bf16 v[82:85], v[150:153], v[182:185], v[82:85]
	v_mfma_f32_16x16x32_bf16 v[86:89], v[158:161], v[182:185], v[86:89]
	v_mfma_f32_16x16x32_bf16 v[66:69], v[150:153], v[214:217], v[66:69]
	v_mfma_f32_16x16x32_bf16 v[70:73], v[158:161], v[214:217], v[70:73]
	s_setprio 0
	s_barrier
	s_add_i32 s14, s53, s42
	v_lshl_add_u64 v[218:219], s[38:39], 0, v[186:187]
	s_mov_b32 m0, s14
	ds_read_b128 v[162:165], v234 offset:16384
	ds_read_b128 v[166:169], v234 offset:17408
	ds_read_b128 v[170:173], v234 offset:18432
	ds_read_b128 v[174:177], v234 offset:19456
	ds_read_b128 v[178:181], v234 offset:20480
	ds_read_b128 v[182:185], v234 offset:21504
	ds_read_b128 v[210:213], v234 offset:22528
	ds_read_b128 v[214:217], v234 offset:23552
	global_load_lds_dwordx4 v[218:219], off
	s_add_i32 m0, s14, 0x2000
	s_add_u32 s14, s38, 0x40000
	v_lshl_add_u64 v[220:221], s[38:39], 0, v[204:205]
	s_addc_u32 s15, s39, 0
	s_add_i32 s53, s54, s42
	global_load_lds_dwordx4 v[220:221], off
	v_lshl_add_u64 v[222:223], s[14:15], 0, v[186:187]
	s_mov_b32 m0, s53
	v_lshl_add_u64 v[236:237], s[40:41], 0, v[202:203]
	global_load_lds_dwordx4 v[222:223], off
	v_lshl_add_u64 v[222:223], s[14:15], 0, v[204:205]
	s_add_i32 m0, s53, 0x2000
	s_nop 0
	global_load_lds_dwordx4 v[222:223], off
	v_lshl_add_u64 v[222:223], s[40:41], 0, v[200:201]
	s_mov_b32 m0, s21
	s_nop 0
	global_load_lds_dwordx4 v[222:223], off
	s_mov_b32 m0, s43
	s_nop 0
	global_load_lds_dwordx4 v[236:237], off
	s_waitcnt vmcnt(24)
	s_waitcnt lgkmcnt(0)
	s_barrier
	s_setprio 1
	s_waitcnt lgkmcnt(0)
	v_mfma_f32_16x16x32_bf16 v[58:61], v[130:133], v[162:165], v[58:61]
	v_mfma_f32_16x16x32_bf16 v[62:65], v[138:141], v[162:165], v[62:65]
	v_mfma_f32_16x16x32_bf16 v[42:45], v[130:133], v[170:173], v[42:45]
	v_mfma_f32_16x16x32_bf16 v[46:49], v[138:141], v[170:173], v[46:49]
	v_mfma_f32_16x16x32_bf16 v[26:29], v[130:133], v[178:181], v[26:29]
	v_mfma_f32_16x16x32_bf16 v[30:33], v[138:141], v[178:181], v[30:33]
	v_mfma_f32_16x16x32_bf16 v[10:13], v[130:133], v[210:213], v[10:13]
	v_mfma_f32_16x16x32_bf16 v[14:17], v[138:141], v[210:213], v[14:17]
	v_mfma_f32_16x16x32_bf16 v[58:61], v[134:137], v[166:169], v[58:61]
	v_mfma_f32_16x16x32_bf16 v[62:65], v[142:145], v[166:169], v[62:65]
	v_mfma_f32_16x16x32_bf16 v[42:45], v[134:137], v[174:177], v[42:45]
	v_mfma_f32_16x16x32_bf16 v[46:49], v[142:145], v[174:177], v[46:49]
	v_mfma_f32_16x16x32_bf16 v[26:29], v[134:137], v[182:185], v[26:29]
	v_mfma_f32_16x16x32_bf16 v[30:33], v[142:145], v[182:185], v[30:33]
	v_mfma_f32_16x16x32_bf16 v[10:13], v[134:137], v[214:217], v[10:13]
	v_mfma_f32_16x16x32_bf16 v[14:17], v[142:145], v[214:217], v[14:17]
	s_setprio 0
	s_setprio 1
	v_mfma_f32_16x16x32_bf16 v[50:53], v[146:149], v[162:165], v[50:53]
	v_mfma_f32_16x16x32_bf16 v[54:57], v[154:157], v[162:165], v[54:57]
	v_mfma_f32_16x16x32_bf16 v[34:37], v[146:149], v[170:173], v[34:37]
	v_mfma_f32_16x16x32_bf16 v[38:41], v[154:157], v[170:173], v[38:41]
	v_mfma_f32_16x16x32_bf16 v[18:21], v[146:149], v[178:181], v[18:21]
	v_mfma_f32_16x16x32_bf16 v[22:25], v[154:157], v[178:181], v[22:25]
	v_mfma_f32_16x16x32_bf16 v[2:5], v[146:149], v[210:213], v[2:5]
	v_mfma_f32_16x16x32_bf16 v[6:9], v[154:157], v[210:213], v[6:9]
	v_mfma_f32_16x16x32_bf16 v[50:53], v[150:153], v[166:169], v[50:53]
	v_mfma_f32_16x16x32_bf16 v[54:57], v[158:161], v[166:169], v[54:57]
	v_mfma_f32_16x16x32_bf16 v[34:37], v[150:153], v[174:177], v[34:37]
	v_mfma_f32_16x16x32_bf16 v[38:41], v[158:161], v[174:177], v[38:41]
	v_mfma_f32_16x16x32_bf16 v[18:21], v[150:153], v[182:185], v[18:21]
	v_mfma_f32_16x16x32_bf16 v[22:25], v[158:161], v[182:185], v[22:25]
	v_mfma_f32_16x16x32_bf16 v[2:5], v[150:153], v[214:217], v[2:5]
	v_mfma_f32_16x16x32_bf16 v[6:9], v[158:161], v[214:217], v[6:9]
	s_setprio 0
	s_barrier
; #define PG8_STAGE(bufoff, gbase, voff) do { _Pragma("unroll") for (int _i = 0; _i < 2; ++_i) \
;         __builtin_amdgcn_global_load_lds((const unsigned*)((const char*)(gbase) + (voff)[_i]), (LAS unsigned*)(lds + (bufoff) + ldsw + _i * 8192), 16, 0, 0); } while (0)
; #define PG8_LDA(dst, b, h) do { _Pragma("unroll") for (int m = 0; m < 4; ++m) _Pragma("unroll") for (int k = 0; k < 2; ++k) dst[m][k] = *(const LAS bf16x8*)(lds + PG8_SA(b, h) + aoff + m * 2048 + k * 1024); } while (0)
; #define PG8_LDB(dst, b, h) do { _Pragma("unroll") for (int n = 0; n < 2; ++n) _Pragma("unroll") for (int k = 0; k < 2; ++k) dst[n][k] = *(const LAS bf16x8*)(lds + PG8_SB(b, h) + boff + n * 2048 + k * 1024); } while (0)
; #define PG8_MMA(ai, bj, At, Bt) do { __builtin_amdgcn_s_setprio(1); _Pragma("unroll") for (int m = 0; m < 4; ++m) _Pragma("unroll") for (int n = 0; n < 2; ++n) _Pragma("unroll") for (int k = 0; k < 2; ++k) \
;         acc[ai][bj][m][n] = __builtin_amdgcn_mfma_f32_16x16x32_bf16(Bt[n][k], At[m][k], acc[ai][bj][m][n], 0, 0, 0); __builtin_amdgcn_s_setprio(0); } while (0)
; #define PG8_WAIT_V(n) asm volatile("s_waitcnt vmcnt(" #n ")" ::: "memory")
; #define PG8_WAIT_L(n) asm volatile("s_waitcnt lgkmcnt(" #n ")" ::: "memory")
; #define PG8_BAR __builtin_amdgcn_s_barrier()
; #define PG8_SCHED __builtin_amdgcn_sched_barrier(0)
; template <class Epi, class Sched>
; __device__ __forceinline__ void gemm_phase(LAS unsigned char* lds, const Gemm g, const Sched& S, const Epi& E, const int tid, unsigned* last_sig = nullptr) {
;     ...
;             PG8_LDB(B0, 1, 0); PG8_LDB(B1, 1, 1); PG8_SCHED; PG8_LDA(At, 1, 0); PG8_STAGE(PG8_SA(0, 1), a2 + hstep, voffA);
;             PG8_WAIT_V(8); PG8_WAIT_L(0); PG8_BAR; PG8_MMA(0, 0, At, B0); PG8_MMA(0, 1, At, B1); PG8_BAR; PG8_SCHED;
	s_add_i32 s53, 0, 0x18000
	s_add_i32 s54, 0, 0x1c000
	v_add_u32_e32 v142, s53, v232
	v_add_u32_e32 v158, s54, v232
	ds_read_b128 v[130:133], v142
	ds_read_b128 v[134:137], v142 offset:1024
	ds_read_b128 v[138:141], v142 offset:2048
	ds_read_b128 v[142:145], v142 offset:3072
	ds_read_b128 v[146:149], v158
	ds_read_b128 v[150:153], v158 offset:1024
	ds_read_b128 v[154:157], v158 offset:2048
	ds_read_b128 v[158:161], v158 offset:3072
	s_add_u32 s14, s40, 0x40000
	s_addc_u32 s15, s41, 0
	s_mov_b32 m0, s44
	v_lshl_add_u64 v[238:239], s[14:15], 0, v[200:201]
	ds_read_b128 v[162:165], v234 offset:32768
	ds_read_b128 v[166:169], v234 offset:33792
	ds_read_b128 v[170:173], v234 offset:34816
	ds_read_b128 v[174:177], v234 offset:35840
	ds_read_b128 v[178:181], v234 offset:36864
	ds_read_b128 v[182:185], v234 offset:37888
	ds_read_b128 v[210:213], v234 offset:38912
	ds_read_b128 v[214:217], v234 offset:39936
	global_load_lds_dwordx4 v[238:239], off
	v_lshl_add_u64 v[238:239], s[14:15], 0, v[202:203]
	s_mov_b32 m0, s45
	s_nop 0
	global_load_lds_dwordx4 v[238:239], off
	s_waitcnt vmcnt(8)
	s_waitcnt lgkmcnt(0)
	s_barrier
	s_setprio 1
	s_waitcnt lgkmcnt(0)
	v_mfma_f32_16x16x32_bf16 v[122:125], v[130:133], v[162:165], v[122:125]
	v_mfma_f32_16x16x32_bf16 v[126:129], v[138:141], v[162:165], v[126:129]
	v_mfma_f32_16x16x32_bf16 v[106:109], v[130:133], v[170:173], v[106:109]
	v_mfma_f32_16x16x32_bf16 v[110:113], v[138:141], v[170:173], v[110:113]
	v_mfma_f32_16x16x32_bf16 v[90:93], v[130:133], v[178:181], v[90:93]
	v_mfma_f32_16x16x32_bf16 v[94:97], v[138:141], v[178:181], v[94:97]
	v_mfma_f32_16x16x32_bf16 v[74:77], v[130:133], v[210:213], v[74:77]
	v_mfma_f32_16x16x32_bf16 v[78:81], v[138:141], v[210:213], v[78:81]
	v_mfma_f32_16x16x32_bf16 v[122:125], v[134:137], v[166:169], v[122:125]
	v_mfma_f32_16x16x32_bf16 v[126:129], v[142:145], v[166:169], v[126:129]
	v_mfma_f32_16x16x32_bf16 v[106:109], v[134:137], v[174:177], v[106:109]
	v_mfma_f32_16x16x32_bf16 v[110:113], v[142:145], v[174:177], v[110:113]
	v_mfma_f32_16x16x32_bf16 v[90:93], v[134:137], v[182:185], v[90:93]
	v_mfma_f32_16x16x32_bf16 v[94:97], v[142:145], v[182:185], v[94:97]
	v_mfma_f32_16x16x32_bf16 v[74:77], v[134:137], v[214:217], v[74:77]
	v_mfma_f32_16x16x32_bf16 v[78:81], v[142:145], v[214:217], v[78:81]
	s_setprio 0
	s_setprio 1
	v_mfma_f32_16x16x32_bf16 v[114:117], v[146:149], v[162:165], v[114:117]
	v_mfma_f32_16x16x32_bf16 v[118:121], v[154:157], v[162:165], v[118:121]
	v_mfma_f32_16x16x32_bf16 v[98:101], v[146:149], v[170:173], v[98:101]
	v_mfma_f32_16x16x32_bf16 v[102:105], v[154:157], v[170:173], v[102:105]
	v_mfma_f32_16x16x32_bf16 v[82:85], v[146:149], v[178:181], v[82:85]
	v_mfma_f32_16x16x32_bf16 v[86:89], v[154:157], v[178:181], v[86:89]
	v_mfma_f32_16x16x32_bf16 v[66:69], v[146:149], v[210:213], v[66:69]
	v_mfma_f32_16x16x32_bf16 v[70:73], v[154:157], v[210:213], v[70:73]
	v_mfma_f32_16x16x32_bf16 v[114:117], v[150:153], v[166:169], v[114:117]
	v_mfma_f32_16x16x32_bf16 v[118:121], v[158:161], v[166:169], v[118:121]
	v_mfma_f32_16x16x32_bf16 v[98:101], v[150:153], v[174:177], v[98:101]
	v_mfma_f32_16x16x32_bf16 v[102:105], v[158:161], v[174:177], v[102:105]
	v_mfma_f32_16x16x32_bf16 v[82:85], v[150:153], v[182:185], v[82:85]
	v_mfma_f32_16x16x32_bf16 v[86:89], v[158:161], v[182:185], v[86:89]
	v_mfma_f32_16x16x32_bf16 v[66:69], v[150:153], v[214:217], v[66:69]
	v_mfma_f32_16x16x32_bf16 v[70:73], v[158:161], v[214:217], v[70:73]
	s_setprio 0
	s_barrier
; #define PG8_STAGE(bufoff, gbase, voff) do { _Pragma("unroll") for (int _i = 0; _i < 2; ++_i) \
;         __builtin_amdgcn_global_load_lds((const unsigned*)((const char*)(gbase) + (voff)[_i]), (LAS unsigned*)(lds + (bufoff) + ldsw + _i * 8192), 16, 0, 0); } while (0)
; #define PG8_LDA(dst, b, h) do { _Pragma("unroll") for (int m = 0; m < 4; ++m) _Pragma("unroll") for (int k = 0; k < 2; ++k) dst[m][k] = *(const LAS bf16x8*)(lds + PG8_SA(b, h) + aoff + m * 2048 + k * 1024); } while (0)
; #define PG8_MMA(ai, bj, At, Bt) do { __builtin_amdgcn_s_setprio(1); _Pragma("unroll") for (int m = 0; m < 4; ++m) _Pragma("unroll") for (int n = 0; n < 2; ++n) _Pragma("unroll") for (int k = 0; k < 2; ++k) \
;         acc[ai][bj][m][n] = __builtin_amdgcn_mfma_f32_16x16x32_bf16(Bt[n][k], At[m][k], acc[ai][bj][m][n], 0, 0, 0); __builtin_amdgcn_s_setprio(0); } while (0)
; #define PG8_WAIT_V(n) asm volatile("s_waitcnt vmcnt(" #n ")" ::: "memory")
; #define PG8_WAIT_L(n) asm volatile("s_waitcnt lgkmcnt(" #n ")" ::: "memory")
; #define PG8_BAR __builtin_amdgcn_s_barrier()
; #define PG8_SCHED __builtin_amdgcn_sched_barrier(0)
; template <class Epi, class Sched>
; __device__ __forceinline__ void gemm_phase(LAS unsigned char* lds, const Gemm g, const Sched& S, const Epi& E, const int tid, unsigned* last_sig = nullptr) {
;     ...
;             PG8_LDA(At, 1, 1); PG8_STAGE(PG8_SB(1, 0), b3, voffB); PG8_STAGE(PG8_SB(1, 1), b3 + hstep, voffB); PG8_STAGE(PG8_SA(1, 0), a3, voffA);
;             PG8_WAIT_V(8); PG8_WAIT_L(0); PG8_BAR; PG8_MMA(1, 0, At, B0); PG8_MMA(1, 1, At, B1); PG8_BAR; PG8_SCHED;
;         }
	s_add_i32 s14, s53, s42
	v_lshl_add_u64 v[218:219], v[218:219], 0, s[34:35]
	s_mov_b32 m0, s14
	ds_read_b128 v[162:165], v234 offset:49152
	ds_read_b128 v[166:169], v234 offset:50176
	ds_read_b128 v[170:173], v234 offset:51200
	ds_read_b128 v[174:177], v234 offset:52224
	ds_read_b128 v[178:181], v234 offset:53248
	ds_read_b128 v[182:185], v234 offset:54272
	ds_read_b128 v[210:213], v234 offset:55296
	ds_read_b128 v[214:217], v234 offset:56320
	global_load_lds_dwordx4 v[218:219], off
	s_add_i32 m0, s14, 0x2000
	s_add_u32 s14, s38, 0x40080
	v_lshl_add_u64 v[218:219], v[220:221], 0, s[34:35]
	s_addc_u32 s15, s39, 0
	s_add_i32 s38, s54, s42
	global_load_lds_dwordx4 v[218:219], off
	v_lshl_add_u64 v[218:219], s[14:15], 0, v[186:187]
	s_mov_b32 m0, s38
	s_nop 0
	global_load_lds_dwordx4 v[218:219], off
	v_lshl_add_u64 v[218:219], s[14:15], 0, v[204:205]
	s_add_i32 m0, s38, 0x2000
	s_nop 0
	global_load_lds_dwordx4 v[218:219], off
	v_lshl_add_u64 v[218:219], v[222:223], 0, s[34:35]
	s_mov_b32 m0, s46
	s_nop 0
	global_load_lds_dwordx4 v[218:219], off
	v_lshl_add_u64 v[218:219], v[236:237], 0, s[34:35]
	s_mov_b32 m0, s47
	s_nop 0
	global_load_lds_dwordx4 v[218:219], off
	s_waitcnt vmcnt(8)
	s_waitcnt lgkmcnt(0)
	s_barrier
	s_setprio 1
	s_waitcnt lgkmcnt(0)
	v_mfma_f32_16x16x32_bf16 v[58:61], v[130:133], v[162:165], v[58:61]
	v_mfma_f32_16x16x32_bf16 v[62:65], v[138:141], v[162:165], v[62:65]
	v_mfma_f32_16x16x32_bf16 v[42:45], v[130:133], v[170:173], v[42:45]
	v_mfma_f32_16x16x32_bf16 v[46:49], v[138:141], v[170:173], v[46:49]
	v_mfma_f32_16x16x32_bf16 v[26:29], v[130:133], v[178:181], v[26:29]
	v_mfma_f32_16x16x32_bf16 v[30:33], v[138:141], v[178:181], v[30:33]
	v_mfma_f32_16x16x32_bf16 v[10:13], v[130:133], v[210:213], v[10:13]
	v_mfma_f32_16x16x32_bf16 v[14:17], v[138:141], v[210:213], v[14:17]
	v_mfma_f32_16x16x32_bf16 v[58:61], v[134:137], v[166:169], v[58:61]
	v_mfma_f32_16x16x32_bf16 v[62:65], v[142:145], v[166:169], v[62:65]
	v_mfma_f32_16x16x32_bf16 v[42:45], v[134:137], v[174:177], v[42:45]
	v_mfma_f32_16x16x32_bf16 v[46:49], v[142:145], v[174:177], v[46:49]
	v_mfma_f32_16x16x32_bf16 v[26:29], v[134:137], v[182:185], v[26:29]
	v_mfma_f32_16x16x32_bf16 v[30:33], v[142:145], v[182:185], v[30:33]
	v_mfma_f32_16x16x32_bf16 v[10:13], v[134:137], v[214:217], v[10:13]
	v_mfma_f32_16x16x32_bf16 v[14:17], v[142:145], v[214:217], v[14:17]
	s_setprio 0
	s_setprio 1
	v_mfma_f32_16x16x32_bf16 v[50:53], v[146:149], v[162:165], v[50:53]
	v_mfma_f32_16x16x32_bf16 v[54:57], v[154:157], v[162:165], v[54:57]
	v_mfma_f32_16x16x32_bf16 v[34:37], v[146:149], v[170:173], v[34:37]
	v_mfma_f32_16x16x32_bf16 v[38:41], v[154:157], v[170:173], v[38:41]
	v_mfma_f32_16x16x32_bf16 v[18:21], v[146:149], v[178:181], v[18:21]
	v_mfma_f32_16x16x32_bf16 v[22:25], v[154:157], v[178:181], v[22:25]
	v_mfma_f32_16x16x32_bf16 v[2:5], v[146:149], v[210:213], v[2:5]
	v_mfma_f32_16x16x32_bf16 v[6:9], v[154:157], v[210:213], v[6:9]
	v_mfma_f32_16x16x32_bf16 v[50:53], v[150:153], v[166:169], v[50:53]
	v_mfma_f32_16x16x32_bf16 v[54:57], v[158:161], v[166:169], v[54:57]
	v_mfma_f32_16x16x32_bf16 v[34:37], v[150:153], v[174:177], v[34:37]
	v_mfma_f32_16x16x32_bf16 v[38:41], v[158:161], v[174:177], v[38:41]
	v_mfma_f32_16x16x32_bf16 v[18:21], v[150:153], v[182:185], v[18:21]
	v_mfma_f32_16x16x32_bf16 v[22:25], v[158:161], v[182:185], v[22:25]
	v_mfma_f32_16x16x32_bf16 v[2:5], v[150:153], v[214:217], v[2:5]
	v_mfma_f32_16x16x32_bf16 v[6:9], v[158:161], v[214:217], v[6:9]
	s_setprio 0
	s_barrier
	s_add_i32 s52, s52, 2
	s_add_u32 s22, s22, 0x100
	s_addc_u32 s23, s23, 0
	s_add_u32 s50, s50, 0x100
	s_addc_u32 s51, s51, 0
	s_cmp_gt_u32 s52, 13
	s_cbranch_scc1 .Lkpeel_exit_2

; #define PG8_BAR __builtin_amdgcn_s_barrier()
; template <class Epi, class Sched>
; __device__ __forceinline__ void gemm_phase(LAS unsigned char* lds, const Gemm g, const Sched& S, const Epi& E, const int tid, unsigned* last_sig = nullptr) {
;     ...
;         if (wr == 0) PG8_BAR;
.Lkpeel_exit_2:
	s_and_b64 vcc, exec, s[6:7]
	s_cbranch_vccz .LBB0_621
	s_barrier

; #define PG8_STAGE(bufoff, gbase, voff) do { _Pragma("unroll") for (int _i = 0; _i < 2; ++_i) \
;         __builtin_amdgcn_global_load_lds((const unsigned*)((const char*)(gbase) + (voff)[_i]), (LAS unsigned*)(lds + (bufoff) + ldsw + _i * 8192), 16, 0, 0); } while (0)
; #define PG8_LDA(dst, b, h) do { _Pragma("unroll") for (int m = 0; m < 4; ++m) _Pragma("unroll") for (int k = 0; k < 2; ++k) dst[m][k] = *(const LAS bf16x8*)(lds + PG8_SA(b, h) + aoff + m * 2048 + k * 1024); } while (0)
; #define PG8_LDB(dst, b, h) do { _Pragma("unroll") for (int n = 0; n < 2; ++n) _Pragma("unroll") for (int k = 0; k < 2; ++k) dst[n][k] = *(const LAS bf16x8*)(lds + PG8_SB(b, h) + boff + n * 2048 + k * 1024); } while (0)
; #define PG8_MMA(ai, bj, At, Bt) do { __builtin_amdgcn_s_setprio(1); _Pragma("unroll") for (int m = 0; m < 4; ++m) _Pragma("unroll") for (int n = 0; n < 2; ++n) _Pragma("unroll") for (int k = 0; k < 2; ++k) \
;         acc[ai][bj][m][n] = __builtin_amdgcn_mfma_f32_16x16x32_bf16(Bt[n][k], At[m][k], acc[ai][bj][m][n], 0, 0, 0); __builtin_amdgcn_s_setprio(0); } while (0)
; #define PG8_WAIT_V(n) asm volatile("s_waitcnt vmcnt(" #n ")" ::: "memory")
; #define PG8_WAIT_L(n) asm volatile("s_waitcnt lgkmcnt(" #n ")" ::: "memory")
; template <class Epi, class Sched>
; __device__ __forceinline__ void gemm_phase(LAS unsigned char* lds, const Gemm g, const Sched& S, const Epi& E, const int tid, unsigned* last_sig = nullptr) {
;     ...
;         for (int t = 0; t < nt; t += 2) {
;             const bool last = (t == nt - 2);
;             const char* a1 = cA + (size_t)(t + 1) * kstep;
;             const char* a2 = last ? nA : cA + (size_t)(t + 2) * kstep; const char* b2 = last ? nB : cB + (size_t)(t + 2) * kstep;
;             const char* a3 = a2 + kstep; const char* b3 = b2 + kstep;
;             PG8_LDB(B0, 0, 0); PG8_LDB(B1, 0, 1); PG8_SCHED; PG8_LDA(At, 0, 0); PG8_STAGE(PG8_SA(1, 1), a1 + hstep, voffA);
;             PG8_WAIT_V(8); PG8_WAIT_L(0); PG8_BAR; PG8_MMA(0, 0, At, B0); PG8_MMA(0, 1, At, B1); PG8_BAR; PG8_SCHED;
;     ...
; #pragma unroll
;         for (int a = 0; a < 2; ++a)
; #pragma unroll
;             for (int b = 0; b < 2; ++b)
; #pragma unroll
;                 for (int m = 0; m < 4; ++m)
; #pragma unroll
;                     for (int n = 0; n < 2; ++n) acc[a][b][m][n] = (f32x4){0.f, 0.f, 0.f, 0.f};
;         cur = nxt; cA = nA; cB = nB; ++ui;
.LBB0_690:
	s_ashr_i32 s13, s12, 31
	s_lshl_b64 s[14:15], s[12:13], 20
	v_readlane_b32 s16, v253, 4
	v_readlane_b32 s17, v253, 5
	s_add_u32 s16, s16, s14
	s_addc_u32 s17, s17, s15
	s_and_b64 s[14:15], s[0:1], exec
	s_cselect_b32 s13, s17, s21
	s_cselect_b32 s52, s16, s20
	s_ashr_i32 s11, s10, 31
	s_lshl_b64 s[14:15], s[10:11], 20
	s_add_u32 s18, s28, s14
	s_addc_u32 s19, s31, s15
	s_and_b64 s[14:15], s[0:1], exec
	s_cselect_b32 s11, s19, s23
	s_cselect_b32 s53, s18, s22
	s_add_u32 s54, s22, 0x100
	v_mov_b32_e32 v2, 0
	s_addc_u32 s55, s23, 0
	s_mov_b32 s56, -2
	v_mov_b32_e32 v3, v2
	v_mov_b32_e32 v4, v2
	v_mov_b32_e32 v5, v2
	v_mov_b32_e32 v6, v2
	v_mov_b32_e32 v7, v2
	v_mov_b32_e32 v8, v2
	v_mov_b32_e32 v9, v2
	v_mov_b32_e32 v14, v2
	v_mov_b32_e32 v15, v2
	v_mov_b32_e32 v16, v2
	v_mov_b32_e32 v17, v2
	v_mov_b32_e32 v18, v2
	v_mov_b32_e32 v19, v2
	v_mov_b32_e32 v20, v2
	v_mov_b32_e32 v21, v2
	v_mov_b32_e32 v30, v2
	v_mov_b32_e32 v31, v2
	v_mov_b32_e32 v32, v2
	v_mov_b32_e32 v33, v2
	v_mov_b32_e32 v34, v2
	v_mov_b32_e32 v35, v2
	v_mov_b32_e32 v36, v2
	v_mov_b32_e32 v37, v2
	v_mov_b32_e32 v46, v2
	v_mov_b32_e32 v47, v2
	v_mov_b32_e32 v48, v2
	v_mov_b32_e32 v49, v2
	v_mov_b32_e32 v50, v2
	v_mov_b32_e32 v51, v2
	v_mov_b32_e32 v52, v2
	v_mov_b32_e32 v53, v2
	v_mov_b32_e32 v10, v2
	v_mov_b32_e32 v11, v2
	v_mov_b32_e32 v12, v2
	v_mov_b32_e32 v13, v2
	v_mov_b32_e32 v22, v2
	v_mov_b32_e32 v23, v2
	v_mov_b32_e32 v24, v2
	v_mov_b32_e32 v25, v2
	v_mov_b32_e32 v26, v2
	v_mov_b32_e32 v27, v2
	v_mov_b32_e32 v28, v2
	v_mov_b32_e32 v29, v2
	v_mov_b32_e32 v38, v2
	v_mov_b32_e32 v39, v2
	v_mov_b32_e32 v40, v2
	v_mov_b32_e32 v41, v2
	v_mov_b32_e32 v42, v2
	v_mov_b32_e32 v43, v2
	v_mov_b32_e32 v44, v2
	v_mov_b32_e32 v45, v2
	v_mov_b32_e32 v54, v2
	v_mov_b32_e32 v55, v2
	v_mov_b32_e32 v56, v2
	v_mov_b32_e32 v57, v2
	v_mov_b32_e32 v58, v2
	v_mov_b32_e32 v59, v2
	v_mov_b32_e32 v60, v2
	v_mov_b32_e32 v61, v2
	v_mov_b32_e32 v62, v2
	v_mov_b32_e32 v63, v2
	v_mov_b32_e32 v64, v2
	v_mov_b32_e32 v65, v2
	v_mov_b32_e32 v66, v2
	v_mov_b32_e32 v67, v2
	v_mov_b32_e32 v68, v2
	v_mov_b32_e32 v69, v2
	v_mov_b32_e32 v70, v2
	v_mov_b32_e32 v71, v2
	v_mov_b32_e32 v72, v2
	v_mov_b32_e32 v73, v2
	v_mov_b32_e32 v78, v2
	v_mov_b32_e32 v79, v2
	v_mov_b32_e32 v80, v2
	v_mov_b32_e32 v81, v2
	v_mov_b32_e32 v82, v2
	v_mov_b32_e32 v83, v2
	v_mov_b32_e32 v84, v2
	v_mov_b32_e32 v85, v2
	v_mov_b32_e32 v94, v2
	v_mov_b32_e32 v95, v2
	v_mov_b32_e32 v96, v2
	v_mov_b32_e32 v97, v2
	v_mov_b32_e32 v98, v2
	v_mov_b32_e32 v99, v2
	v_mov_b32_e32 v100, v2
	v_mov_b32_e32 v101, v2
	v_mov_b32_e32 v110, v2
	v_mov_b32_e32 v111, v2
	v_mov_b32_e32 v112, v2
	v_mov_b32_e32 v113, v2
	v_mov_b32_e32 v114, v2
	v_mov_b32_e32 v115, v2
	v_mov_b32_e32 v116, v2
	v_mov_b32_e32 v117, v2
	v_mov_b32_e32 v74, v2
	v_mov_b32_e32 v75, v2
	v_mov_b32_e32 v76, v2
	v_mov_b32_e32 v77, v2
	v_mov_b32_e32 v86, v2
	v_mov_b32_e32 v87, v2
	v_mov_b32_e32 v88, v2
	v_mov_b32_e32 v89, v2
	v_mov_b32_e32 v90, v2
	v_mov_b32_e32 v91, v2
	v_mov_b32_e32 v92, v2
	v_mov_b32_e32 v93, v2
	v_mov_b32_e32 v102, v2
	v_mov_b32_e32 v103, v2
	v_mov_b32_e32 v104, v2
	v_mov_b32_e32 v105, v2
	v_mov_b32_e32 v106, v2
	v_mov_b32_e32 v107, v2
	v_mov_b32_e32 v108, v2
	v_mov_b32_e32 v109, v2
	v_mov_b32_e32 v118, v2
	v_mov_b32_e32 v119, v2
	v_mov_b32_e32 v120, v2
	v_mov_b32_e32 v121, v2
	v_mov_b32_e32 v122, v2
	v_mov_b32_e32 v123, v2
	v_mov_b32_e32 v124, v2
	v_mov_b32_e32 v125, v2
	v_mov_b32_e32 v126, v2
	v_mov_b32_e32 v127, v2
	v_mov_b32_e32 v128, v2
	v_mov_b32_e32 v129, v2
	s_cmp_eq_u32 s49, 1
	s_cbranch_scc1 .LBB0_691
	s_add_u32 s22, s20, 0x100
	s_addc_u32 s23, s21, 0
	s_add_i32 s14, 0, 0x10000
	s_cmp_eq_u32 s56, 28
	s_cselect_b32 s41, s13, s23
	s_cselect_b32 s40, s52, s22
	s_cselect_b32 s39, s11, s55
	s_cselect_b32 s38, s53, s54
	s_add_i32 s57, 0, 0x14000
	v_add_u32_e32 v148, s14, v156
	v_add_u32_e32 v159, s57, v156
	ds_read_b128 v[130:133], v148
	ds_read_b128 v[134:137], v148 offset:1024
	ds_read_b128 v[138:141], v148 offset:2048
	ds_read_b128 v[148:151], v148 offset:3072
	ds_read_b128 v[152:155], v159
	ds_read_b128 v[160:163], v159 offset:1024
	ds_read_b128 v[164:167], v159 offset:2048
	ds_read_b128 v[168:171], v159 offset:3072
	v_lshl_add_u64 v[184:185], s[20:21], 0, v[144:145]
	s_add_i32 m0, s43, 0xc000
	ds_read_b128 v[172:175], v158
	ds_read_b128 v[176:179], v158 offset:1024
	ds_read_b128 v[180:183], v158 offset:2048
	ds_read_b128 v[200:203], v158 offset:3072
	ds_read_b128 v[204:207], v158 offset:4096
	ds_read_b128 v[208:211], v158 offset:5120
	ds_read_b128 v[212:215], v158 offset:6144
	ds_read_b128 v[216:219], v158 offset:7168
	global_load_lds_dwordx4 v[184:185], off
	v_lshl_add_u64 v[184:185], s[20:21], 0, v[146:147]
	s_add_i32 m0, s43, 0xe000
	s_nop 0
	global_load_lds_dwordx4 v[184:185], off
	s_waitcnt vmcnt(24)
	s_waitcnt lgkmcnt(0)
	s_barrier
; #define PG8_STAGE(bufoff, gbase, voff) do { _Pragma("unroll") for (int _i = 0; _i < 2; ++_i) \
;         __builtin_amdgcn_global_load_lds((const unsigned*)((const char*)(gbase) + (voff)[_i]), (LAS unsigned*)(lds + (bufoff) + ldsw + _i * 8192), 16, 0, 0); } while (0)
; #define PG8_LDA(dst, b, h) do { _Pragma("unroll") for (int m = 0; m < 4; ++m) _Pragma("unroll") for (int k = 0; k < 2; ++k) dst[m][k] = *(const LAS bf16x8*)(lds + PG8_SA(b, h) + aoff + m * 2048 + k * 1024); } while (0)
; #define PG8_MMA(ai, bj, At, Bt) do { __builtin_amdgcn_s_setprio(1); _Pragma("unroll") for (int m = 0; m < 4; ++m) _Pragma("unroll") for (int n = 0; n < 2; ++n) _Pragma("unroll") for (int k = 0; k < 2; ++k) \
;         acc[ai][bj][m][n] = __builtin_amdgcn_mfma_f32_16x16x32_bf16(Bt[n][k], At[m][k], acc[ai][bj][m][n], 0, 0, 0); __builtin_amdgcn_s_setprio(0); } while (0)
; #define PG8_WAIT_V(n) asm volatile("s_waitcnt vmcnt(" #n ")" ::: "memory")
; #define PG8_WAIT_L(n) asm volatile("s_waitcnt lgkmcnt(" #n ")" ::: "memory")
; #define PG8_BAR __builtin_amdgcn_s_barrier()
; #define PG8_SCHED __builtin_amdgcn_sched_barrier(0)
; template <class Epi, class Sched>
; __device__ __forceinline__ void gemm_phase(LAS unsigned char* lds, const Gemm g, const Sched& S, const Epi& E, const int tid, unsigned* last_sig = nullptr) {
;     ...
;             PG8_WAIT_V(8); PG8_WAIT_L(0); PG8_BAR; PG8_MMA(0, 0, At, B0); PG8_MMA(0, 1, At, B1); PG8_BAR; PG8_SCHED;
;             PG8_LDA(At, 0, 1); PG8_STAGE(PG8_SB(0, 0), b2, voffB); PG8_STAGE(PG8_SB(0, 1), b2 + hstep, voffB); PG8_STAGE(PG8_SA(0, 0), a2, voffA);
;             PG8_WAIT_V(8); PG8_WAIT_L(0); PG8_BAR; PG8_MMA(1, 0, At, B0); PG8_MMA(1, 1, At, B1); PG8_BAR; PG8_SCHED;
	s_setprio 1
	s_waitcnt lgkmcnt(0)
	v_mfma_f32_16x16x32_bf16 v[126:129], v[130:133], v[172:175], v[126:129]
	v_mfma_f32_16x16x32_bf16 v[122:125], v[138:141], v[172:175], v[122:125]
	v_mfma_f32_16x16x32_bf16 v[118:121], v[130:133], v[180:183], v[118:121]
	v_mfma_f32_16x16x32_bf16 v[106:109], v[138:141], v[180:183], v[106:109]
	v_mfma_f32_16x16x32_bf16 v[102:105], v[130:133], v[204:207], v[102:105]
	v_mfma_f32_16x16x32_bf16 v[90:93], v[138:141], v[204:207], v[90:93]
	v_mfma_f32_16x16x32_bf16 v[86:89], v[130:133], v[212:215], v[86:89]
	v_mfma_f32_16x16x32_bf16 v[74:77], v[138:141], v[212:215], v[74:77]
	v_mfma_f32_16x16x32_bf16 v[126:129], v[134:137], v[176:179], v[126:129]
	v_mfma_f32_16x16x32_bf16 v[122:125], v[148:151], v[176:179], v[122:125]
	v_mfma_f32_16x16x32_bf16 v[118:121], v[134:137], v[200:203], v[118:121]
	v_mfma_f32_16x16x32_bf16 v[106:109], v[148:151], v[200:203], v[106:109]
	v_mfma_f32_16x16x32_bf16 v[102:105], v[134:137], v[208:211], v[102:105]
	v_mfma_f32_16x16x32_bf16 v[90:93], v[148:151], v[208:211], v[90:93]
	v_mfma_f32_16x16x32_bf16 v[86:89], v[134:137], v[216:219], v[86:89]
	v_mfma_f32_16x16x32_bf16 v[74:77], v[148:151], v[216:219], v[74:77]
	s_setprio 0
	s_setprio 1
	v_mfma_f32_16x16x32_bf16 v[114:117], v[152:155], v[172:175], v[114:117]
	v_mfma_f32_16x16x32_bf16 v[110:113], v[164:167], v[172:175], v[110:113]
	v_mfma_f32_16x16x32_bf16 v[98:101], v[152:155], v[180:183], v[98:101]
	v_mfma_f32_16x16x32_bf16 v[94:97], v[164:167], v[180:183], v[94:97]
	v_mfma_f32_16x16x32_bf16 v[82:85], v[152:155], v[204:207], v[82:85]
	v_mfma_f32_16x16x32_bf16 v[78:81], v[164:167], v[204:207], v[78:81]
	v_mfma_f32_16x16x32_bf16 v[70:73], v[152:155], v[212:215], v[70:73]
	v_mfma_f32_16x16x32_bf16 v[66:69], v[164:167], v[212:215], v[66:69]
	v_mfma_f32_16x16x32_bf16 v[114:117], v[160:163], v[176:179], v[114:117]
	v_mfma_f32_16x16x32_bf16 v[110:113], v[168:171], v[176:179], v[110:113]
	v_mfma_f32_16x16x32_bf16 v[98:101], v[160:163], v[200:203], v[98:101]
	v_mfma_f32_16x16x32_bf16 v[94:97], v[168:171], v[200:203], v[94:97]
	v_mfma_f32_16x16x32_bf16 v[82:85], v[160:163], v[208:211], v[82:85]
	v_mfma_f32_16x16x32_bf16 v[78:81], v[168:171], v[208:211], v[78:81]
	v_mfma_f32_16x16x32_bf16 v[70:73], v[160:163], v[216:219], v[70:73]
	v_mfma_f32_16x16x32_bf16 v[66:69], v[168:171], v[216:219], v[66:69]
	s_setprio 0
	s_barrier
	s_add_i32 s14, s14, s42
	v_lshl_add_u64 v[184:185], s[38:39], 0, v[186:187]
	s_mov_b32 m0, s14
	ds_read_b128 v[172:175], v158 offset:16384
	ds_read_b128 v[176:179], v158 offset:17408
	ds_read_b128 v[180:183], v158 offset:18432
	ds_read_b128 v[200:203], v158 offset:19456
	ds_read_b128 v[204:207], v158 offset:20480
	ds_read_b128 v[208:211], v158 offset:21504
	ds_read_b128 v[212:215], v158 offset:22528
	ds_read_b128 v[216:219], v158 offset:23552
	global_load_lds_dwordx4 v[184:185], off
	s_add_i32 m0, s14, 0x2000
	s_add_u32 s14, s38, 0x80000
	v_lshl_add_u64 v[220:221], s[38:39], 0, v[142:143]
	s_addc_u32 s15, s39, 0
	s_add_i32 s20, s57, s42
	global_load_lds_dwordx4 v[220:221], off
	v_lshl_add_u64 v[222:223], s[14:15], 0, v[186:187]
	s_mov_b32 m0, s20
	v_lshl_add_u64 v[232:233], s[40:41], 0, v[142:143]
	global_load_lds_dwordx4 v[222:223], off
	v_lshl_add_u64 v[222:223], s[14:15], 0, v[142:143]
	s_add_i32 m0, s20, 0x2000
	s_nop 0
	global_load_lds_dwordx4 v[222:223], off
	v_lshl_add_u64 v[222:223], s[40:41], 0, v[186:187]
	s_mov_b32 m0, s43
	s_nop 0
	global_load_lds_dwordx4 v[222:223], off
	s_mov_b32 m0, s44
	s_nop 0
	global_load_lds_dwordx4 v[232:233], off
	s_waitcnt vmcnt(24)
	s_waitcnt lgkmcnt(0)
	s_barrier
	s_setprio 1
	s_waitcnt lgkmcnt(0)
	v_mfma_f32_16x16x32_bf16 v[62:65], v[130:133], v[172:175], v[62:65]
	v_mfma_f32_16x16x32_bf16 v[58:61], v[138:141], v[172:175], v[58:61]
	v_mfma_f32_16x16x32_bf16 v[54:57], v[130:133], v[180:183], v[54:57]
	v_mfma_f32_16x16x32_bf16 v[42:45], v[138:141], v[180:183], v[42:45]
	v_mfma_f32_16x16x32_bf16 v[38:41], v[130:133], v[204:207], v[38:41]
	v_mfma_f32_16x16x32_bf16 v[26:29], v[138:141], v[204:207], v[26:29]
	v_mfma_f32_16x16x32_bf16 v[22:25], v[130:133], v[212:215], v[22:25]
	v_mfma_f32_16x16x32_bf16 v[10:13], v[138:141], v[212:215], v[10:13]
	v_mfma_f32_16x16x32_bf16 v[62:65], v[134:137], v[176:179], v[62:65]
	v_mfma_f32_16x16x32_bf16 v[58:61], v[148:151], v[176:179], v[58:61]
	v_mfma_f32_16x16x32_bf16 v[54:57], v[134:137], v[200:203], v[54:57]
	v_mfma_f32_16x16x32_bf16 v[42:45], v[148:151], v[200:203], v[42:45]
	v_mfma_f32_16x16x32_bf16 v[38:41], v[134:137], v[208:211], v[38:41]
	v_mfma_f32_16x16x32_bf16 v[26:29], v[148:151], v[208:211], v[26:29]
	v_mfma_f32_16x16x32_bf16 v[22:25], v[134:137], v[216:219], v[22:25]
	v_mfma_f32_16x16x32_bf16 v[10:13], v[148:151], v[216:219], v[10:13]
	s_setprio 0
	s_setprio 1
	v_mfma_f32_16x16x32_bf16 v[50:53], v[152:155], v[172:175], v[50:53]
	v_mfma_f32_16x16x32_bf16 v[46:49], v[164:167], v[172:175], v[46:49]
	v_mfma_f32_16x16x32_bf16 v[34:37], v[152:155], v[180:183], v[34:37]
	v_mfma_f32_16x16x32_bf16 v[30:33], v[164:167], v[180:183], v[30:33]
	v_mfma_f32_16x16x32_bf16 v[18:21], v[152:155], v[204:207], v[18:21]
	v_mfma_f32_16x16x32_bf16 v[14:17], v[164:167], v[204:207], v[14:17]
	v_mfma_f32_16x16x32_bf16 v[6:9], v[152:155], v[212:215], v[6:9]
	v_mfma_f32_16x16x32_bf16 v[2:5], v[164:167], v[212:215], v[2:5]
	v_mfma_f32_16x16x32_bf16 v[50:53], v[160:163], v[176:179], v[50:53]
	v_mfma_f32_16x16x32_bf16 v[46:49], v[168:171], v[176:179], v[46:49]
	v_mfma_f32_16x16x32_bf16 v[34:37], v[160:163], v[200:203], v[34:37]
	v_mfma_f32_16x16x32_bf16 v[30:33], v[168:171], v[200:203], v[30:33]
	v_mfma_f32_16x16x32_bf16 v[18:21], v[160:163], v[208:211], v[18:21]
	v_mfma_f32_16x16x32_bf16 v[14:17], v[168:171], v[208:211], v[14:17]
	v_mfma_f32_16x16x32_bf16 v[6:9], v[160:163], v[216:219], v[6:9]
	v_mfma_f32_16x16x32_bf16 v[2:5], v[168:171], v[216:219], v[2:5]
	s_setprio 0
	s_barrier
; #define PG8_STAGE(bufoff, gbase, voff) do { _Pragma("unroll") for (int _i = 0; _i < 2; ++_i) \
;         __builtin_amdgcn_global_load_lds((const unsigned*)((const char*)(gbase) + (voff)[_i]), (LAS unsigned*)(lds + (bufoff) + ldsw + _i * 8192), 16, 0, 0); } while (0)
; #define PG8_LDA(dst, b, h) do { _Pragma("unroll") for (int m = 0; m < 4; ++m) _Pragma("unroll") for (int k = 0; k < 2; ++k) dst[m][k] = *(const LAS bf16x8*)(lds + PG8_SA(b, h) + aoff + m * 2048 + k * 1024); } while (0)
; #define PG8_LDB(dst, b, h) do { _Pragma("unroll") for (int n = 0; n < 2; ++n) _Pragma("unroll") for (int k = 0; k < 2; ++k) dst[n][k] = *(const LAS bf16x8*)(lds + PG8_SB(b, h) + boff + n * 2048 + k * 1024); } while (0)
; #define PG8_MMA(ai, bj, At, Bt) do { __builtin_amdgcn_s_setprio(1); _Pragma("unroll") for (int m = 0; m < 4; ++m) _Pragma("unroll") for (int n = 0; n < 2; ++n) _Pragma("unroll") for (int k = 0; k < 2; ++k) \
;         acc[ai][bj][m][n] = __builtin_amdgcn_mfma_f32_16x16x32_bf16(Bt[n][k], At[m][k], acc[ai][bj][m][n], 0, 0, 0); __builtin_amdgcn_s_setprio(0); } while (0)
; #define PG8_WAIT_V(n) asm volatile("s_waitcnt vmcnt(" #n ")" ::: "memory")
; #define PG8_WAIT_L(n) asm volatile("s_waitcnt lgkmcnt(" #n ")" ::: "memory")
; #define PG8_BAR __builtin_amdgcn_s_barrier()
; #define PG8_SCHED __builtin_amdgcn_sched_barrier(0)
; template <class Epi, class Sched>
; __device__ __forceinline__ void gemm_phase(LAS unsigned char* lds, const Gemm g, const Sched& S, const Epi& E, const int tid, unsigned* last_sig = nullptr) {
;     ...
;             PG8_LDB(B0, 1, 0); PG8_LDB(B1, 1, 1); PG8_SCHED; PG8_LDA(At, 1, 0); PG8_STAGE(PG8_SA(0, 1), a2 + hstep, voffA);
;             PG8_WAIT_V(8); PG8_WAIT_L(0); PG8_BAR; PG8_MMA(0, 0, At, B0); PG8_MMA(0, 1, At, B1); PG8_BAR; PG8_SCHED;
	s_add_i32 s20, 0, 0x18000
	s_add_i32 s21, 0, 0x1c000
	v_add_u32_e32 v148, s20, v156
	v_add_u32_e32 v159, s21, v156
	ds_read_b128 v[130:133], v148
	ds_read_b128 v[134:137], v148 offset:1024
	ds_read_b128 v[138:141], v148 offset:2048
	ds_read_b128 v[148:151], v148 offset:3072
	ds_read_b128 v[152:155], v159
	ds_read_b128 v[160:163], v159 offset:1024
	ds_read_b128 v[164:167], v159 offset:2048
	ds_read_b128 v[168:171], v159 offset:3072
	s_add_u32 s14, s40, 0x80000
	s_addc_u32 s15, s41, 0
	s_mov_b32 m0, s45
	v_lshl_add_u64 v[234:235], s[14:15], 0, v[186:187]
	ds_read_b128 v[172:175], v158 offset:32768
	ds_read_b128 v[176:179], v158 offset:33792
	ds_read_b128 v[180:183], v158 offset:34816
	ds_read_b128 v[200:203], v158 offset:35840
	ds_read_b128 v[204:207], v158 offset:36864
	ds_read_b128 v[208:211], v158 offset:37888
	ds_read_b128 v[212:215], v158 offset:38912
	ds_read_b128 v[216:219], v158 offset:39936
	global_load_lds_dwordx4 v[234:235], off
	v_lshl_add_u64 v[234:235], s[14:15], 0, v[142:143]
	s_mov_b32 m0, s46
	s_nop 0
	global_load_lds_dwordx4 v[234:235], off
	s_waitcnt vmcnt(8)
	s_waitcnt lgkmcnt(0)
	s_barrier
	s_setprio 1
	s_waitcnt lgkmcnt(0)
	v_mfma_f32_16x16x32_bf16 v[126:129], v[130:133], v[172:175], v[126:129]
	v_mfma_f32_16x16x32_bf16 v[122:125], v[138:141], v[172:175], v[122:125]
	v_mfma_f32_16x16x32_bf16 v[118:121], v[130:133], v[180:183], v[118:121]
	v_mfma_f32_16x16x32_bf16 v[106:109], v[138:141], v[180:183], v[106:109]
	v_mfma_f32_16x16x32_bf16 v[102:105], v[130:133], v[204:207], v[102:105]
	v_mfma_f32_16x16x32_bf16 v[90:93], v[138:141], v[204:207], v[90:93]
	v_mfma_f32_16x16x32_bf16 v[86:89], v[130:133], v[212:215], v[86:89]
	v_mfma_f32_16x16x32_bf16 v[74:77], v[138:141], v[212:215], v[74:77]
	v_mfma_f32_16x16x32_bf16 v[126:129], v[134:137], v[176:179], v[126:129]
	v_mfma_f32_16x16x32_bf16 v[122:125], v[148:151], v[176:179], v[122:125]
	v_mfma_f32_16x16x32_bf16 v[118:121], v[134:137], v[200:203], v[118:121]
	v_mfma_f32_16x16x32_bf16 v[106:109], v[148:151], v[200:203], v[106:109]
	v_mfma_f32_16x16x32_bf16 v[102:105], v[134:137], v[208:211], v[102:105]
	v_mfma_f32_16x16x32_bf16 v[90:93], v[148:151], v[208:211], v[90:93]
	v_mfma_f32_16x16x32_bf16 v[86:89], v[134:137], v[216:219], v[86:89]
	v_mfma_f32_16x16x32_bf16 v[74:77], v[148:151], v[216:219], v[74:77]
	s_setprio 0
	s_setprio 1
	v_mfma_f32_16x16x32_bf16 v[114:117], v[152:155], v[172:175], v[114:117]
	v_mfma_f32_16x16x32_bf16 v[110:113], v[164:167], v[172:175], v[110:113]
	v_mfma_f32_16x16x32_bf16 v[98:101], v[152:155], v[180:183], v[98:101]
	v_mfma_f32_16x16x32_bf16 v[94:97], v[164:167], v[180:183], v[94:97]
	v_mfma_f32_16x16x32_bf16 v[82:85], v[152:155], v[204:207], v[82:85]
	v_mfma_f32_16x16x32_bf16 v[78:81], v[164:167], v[204:207], v[78:81]
	v_mfma_f32_16x16x32_bf16 v[70:73], v[152:155], v[212:215], v[70:73]
	v_mfma_f32_16x16x32_bf16 v[66:69], v[164:167], v[212:215], v[66:69]
	v_mfma_f32_16x16x32_bf16 v[114:117], v[160:163], v[176:179], v[114:117]
	v_mfma_f32_16x16x32_bf16 v[110:113], v[168:171], v[176:179], v[110:113]
	v_mfma_f32_16x16x32_bf16 v[98:101], v[160:163], v[200:203], v[98:101]
	v_mfma_f32_16x16x32_bf16 v[94:97], v[168:171], v[200:203], v[94:97]
	v_mfma_f32_16x16x32_bf16 v[82:85], v[160:163], v[208:211], v[82:85]
	v_mfma_f32_16x16x32_bf16 v[78:81], v[168:171], v[208:211], v[78:81]
	v_mfma_f32_16x16x32_bf16 v[70:73], v[160:163], v[216:219], v[70:73]
	v_mfma_f32_16x16x32_bf16 v[66:69], v[168:171], v[216:219], v[66:69]
	s_setprio 0
	s_barrier
; #define PG8_STAGE(bufoff, gbase, voff) do { _Pragma("unroll") for (int _i = 0; _i < 2; ++_i) \
;         __builtin_amdgcn_global_load_lds((const unsigned*)((const char*)(gbase) + (voff)[_i]), (LAS unsigned*)(lds + (bufoff) + ldsw + _i * 8192), 16, 0, 0); } while (0)
; #define PG8_LDA(dst, b, h) do { _Pragma("unroll") for (int m = 0; m < 4; ++m) _Pragma("unroll") for (int k = 0; k < 2; ++k) dst[m][k] = *(const LAS bf16x8*)(lds + PG8_SA(b, h) + aoff + m * 2048 + k * 1024); } while (0)
; #define PG8_MMA(ai, bj, At, Bt) do { __builtin_amdgcn_s_setprio(1); _Pragma("unroll") for (int m = 0; m < 4; ++m) _Pragma("unroll") for (int n = 0; n < 2; ++n) _Pragma("unroll") for (int k = 0; k < 2; ++k) \
;         acc[ai][bj][m][n] = __builtin_amdgcn_mfma_f32_16x16x32_bf16(Bt[n][k], At[m][k], acc[ai][bj][m][n], 0, 0, 0); __builtin_amdgcn_s_setprio(0); } while (0)
; #define PG8_WAIT_V(n) asm volatile("s_waitcnt vmcnt(" #n ")" ::: "memory")
; #define PG8_WAIT_L(n) asm volatile("s_waitcnt lgkmcnt(" #n ")" ::: "memory")
; #define PG8_BAR __builtin_amdgcn_s_barrier()
; #define PG8_SCHED __builtin_amdgcn_sched_barrier(0)
; template <class Epi, class Sched>
; __device__ __forceinline__ void gemm_phase(LAS unsigned char* lds, const Gemm g, const Sched& S, const Epi& E, const int tid, unsigned* last_sig = nullptr) {
;     ...
;             PG8_LDA(At, 1, 1); PG8_STAGE(PG8_SB(1, 0), b3, voffB); PG8_STAGE(PG8_SB(1, 1), b3 + hstep, voffB); PG8_STAGE(PG8_SA(1, 0), a3, voffA);
;             PG8_WAIT_V(8); PG8_WAIT_L(0); PG8_BAR; PG8_MMA(1, 0, At, B0); PG8_MMA(1, 1, At, B1); PG8_BAR; PG8_SCHED;
;         }
	s_add_i32 s14, s20, s42
	v_lshl_add_u64 v[184:185], v[184:185], 0, s[34:35]
	s_mov_b32 m0, s14
	ds_read_b128 v[172:175], v158 offset:49152
	ds_read_b128 v[176:179], v158 offset:50176
	ds_read_b128 v[180:183], v158 offset:51200
	ds_read_b128 v[200:203], v158 offset:52224
	ds_read_b128 v[204:207], v158 offset:53248
	ds_read_b128 v[208:211], v158 offset:54272
	ds_read_b128 v[212:215], v158 offset:55296
	ds_read_b128 v[216:219], v158 offset:56320
	global_load_lds_dwordx4 v[184:185], off
	s_add_i32 m0, s14, 0x2000
	s_add_u32 s14, s38, 0x80080
	v_lshl_add_u64 v[184:185], v[220:221], 0, s[34:35]
	s_addc_u32 s15, s39, 0
	s_add_i32 s20, s21, s42
	global_load_lds_dwordx4 v[184:185], off
	v_lshl_add_u64 v[184:185], s[14:15], 0, v[186:187]
	s_mov_b32 m0, s20
	s_nop 0
	global_load_lds_dwordx4 v[184:185], off
	v_lshl_add_u64 v[184:185], s[14:15], 0, v[142:143]
	s_add_i32 m0, s20, 0x2000
	s_nop 0
	global_load_lds_dwordx4 v[184:185], off
	v_lshl_add_u64 v[184:185], v[222:223], 0, s[34:35]
	s_mov_b32 m0, s47
	s_nop 0
	global_load_lds_dwordx4 v[184:185], off
	v_lshl_add_u64 v[184:185], v[232:233], 0, s[34:35]
	s_mov_b32 m0, s48
	s_nop 0
	global_load_lds_dwordx4 v[184:185], off
	s_waitcnt vmcnt(8)
	s_waitcnt lgkmcnt(0)
	s_barrier
	s_setprio 1
	s_waitcnt lgkmcnt(0)
	v_mfma_f32_16x16x32_bf16 v[62:65], v[130:133], v[172:175], v[62:65]
	v_mfma_f32_16x16x32_bf16 v[58:61], v[138:141], v[172:175], v[58:61]
	v_mfma_f32_16x16x32_bf16 v[54:57], v[130:133], v[180:183], v[54:57]
	v_mfma_f32_16x16x32_bf16 v[42:45], v[138:141], v[180:183], v[42:45]
	v_mfma_f32_16x16x32_bf16 v[38:41], v[130:133], v[204:207], v[38:41]
	v_mfma_f32_16x16x32_bf16 v[26:29], v[138:141], v[204:207], v[26:29]
	v_mfma_f32_16x16x32_bf16 v[22:25], v[130:133], v[212:215], v[22:25]
	v_mfma_f32_16x16x32_bf16 v[10:13], v[138:141], v[212:215], v[10:13]
	v_mfma_f32_16x16x32_bf16 v[62:65], v[134:137], v[176:179], v[62:65]
	v_mfma_f32_16x16x32_bf16 v[58:61], v[148:151], v[176:179], v[58:61]
	v_mfma_f32_16x16x32_bf16 v[54:57], v[134:137], v[200:203], v[54:57]
	v_mfma_f32_16x16x32_bf16 v[42:45], v[148:151], v[200:203], v[42:45]
	v_mfma_f32_16x16x32_bf16 v[38:41], v[134:137], v[208:211], v[38:41]
	v_mfma_f32_16x16x32_bf16 v[26:29], v[148:151], v[208:211], v[26:29]
	v_mfma_f32_16x16x32_bf16 v[22:25], v[134:137], v[216:219], v[22:25]
	v_mfma_f32_16x16x32_bf16 v[10:13], v[148:151], v[216:219], v[10:13]
	s_setprio 0
	s_setprio 1
	v_mfma_f32_16x16x32_bf16 v[50:53], v[152:155], v[172:175], v[50:53]
	v_mfma_f32_16x16x32_bf16 v[46:49], v[164:167], v[172:175], v[46:49]
	v_mfma_f32_16x16x32_bf16 v[34:37], v[152:155], v[180:183], v[34:37]
	v_mfma_f32_16x16x32_bf16 v[30:33], v[164:167], v[180:183], v[30:33]
	v_mfma_f32_16x16x32_bf16 v[18:21], v[152:155], v[204:207], v[18:21]
	v_mfma_f32_16x16x32_bf16 v[14:17], v[164:167], v[204:207], v[14:17]
	v_mfma_f32_16x16x32_bf16 v[6:9], v[152:155], v[212:215], v[6:9]
	v_mfma_f32_16x16x32_bf16 v[2:5], v[164:167], v[212:215], v[2:5]
	v_mfma_f32_16x16x32_bf16 v[50:53], v[160:163], v[176:179], v[50:53]
	v_mfma_f32_16x16x32_bf16 v[46:49], v[168:171], v[176:179], v[46:49]
	v_mfma_f32_16x16x32_bf16 v[34:37], v[160:163], v[200:203], v[34:37]
	v_mfma_f32_16x16x32_bf16 v[30:33], v[168:171], v[200:203], v[30:33]
	v_mfma_f32_16x16x32_bf16 v[18:21], v[160:163], v[208:211], v[18:21]
	v_mfma_f32_16x16x32_bf16 v[14:17], v[168:171], v[208:211], v[14:17]
	v_mfma_f32_16x16x32_bf16 v[6:9], v[160:163], v[216:219], v[6:9]
	v_mfma_f32_16x16x32_bf16 v[2:5], v[168:171], v[216:219], v[2:5]
	s_setprio 0
	s_barrier
	s_add_i32 s56, s56, 2
	s_add_u32 s54, s54, 0x100
	s_addc_u32 s55, s55, 0
	s_cmp_gt_u32 s56, 29
	s_mov_b64 s[20:21], s[22:23]
	s_cbranch_scc1 .Lkpeel_exit_3

; #define PG8_STAGE(bufoff, gbase, voff) do { _Pragma("unroll") for (int _i = 0; _i < 2; ++_i) \
;         __builtin_amdgcn_global_load_lds((const unsigned*)((const char*)(gbase) + (voff)[_i]), (LAS unsigned*)(lds + (bufoff) + ldsw + _i * 8192), 16, 0, 0); } while (0)
; #define PG8_LDA(dst, b, h) do { _Pragma("unroll") for (int m = 0; m < 4; ++m) _Pragma("unroll") for (int k = 0; k < 2; ++k) dst[m][k] = *(const LAS bf16x8*)(lds + PG8_SA(b, h) + aoff + m * 2048 + k * 1024); } while (0)
; #define PG8_LDB(dst, b, h) do { _Pragma("unroll") for (int n = 0; n < 2; ++n) _Pragma("unroll") for (int k = 0; k < 2; ++k) dst[n][k] = *(const LAS bf16x8*)(lds + PG8_SB(b, h) + boff + n * 2048 + k * 1024); } while (0)
; #define PG8_MMA(ai, bj, At, Bt) do { __builtin_amdgcn_s_setprio(1); _Pragma("unroll") for (int m = 0; m < 4; ++m) _Pragma("unroll") for (int n = 0; n < 2; ++n) _Pragma("unroll") for (int k = 0; k < 2; ++k) \
;         acc[ai][bj][m][n] = __builtin_amdgcn_mfma_f32_16x16x32_bf16(Bt[n][k], At[m][k], acc[ai][bj][m][n], 0, 0, 0); __builtin_amdgcn_s_setprio(0); } while (0)
; #define PG8_WAIT_V(n) asm volatile("s_waitcnt vmcnt(" #n ")" ::: "memory")
; #define PG8_WAIT_L(n) asm volatile("s_waitcnt lgkmcnt(" #n ")" ::: "memory")
; template <class Epi, class Sched>
; __device__ __forceinline__ void gemm_phase(LAS unsigned char* lds, const Gemm g, const Sched& S, const Epi& E, const int tid, unsigned* last_sig = nullptr) {
;     ...
;         for (int t = 0; t < nt; t += 2) {
;             const bool last = (t == nt - 2);
;             const char* a1 = cA + (size_t)(t + 1) * kstep;
;             const char* a2 = last ? nA : cA + (size_t)(t + 2) * kstep; const char* b2 = last ? nB : cB + (size_t)(t + 2) * kstep;
;             const char* a3 = a2 + kstep; const char* b3 = b2 + kstep;
;             PG8_LDB(B0, 0, 0); PG8_LDB(B1, 0, 1); PG8_SCHED; PG8_LDA(At, 0, 0); PG8_STAGE(PG8_SA(1, 1), a1 + hstep, voffA);
;             PG8_WAIT_V(8); PG8_WAIT_L(0); PG8_BAR; PG8_MMA(0, 0, At, B0); PG8_MMA(0, 1, At, B1); PG8_BAR; PG8_SCHED;
;     ...
; #pragma unroll
;         for (int a = 0; a < 2; ++a)
; #pragma unroll
;             for (int b = 0; b < 2; ++b)
; #pragma unroll
;                 for (int m = 0; m < 4; ++m)
; #pragma unroll
;                     for (int n = 0; n < 2; ++n) acc[a][b][m][n] = (f32x4){0.f, 0.f, 0.f, 0.f};
;         cur = nxt; cA = nA; cB = nB; ++ui;
.LBB0_1103:
	s_ashr_i32 s19, s18, 31
	s_lshl_b64 s[14:15], s[18:19], 20
	v_readlane_b32 s22, v252, 31
	v_readlane_b32 s23, v252, 32
	s_add_u32 s22, s22, s14
	s_addc_u32 s23, s23, s15
	s_and_b64 s[4:5], s[4:5], exec
	s_cselect_b32 s17, s23, s47
	s_cselect_b32 s19, s22, s46
	s_add_u32 s4, s46, 0x80080
	s_addc_u32 s5, s47, 0
	s_add_u32 s56, s44, 0x100
	v_mov_b32_e32 v2, 0
	s_addc_u32 s57, s45, 0
	s_mov_b32 s58, -2
	v_mov_b32_e32 v3, v2
	v_mov_b32_e32 v4, v2
	v_mov_b32_e32 v5, v2
	v_mov_b32_e32 v10, v2
	v_mov_b32_e32 v11, v2
	v_mov_b32_e32 v12, v2
	v_mov_b32_e32 v13, v2
	v_mov_b32_e32 v18, v2
	v_mov_b32_e32 v19, v2
	v_mov_b32_e32 v20, v2
	v_mov_b32_e32 v21, v2
	v_mov_b32_e32 v26, v2
	v_mov_b32_e32 v27, v2
	v_mov_b32_e32 v28, v2
	v_mov_b32_e32 v29, v2
	v_mov_b32_e32 v34, v2
	v_mov_b32_e32 v35, v2
	v_mov_b32_e32 v36, v2
	v_mov_b32_e32 v37, v2
	v_mov_b32_e32 v42, v2
	v_mov_b32_e32 v43, v2
	v_mov_b32_e32 v44, v2
	v_mov_b32_e32 v45, v2
	v_mov_b32_e32 v50, v2
	v_mov_b32_e32 v51, v2
	v_mov_b32_e32 v52, v2
	v_mov_b32_e32 v53, v2
	v_mov_b32_e32 v58, v2
	v_mov_b32_e32 v59, v2
	v_mov_b32_e32 v60, v2
	v_mov_b32_e32 v61, v2
	v_mov_b32_e32 v6, v2
	v_mov_b32_e32 v7, v2
	v_mov_b32_e32 v8, v2
	v_mov_b32_e32 v9, v2
	v_mov_b32_e32 v14, v2
	v_mov_b32_e32 v15, v2
	v_mov_b32_e32 v16, v2
	v_mov_b32_e32 v17, v2
	v_mov_b32_e32 v22, v2
	v_mov_b32_e32 v23, v2
	v_mov_b32_e32 v24, v2
	v_mov_b32_e32 v25, v2
	v_mov_b32_e32 v30, v2
	v_mov_b32_e32 v31, v2
	v_mov_b32_e32 v32, v2
	v_mov_b32_e32 v33, v2
	v_mov_b32_e32 v38, v2
	v_mov_b32_e32 v39, v2
	v_mov_b32_e32 v40, v2
	v_mov_b32_e32 v41, v2
	v_mov_b32_e32 v46, v2
	v_mov_b32_e32 v47, v2
	v_mov_b32_e32 v48, v2
	v_mov_b32_e32 v49, v2
	v_mov_b32_e32 v54, v2
	v_mov_b32_e32 v55, v2
	v_mov_b32_e32 v56, v2
	v_mov_b32_e32 v57, v2
	v_mov_b32_e32 v62, v2
	v_mov_b32_e32 v63, v2
	v_mov_b32_e32 v64, v2
	v_mov_b32_e32 v65, v2
	v_mov_b32_e32 v66, v2
	v_mov_b32_e32 v67, v2
	v_mov_b32_e32 v68, v2
	v_mov_b32_e32 v69, v2
	v_mov_b32_e32 v74, v2
	v_mov_b32_e32 v75, v2
	v_mov_b32_e32 v76, v2
	v_mov_b32_e32 v77, v2
	v_mov_b32_e32 v82, v2
	v_mov_b32_e32 v83, v2
	v_mov_b32_e32 v84, v2
	v_mov_b32_e32 v85, v2
	v_mov_b32_e32 v90, v2
	v_mov_b32_e32 v91, v2
	v_mov_b32_e32 v92, v2
	v_mov_b32_e32 v93, v2
	v_mov_b32_e32 v98, v2
	v_mov_b32_e32 v99, v2
	v_mov_b32_e32 v100, v2
	v_mov_b32_e32 v101, v2
	v_mov_b32_e32 v106, v2
	v_mov_b32_e32 v107, v2
	v_mov_b32_e32 v108, v2
	v_mov_b32_e32 v109, v2
	v_mov_b32_e32 v114, v2
	v_mov_b32_e32 v115, v2
	v_mov_b32_e32 v116, v2
	v_mov_b32_e32 v117, v2
	v_mov_b32_e32 v122, v2
	v_mov_b32_e32 v123, v2
	v_mov_b32_e32 v124, v2
	v_mov_b32_e32 v125, v2
	v_mov_b32_e32 v70, v2
	v_mov_b32_e32 v71, v2
	v_mov_b32_e32 v72, v2
	v_mov_b32_e32 v73, v2
	v_mov_b32_e32 v78, v2
	v_mov_b32_e32 v79, v2
	v_mov_b32_e32 v80, v2
	v_mov_b32_e32 v81, v2
	v_mov_b32_e32 v86, v2
	v_mov_b32_e32 v87, v2
	v_mov_b32_e32 v88, v2
	v_mov_b32_e32 v89, v2
	v_mov_b32_e32 v94, v2
	v_mov_b32_e32 v95, v2
	v_mov_b32_e32 v96, v2
	v_mov_b32_e32 v97, v2
	v_mov_b32_e32 v102, v2
	v_mov_b32_e32 v103, v2
	v_mov_b32_e32 v104, v2
	v_mov_b32_e32 v105, v2
	v_mov_b32_e32 v110, v2
	v_mov_b32_e32 v111, v2
	v_mov_b32_e32 v112, v2
	v_mov_b32_e32 v113, v2
	v_mov_b32_e32 v118, v2
	v_mov_b32_e32 v119, v2
	v_mov_b32_e32 v120, v2
	v_mov_b32_e32 v121, v2
	v_mov_b32_e32 v126, v2
	v_mov_b32_e32 v127, v2
	v_mov_b32_e32 v128, v2
	v_mov_b32_e32 v129, v2
	s_cmp_eq_u32 s54, 1
	s_cbranch_scc1 .LBB0_1104
	s_add_u32 s14, s4, 0xfff80080
	s_addc_u32 s15, s5, -1
	s_add_i32 s59, 0, 0x10000
	s_cmp_eq_u32 s58, 28
	s_cselect_b32 s47, s17, s15
	s_cselect_b32 s46, s19, s14
	v_add_u32_e32 v140, s59, v143
	s_cselect_b32 s45, s21, s57
	s_cselect_b32 s44, s20, s56
	s_add_i32 s60, 0, 0x14000
	ds_read_b128 v[146:149], v140
	ds_read_b128 v[150:153], v140 offset:1024
	ds_read_b128 v[154:157], v140 offset:2048
	ds_read_b128 v[158:161], v140 offset:3072
	v_add_u32_e32 v140, s60, v143
	ds_read_b128 v[162:165], v140
	ds_read_b128 v[166:169], v140 offset:1024
	ds_read_b128 v[170:173], v140 offset:2048
	ds_read_b128 v[174:177], v140 offset:3072
	v_lshl_add_u64 v[140:141], s[4:5], 0, v[136:137]
	s_add_i32 m0, s41, 0xc000
	ds_read_b128 v[178:181], v145
	ds_read_b128 v[182:185], v145 offset:1024
	ds_read_b128 v[200:203], v145 offset:2048
	ds_read_b128 v[204:207], v145 offset:3072
	ds_read_b128 v[208:211], v145 offset:4096
	ds_read_b128 v[212:215], v145 offset:5120
	ds_read_b128 v[216:219], v145 offset:6144
	ds_read_b128 v[220:223], v145 offset:7168
	global_load_lds_dwordx4 v[140:141], off
	v_lshl_add_u64 v[140:141], s[4:5], 0, v[138:139]
	s_add_i32 m0, s41, 0xe000
	s_nop 0
	global_load_lds_dwordx4 v[140:141], off
	s_waitcnt vmcnt(16)
	s_waitcnt lgkmcnt(0)
	s_barrier
; #define PG8_STAGE(bufoff, gbase, voff) do { _Pragma("unroll") for (int _i = 0; _i < 2; ++_i) \
;         __builtin_amdgcn_global_load_lds((const unsigned*)((const char*)(gbase) + (voff)[_i]), (LAS unsigned*)(lds + (bufoff) + ldsw + _i * 8192), 16, 0, 0); } while (0)
; #define PG8_LDA(dst, b, h) do { _Pragma("unroll") for (int m = 0; m < 4; ++m) _Pragma("unroll") for (int k = 0; k < 2; ++k) dst[m][k] = *(const LAS bf16x8*)(lds + PG8_SA(b, h) + aoff + m * 2048 + k * 1024); } while (0)
; #define PG8_MMA(ai, bj, At, Bt) do { __builtin_amdgcn_s_setprio(1); _Pragma("unroll") for (int m = 0; m < 4; ++m) _Pragma("unroll") for (int n = 0; n < 2; ++n) _Pragma("unroll") for (int k = 0; k < 2; ++k) \
;         acc[ai][bj][m][n] = __builtin_amdgcn_mfma_f32_16x16x32_bf16(Bt[n][k], At[m][k], acc[ai][bj][m][n], 0, 0, 0); __builtin_amdgcn_s_setprio(0); } while (0)
; #define PG8_WAIT_V(n) asm volatile("s_waitcnt vmcnt(" #n ")" ::: "memory")
; #define PG8_WAIT_L(n) asm volatile("s_waitcnt lgkmcnt(" #n ")" ::: "memory")
; #define PG8_BAR __builtin_amdgcn_s_barrier()
; #define PG8_SCHED __builtin_amdgcn_sched_barrier(0)
; template <class Epi, class Sched>
; __device__ __forceinline__ void gemm_phase(LAS unsigned char* lds, const Gemm g, const Sched& S, const Epi& E, const int tid, unsigned* last_sig = nullptr) {
;     ...
;             PG8_WAIT_V(8); PG8_WAIT_L(0); PG8_BAR; PG8_MMA(0, 0, At, B0); PG8_MMA(0, 1, At, B1); PG8_BAR; PG8_SCHED;
;             PG8_LDA(At, 0, 1); PG8_STAGE(PG8_SB(0, 0), b2, voffB); PG8_STAGE(PG8_SB(0, 1), b2 + hstep, voffB); PG8_STAGE(PG8_SA(0, 0), a2, voffA);
;             PG8_WAIT_V(8); PG8_WAIT_L(0); PG8_BAR; PG8_MMA(1, 0, At, B0); PG8_MMA(1, 1, At, B1); PG8_BAR; PG8_SCHED;
	s_setprio 1
	s_waitcnt lgkmcnt(0)
	v_mfma_f32_16x16x32_bf16 v[126:129], v[146:149], v[178:181], v[126:129]
	v_mfma_f32_16x16x32_bf16 v[118:121], v[154:157], v[178:181], v[118:121]
	v_mfma_f32_16x16x32_bf16 v[110:113], v[146:149], v[200:203], v[110:113]
	v_mfma_f32_16x16x32_bf16 v[102:105], v[154:157], v[200:203], v[102:105]
	v_mfma_f32_16x16x32_bf16 v[94:97], v[146:149], v[208:211], v[94:97]
	v_mfma_f32_16x16x32_bf16 v[86:89], v[154:157], v[208:211], v[86:89]
	v_mfma_f32_16x16x32_bf16 v[78:81], v[146:149], v[216:219], v[78:81]
	v_mfma_f32_16x16x32_bf16 v[70:73], v[154:157], v[216:219], v[70:73]
	v_mfma_f32_16x16x32_bf16 v[126:129], v[150:153], v[182:185], v[126:129]
	v_mfma_f32_16x16x32_bf16 v[118:121], v[158:161], v[182:185], v[118:121]
	v_mfma_f32_16x16x32_bf16 v[110:113], v[150:153], v[204:207], v[110:113]
	v_mfma_f32_16x16x32_bf16 v[102:105], v[158:161], v[204:207], v[102:105]
	v_mfma_f32_16x16x32_bf16 v[94:97], v[150:153], v[212:215], v[94:97]
	v_mfma_f32_16x16x32_bf16 v[86:89], v[158:161], v[212:215], v[86:89]
	v_mfma_f32_16x16x32_bf16 v[78:81], v[150:153], v[220:223], v[78:81]
	v_mfma_f32_16x16x32_bf16 v[70:73], v[158:161], v[220:223], v[70:73]
	s_setprio 0
	s_setprio 1
	v_mfma_f32_16x16x32_bf16 v[122:125], v[162:165], v[178:181], v[122:125]
	v_mfma_f32_16x16x32_bf16 v[114:117], v[170:173], v[178:181], v[114:117]
	v_mfma_f32_16x16x32_bf16 v[106:109], v[162:165], v[200:203], v[106:109]
	v_mfma_f32_16x16x32_bf16 v[98:101], v[170:173], v[200:203], v[98:101]
	v_mfma_f32_16x16x32_bf16 v[90:93], v[162:165], v[208:211], v[90:93]
	v_mfma_f32_16x16x32_bf16 v[82:85], v[170:173], v[208:211], v[82:85]
	v_mfma_f32_16x16x32_bf16 v[74:77], v[162:165], v[216:219], v[74:77]
	v_mfma_f32_16x16x32_bf16 v[66:69], v[170:173], v[216:219], v[66:69]
	v_mfma_f32_16x16x32_bf16 v[122:125], v[166:169], v[182:185], v[122:125]
	v_mfma_f32_16x16x32_bf16 v[114:117], v[174:177], v[182:185], v[114:117]
	v_mfma_f32_16x16x32_bf16 v[106:109], v[166:169], v[204:207], v[106:109]
	v_mfma_f32_16x16x32_bf16 v[98:101], v[174:177], v[204:207], v[98:101]
	v_mfma_f32_16x16x32_bf16 v[90:93], v[166:169], v[212:215], v[90:93]
	v_mfma_f32_16x16x32_bf16 v[82:85], v[174:177], v[212:215], v[82:85]
	v_mfma_f32_16x16x32_bf16 v[74:77], v[166:169], v[220:223], v[74:77]
	v_mfma_f32_16x16x32_bf16 v[66:69], v[174:177], v[220:223], v[66:69]
	s_setprio 0
	s_barrier
	s_add_i32 s14, s59, s31
	v_lshl_add_u64 v[140:141], s[44:45], 0, v[186:187]
	s_mov_b32 m0, s14
	ds_read_b128 v[178:181], v145 offset:16384
	ds_read_b128 v[182:185], v145 offset:17408
	ds_read_b128 v[200:203], v145 offset:18432
	ds_read_b128 v[204:207], v145 offset:19456
	ds_read_b128 v[208:211], v145 offset:20480
	ds_read_b128 v[212:215], v145 offset:21504
	ds_read_b128 v[216:219], v145 offset:22528
	ds_read_b128 v[220:223], v145 offset:23552
	global_load_lds_dwordx4 v[140:141], off
	s_add_i32 m0, s14, 0x2000
	s_add_u32 s14, s44, 0x80000
	v_lshl_add_u64 v[232:233], s[44:45], 0, v[132:133]
	s_addc_u32 s15, s45, 0
	s_add_i32 s59, s60, s31
	global_load_lds_dwordx4 v[232:233], off
	v_lshl_add_u64 v[234:235], s[14:15], 0, v[186:187]
	s_mov_b32 m0, s59
	v_lshl_add_u64 v[236:237], s[46:47], 0, v[134:135]
	global_load_lds_dwordx4 v[234:235], off
	v_lshl_add_u64 v[234:235], s[14:15], 0, v[132:133]
	s_add_i32 m0, s59, 0x2000
	s_nop 0
	global_load_lds_dwordx4 v[234:235], off
	v_lshl_add_u64 v[234:235], s[46:47], 0, v[130:131]
	s_mov_b32 m0, s41
	s_nop 0
	global_load_lds_dwordx4 v[234:235], off
	s_mov_b32 m0, s43
	s_nop 0
	global_load_lds_dwordx4 v[236:237], off
	s_waitcnt vmcnt(16)
	s_waitcnt lgkmcnt(0)
	s_barrier
	s_setprio 1
	s_waitcnt lgkmcnt(0)
	v_mfma_f32_16x16x32_bf16 v[62:65], v[146:149], v[178:181], v[62:65]
	v_mfma_f32_16x16x32_bf16 v[54:57], v[154:157], v[178:181], v[54:57]
	v_mfma_f32_16x16x32_bf16 v[46:49], v[146:149], v[200:203], v[46:49]
	v_mfma_f32_16x16x32_bf16 v[38:41], v[154:157], v[200:203], v[38:41]
	v_mfma_f32_16x16x32_bf16 v[30:33], v[146:149], v[208:211], v[30:33]
	v_mfma_f32_16x16x32_bf16 v[22:25], v[154:157], v[208:211], v[22:25]
	v_mfma_f32_16x16x32_bf16 v[14:17], v[146:149], v[216:219], v[14:17]
	v_mfma_f32_16x16x32_bf16 v[6:9], v[154:157], v[216:219], v[6:9]
	v_mfma_f32_16x16x32_bf16 v[62:65], v[150:153], v[182:185], v[62:65]
	v_mfma_f32_16x16x32_bf16 v[54:57], v[158:161], v[182:185], v[54:57]
	v_mfma_f32_16x16x32_bf16 v[46:49], v[150:153], v[204:207], v[46:49]
	v_mfma_f32_16x16x32_bf16 v[38:41], v[158:161], v[204:207], v[38:41]
	v_mfma_f32_16x16x32_bf16 v[30:33], v[150:153], v[212:215], v[30:33]
	v_mfma_f32_16x16x32_bf16 v[22:25], v[158:161], v[212:215], v[22:25]
	v_mfma_f32_16x16x32_bf16 v[14:17], v[150:153], v[220:223], v[14:17]
	v_mfma_f32_16x16x32_bf16 v[6:9], v[158:161], v[220:223], v[6:9]
	s_setprio 0
	s_setprio 1
	v_mfma_f32_16x16x32_bf16 v[58:61], v[162:165], v[178:181], v[58:61]
	v_mfma_f32_16x16x32_bf16 v[50:53], v[170:173], v[178:181], v[50:53]
	v_mfma_f32_16x16x32_bf16 v[42:45], v[162:165], v[200:203], v[42:45]
	v_mfma_f32_16x16x32_bf16 v[34:37], v[170:173], v[200:203], v[34:37]
	v_mfma_f32_16x16x32_bf16 v[26:29], v[162:165], v[208:211], v[26:29]
	v_mfma_f32_16x16x32_bf16 v[18:21], v[170:173], v[208:211], v[18:21]
	v_mfma_f32_16x16x32_bf16 v[10:13], v[162:165], v[216:219], v[10:13]
	v_mfma_f32_16x16x32_bf16 v[2:5], v[170:173], v[216:219], v[2:5]
	v_mfma_f32_16x16x32_bf16 v[58:61], v[166:169], v[182:185], v[58:61]
	v_mfma_f32_16x16x32_bf16 v[50:53], v[174:177], v[182:185], v[50:53]
	v_mfma_f32_16x16x32_bf16 v[42:45], v[166:169], v[204:207], v[42:45]
	v_mfma_f32_16x16x32_bf16 v[34:37], v[174:177], v[204:207], v[34:37]
	v_mfma_f32_16x16x32_bf16 v[26:29], v[166:169], v[212:215], v[26:29]
	v_mfma_f32_16x16x32_bf16 v[18:21], v[174:177], v[212:215], v[18:21]
	v_mfma_f32_16x16x32_bf16 v[10:13], v[166:169], v[220:223], v[10:13]
	v_mfma_f32_16x16x32_bf16 v[2:5], v[174:177], v[220:223], v[2:5]
	s_setprio 0
	s_barrier
; #define PG8_STAGE(bufoff, gbase, voff) do { _Pragma("unroll") for (int _i = 0; _i < 2; ++_i) \
;         __builtin_amdgcn_global_load_lds((const unsigned*)((const char*)(gbase) + (voff)[_i]), (LAS unsigned*)(lds + (bufoff) + ldsw + _i * 8192), 16, 0, 0); } while (0)
; #define PG8_LDA(dst, b, h) do { _Pragma("unroll") for (int m = 0; m < 4; ++m) _Pragma("unroll") for (int k = 0; k < 2; ++k) dst[m][k] = *(const LAS bf16x8*)(lds + PG8_SA(b, h) + aoff + m * 2048 + k * 1024); } while (0)
; #define PG8_LDB(dst, b, h) do { _Pragma("unroll") for (int n = 0; n < 2; ++n) _Pragma("unroll") for (int k = 0; k < 2; ++k) dst[n][k] = *(const LAS bf16x8*)(lds + PG8_SB(b, h) + boff + n * 2048 + k * 1024); } while (0)
; #define PG8_MMA(ai, bj, At, Bt) do { __builtin_amdgcn_s_setprio(1); _Pragma("unroll") for (int m = 0; m < 4; ++m) _Pragma("unroll") for (int n = 0; n < 2; ++n) _Pragma("unroll") for (int k = 0; k < 2; ++k) \
;         acc[ai][bj][m][n] = __builtin_amdgcn_mfma_f32_16x16x32_bf16(Bt[n][k], At[m][k], acc[ai][bj][m][n], 0, 0, 0); __builtin_amdgcn_s_setprio(0); } while (0)
; #define PG8_WAIT_V(n) asm volatile("s_waitcnt vmcnt(" #n ")" ::: "memory")
; #define PG8_WAIT_L(n) asm volatile("s_waitcnt lgkmcnt(" #n ")" ::: "memory")
; #define PG8_BAR __builtin_amdgcn_s_barrier()
; #define PG8_SCHED __builtin_amdgcn_sched_barrier(0)
; template <class Epi, class Sched>
; __device__ __forceinline__ void gemm_phase(LAS unsigned char* lds, const Gemm g, const Sched& S, const Epi& E, const int tid, unsigned* last_sig = nullptr) {
;     ...
;             PG8_LDB(B0, 1, 0); PG8_LDB(B1, 1, 1); PG8_SCHED; PG8_LDA(At, 1, 0); PG8_STAGE(PG8_SA(0, 1), a2 + hstep, voffA);
;             PG8_WAIT_V(8); PG8_WAIT_L(0); PG8_BAR; PG8_MMA(0, 0, At, B0); PG8_MMA(0, 1, At, B1); PG8_BAR; PG8_SCHED;
	s_add_i32 s59, 0, 0x18000
	s_add_i32 s60, 0, 0x1c000
	v_add_u32_e32 v158, s59, v143
	v_add_u32_e32 v174, s60, v143
	ds_read_b128 v[146:149], v158
	ds_read_b128 v[150:153], v158 offset:1024
	ds_read_b128 v[154:157], v158 offset:2048
	ds_read_b128 v[158:161], v158 offset:3072
	ds_read_b128 v[162:165], v174
	ds_read_b128 v[166:169], v174 offset:1024
	ds_read_b128 v[170:173], v174 offset:2048
	ds_read_b128 v[174:177], v174 offset:3072
	s_add_u32 s14, s46, 0x80000
	s_addc_u32 s15, s47, 0
	s_mov_b32 m0, s50
	v_lshl_add_u64 v[238:239], s[14:15], 0, v[130:131]
	ds_read_b128 v[178:181], v145 offset:32768
	ds_read_b128 v[182:185], v145 offset:33792
	ds_read_b128 v[200:203], v145 offset:34816
	ds_read_b128 v[204:207], v145 offset:35840
	ds_read_b128 v[208:211], v145 offset:36864
	ds_read_b128 v[212:215], v145 offset:37888
	ds_read_b128 v[216:219], v145 offset:38912
	ds_read_b128 v[220:223], v145 offset:39936
	global_load_lds_dwordx4 v[238:239], off
	v_lshl_add_u64 v[238:239], s[14:15], 0, v[134:135]
	s_mov_b32 m0, s51
	s_nop 0
	global_load_lds_dwordx4 v[238:239], off
	s_waitcnt vmcnt(8)
	s_waitcnt lgkmcnt(0)
	s_barrier
	s_setprio 1
	s_waitcnt lgkmcnt(0)
	v_mfma_f32_16x16x32_bf16 v[126:129], v[146:149], v[178:181], v[126:129]
	v_mfma_f32_16x16x32_bf16 v[118:121], v[154:157], v[178:181], v[118:121]
	v_mfma_f32_16x16x32_bf16 v[110:113], v[146:149], v[200:203], v[110:113]
	v_mfma_f32_16x16x32_bf16 v[102:105], v[154:157], v[200:203], v[102:105]
	v_mfma_f32_16x16x32_bf16 v[94:97], v[146:149], v[208:211], v[94:97]
	v_mfma_f32_16x16x32_bf16 v[86:89], v[154:157], v[208:211], v[86:89]
	v_mfma_f32_16x16x32_bf16 v[78:81], v[146:149], v[216:219], v[78:81]
	v_mfma_f32_16x16x32_bf16 v[70:73], v[154:157], v[216:219], v[70:73]
	v_mfma_f32_16x16x32_bf16 v[126:129], v[150:153], v[182:185], v[126:129]
	v_mfma_f32_16x16x32_bf16 v[118:121], v[158:161], v[182:185], v[118:121]
	v_mfma_f32_16x16x32_bf16 v[110:113], v[150:153], v[204:207], v[110:113]
	v_mfma_f32_16x16x32_bf16 v[102:105], v[158:161], v[204:207], v[102:105]
	v_mfma_f32_16x16x32_bf16 v[94:97], v[150:153], v[212:215], v[94:97]
	v_mfma_f32_16x16x32_bf16 v[86:89], v[158:161], v[212:215], v[86:89]
	v_mfma_f32_16x16x32_bf16 v[78:81], v[150:153], v[220:223], v[78:81]
	v_mfma_f32_16x16x32_bf16 v[70:73], v[158:161], v[220:223], v[70:73]
	s_setprio 0
	s_setprio 1
	v_mfma_f32_16x16x32_bf16 v[122:125], v[162:165], v[178:181], v[122:125]
	v_mfma_f32_16x16x32_bf16 v[114:117], v[170:173], v[178:181], v[114:117]
	v_mfma_f32_16x16x32_bf16 v[106:109], v[162:165], v[200:203], v[106:109]
	v_mfma_f32_16x16x32_bf16 v[98:101], v[170:173], v[200:203], v[98:101]
	v_mfma_f32_16x16x32_bf16 v[90:93], v[162:165], v[208:211], v[90:93]
	v_mfma_f32_16x16x32_bf16 v[82:85], v[170:173], v[208:211], v[82:85]
	v_mfma_f32_16x16x32_bf16 v[74:77], v[162:165], v[216:219], v[74:77]
	v_mfma_f32_16x16x32_bf16 v[66:69], v[170:173], v[216:219], v[66:69]
	v_mfma_f32_16x16x32_bf16 v[122:125], v[166:169], v[182:185], v[122:125]
	v_mfma_f32_16x16x32_bf16 v[114:117], v[174:177], v[182:185], v[114:117]
	v_mfma_f32_16x16x32_bf16 v[106:109], v[166:169], v[204:207], v[106:109]
	v_mfma_f32_16x16x32_bf16 v[98:101], v[174:177], v[204:207], v[98:101]
	v_mfma_f32_16x16x32_bf16 v[90:93], v[166:169], v[212:215], v[90:93]
	v_mfma_f32_16x16x32_bf16 v[82:85], v[174:177], v[212:215], v[82:85]
	v_mfma_f32_16x16x32_bf16 v[74:77], v[166:169], v[220:223], v[74:77]
	v_mfma_f32_16x16x32_bf16 v[66:69], v[174:177], v[220:223], v[66:69]
	s_setprio 0
	s_barrier
; #define PG8_STAGE(bufoff, gbase, voff) do { _Pragma("unroll") for (int _i = 0; _i < 2; ++_i) \
;         __builtin_amdgcn_global_load_lds((const unsigned*)((const char*)(gbase) + (voff)[_i]), (LAS unsigned*)(lds + (bufoff) + ldsw + _i * 8192), 16, 0, 0); } while (0)
; #define PG8_LDA(dst, b, h) do { _Pragma("unroll") for (int m = 0; m < 4; ++m) _Pragma("unroll") for (int k = 0; k < 2; ++k) dst[m][k] = *(const LAS bf16x8*)(lds + PG8_SA(b, h) + aoff + m * 2048 + k * 1024); } while (0)
; #define PG8_MMA(ai, bj, At, Bt) do { __builtin_amdgcn_s_setprio(1); _Pragma("unroll") for (int m = 0; m < 4; ++m) _Pragma("unroll") for (int n = 0; n < 2; ++n) _Pragma("unroll") for (int k = 0; k < 2; ++k) \
;         acc[ai][bj][m][n] = __builtin_amdgcn_mfma_f32_16x16x32_bf16(Bt[n][k], At[m][k], acc[ai][bj][m][n], 0, 0, 0); __builtin_amdgcn_s_setprio(0); } while (0)
; #define PG8_WAIT_V(n) asm volatile("s_waitcnt vmcnt(" #n ")" ::: "memory")
; #define PG8_WAIT_L(n) asm volatile("s_waitcnt lgkmcnt(" #n ")" ::: "memory")
; #define PG8_BAR __builtin_amdgcn_s_barrier()
; #define PG8_SCHED __builtin_amdgcn_sched_barrier(0)
; template <class Epi, class Sched>
; __device__ __forceinline__ void gemm_phase(LAS unsigned char* lds, const Gemm g, const Sched& S, const Epi& E, const int tid, unsigned* last_sig = nullptr) {
;     ...
;             PG8_LDA(At, 1, 1); PG8_STAGE(PG8_SB(1, 0), b3, voffB); PG8_STAGE(PG8_SB(1, 1), b3 + hstep, voffB); PG8_STAGE(PG8_SA(1, 0), a3, voffA);
;             PG8_WAIT_V(8); PG8_WAIT_L(0); PG8_BAR; PG8_MMA(1, 0, At, B0); PG8_MMA(1, 1, At, B1); PG8_BAR; PG8_SCHED;
;         }
	s_add_i32 s14, s59, s31
	v_lshl_add_u64 v[140:141], v[140:141], 0, s[34:35]
	s_mov_b32 m0, s14
	ds_read_b128 v[178:181], v145 offset:49152
	ds_read_b128 v[182:185], v145 offset:50176
	ds_read_b128 v[200:203], v145 offset:51200
	ds_read_b128 v[204:207], v145 offset:52224
	ds_read_b128 v[208:211], v145 offset:53248
	ds_read_b128 v[212:215], v145 offset:54272
	ds_read_b128 v[216:219], v145 offset:55296
	ds_read_b128 v[220:223], v145 offset:56320
	global_load_lds_dwordx4 v[140:141], off
	s_add_i32 m0, s14, 0x2000
	s_add_u32 s14, s44, 0x80080
	v_lshl_add_u64 v[140:141], v[232:233], 0, s[34:35]
	s_addc_u32 s15, s45, 0
	s_add_i32 s44, s60, s31
	global_load_lds_dwordx4 v[140:141], off
	v_lshl_add_u64 v[140:141], s[14:15], 0, v[186:187]
	s_mov_b32 m0, s44
	s_nop 0
	global_load_lds_dwordx4 v[140:141], off
	v_lshl_add_u64 v[140:141], s[14:15], 0, v[132:133]
	s_add_i32 m0, s44, 0x2000
	s_nop 0
	global_load_lds_dwordx4 v[140:141], off
	v_lshl_add_u64 v[140:141], v[234:235], 0, s[34:35]
	s_mov_b32 m0, s52
	s_nop 0
	global_load_lds_dwordx4 v[140:141], off
	v_lshl_add_u64 v[140:141], v[236:237], 0, s[34:35]
	s_mov_b32 m0, s53
	s_nop 0
	global_load_lds_dwordx4 v[140:141], off
	s_waitcnt vmcnt(8)
	s_waitcnt lgkmcnt(0)
	s_barrier
	s_setprio 1
	s_waitcnt lgkmcnt(0)
	v_mfma_f32_16x16x32_bf16 v[62:65], v[146:149], v[178:181], v[62:65]
	v_mfma_f32_16x16x32_bf16 v[54:57], v[154:157], v[178:181], v[54:57]
	v_mfma_f32_16x16x32_bf16 v[46:49], v[146:149], v[200:203], v[46:49]
	v_mfma_f32_16x16x32_bf16 v[38:41], v[154:157], v[200:203], v[38:41]
	v_mfma_f32_16x16x32_bf16 v[30:33], v[146:149], v[208:211], v[30:33]
	v_mfma_f32_16x16x32_bf16 v[22:25], v[154:157], v[208:211], v[22:25]
	v_mfma_f32_16x16x32_bf16 v[14:17], v[146:149], v[216:219], v[14:17]
	v_mfma_f32_16x16x32_bf16 v[6:9], v[154:157], v[216:219], v[6:9]
	v_mfma_f32_16x16x32_bf16 v[62:65], v[150:153], v[182:185], v[62:65]
	v_mfma_f32_16x16x32_bf16 v[54:57], v[158:161], v[182:185], v[54:57]
	v_mfma_f32_16x16x32_bf16 v[46:49], v[150:153], v[204:207], v[46:49]
	v_mfma_f32_16x16x32_bf16 v[38:41], v[158:161], v[204:207], v[38:41]
	v_mfma_f32_16x16x32_bf16 v[30:33], v[150:153], v[212:215], v[30:33]
	v_mfma_f32_16x16x32_bf16 v[22:25], v[158:161], v[212:215], v[22:25]
	v_mfma_f32_16x16x32_bf16 v[14:17], v[150:153], v[220:223], v[14:17]
	v_mfma_f32_16x16x32_bf16 v[6:9], v[158:161], v[220:223], v[6:9]
	s_setprio 0
	s_setprio 1
	v_mfma_f32_16x16x32_bf16 v[58:61], v[162:165], v[178:181], v[58:61]
	v_mfma_f32_16x16x32_bf16 v[50:53], v[170:173], v[178:181], v[50:53]
	v_mfma_f32_16x16x32_bf16 v[42:45], v[162:165], v[200:203], v[42:45]
	v_mfma_f32_16x16x32_bf16 v[34:37], v[170:173], v[200:203], v[34:37]
	v_mfma_f32_16x16x32_bf16 v[26:29], v[162:165], v[208:211], v[26:29]
	v_mfma_f32_16x16x32_bf16 v[18:21], v[170:173], v[208:211], v[18:21]
	v_mfma_f32_16x16x32_bf16 v[10:13], v[162:165], v[216:219], v[10:13]
	v_mfma_f32_16x16x32_bf16 v[2:5], v[170:173], v[216:219], v[2:5]
	v_mfma_f32_16x16x32_bf16 v[58:61], v[166:169], v[182:185], v[58:61]
	v_mfma_f32_16x16x32_bf16 v[50:53], v[174:177], v[182:185], v[50:53]
	v_mfma_f32_16x16x32_bf16 v[42:45], v[166:169], v[204:207], v[42:45]
	v_mfma_f32_16x16x32_bf16 v[34:37], v[174:177], v[204:207], v[34:37]
	v_mfma_f32_16x16x32_bf16 v[26:29], v[166:169], v[212:215], v[26:29]
	v_mfma_f32_16x16x32_bf16 v[18:21], v[174:177], v[212:215], v[18:21]
	v_mfma_f32_16x16x32_bf16 v[10:13], v[166:169], v[220:223], v[10:13]
	v_mfma_f32_16x16x32_bf16 v[2:5], v[174:177], v[220:223], v[2:5]
	s_setprio 0
	s_barrier
	s_add_i32 s58, s58, 2
	s_add_u32 s4, s4, 0x100
	s_addc_u32 s5, s5, 0
	s_add_u32 s56, s56, 0x100
	s_addc_u32 s57, s57, 0
	s_cmp_gt_u32 s58, 29
	s_cbranch_scc1 .Lkpeel_exit_4

; #define PG8_BAR __builtin_amdgcn_s_barrier()
; template <class Epi, class Sched>
; __device__ __forceinline__ void gemm_phase(LAS unsigned char* lds, const Gemm g, const Sched& S, const Epi& E, const int tid, unsigned* last_sig = nullptr) {
;     ...
;         if (wr == 0) PG8_BAR;
.Lkpeel_exit_4:
	s_and_b64 vcc, exec, s[12:13]
	s_cbranch_vccz .LBB0_1107
	s_barrier

; #define PG8_STAGE(bufoff, gbase, voff) do { _Pragma("unroll") for (int _i = 0; _i < 2; ++_i) \
;         __builtin_amdgcn_global_load_lds((const unsigned*)((const char*)(gbase) + (voff)[_i]), (LAS unsigned*)(lds + (bufoff) + ldsw + _i * 8192), 16, 0, 0); } while (0)
; #define PG8_LDA(dst, b, h) do { _Pragma("unroll") for (int m = 0; m < 4; ++m) _Pragma("unroll") for (int k = 0; k < 2; ++k) dst[m][k] = *(const LAS bf16x8*)(lds + PG8_SA(b, h) + aoff + m * 2048 + k * 1024); } while (0)
; #define PG8_LDB(dst, b, h) do { _Pragma("unroll") for (int n = 0; n < 2; ++n) _Pragma("unroll") for (int k = 0; k < 2; ++k) dst[n][k] = *(const LAS bf16x8*)(lds + PG8_SB(b, h) + boff + n * 2048 + k * 1024); } while (0)
; #define PG8_MMA(ai, bj, At, Bt) do { __builtin_amdgcn_s_setprio(1); _Pragma("unroll") for (int m = 0; m < 4; ++m) _Pragma("unroll") for (int n = 0; n < 2; ++n) _Pragma("unroll") for (int k = 0; k < 2; ++k) \
;         acc[ai][bj][m][n] = __builtin_amdgcn_mfma_f32_16x16x32_bf16(Bt[n][k], At[m][k], acc[ai][bj][m][n], 0, 0, 0); __builtin_amdgcn_s_setprio(0); } while (0)
; #define PG8_WAIT_V(n) asm volatile("s_waitcnt vmcnt(" #n ")" ::: "memory")
; #define PG8_WAIT_L(n) asm volatile("s_waitcnt lgkmcnt(" #n ")" ::: "memory")
; template <class Epi, class Sched>
; __device__ __forceinline__ void gemm_phase(LAS unsigned char* lds, const Gemm g, const Sched& S, const Epi& E, const int tid, unsigned* last_sig = nullptr) {
;     ...
;         for (int t = 0; t < nt; t += 2) {
;             const bool last = (t == nt - 2);
;             const char* a1 = cA + (size_t)(t + 1) * kstep;
;             const char* a2 = last ? nA : cA + (size_t)(t + 2) * kstep; const char* b2 = last ? nB : cB + (size_t)(t + 2) * kstep;
;             const char* a3 = a2 + kstep; const char* b3 = b2 + kstep;
;             PG8_LDB(B0, 0, 0); PG8_LDB(B1, 0, 1); PG8_SCHED; PG8_LDA(At, 0, 0); PG8_STAGE(PG8_SA(1, 1), a1 + hstep, voffA);
;             PG8_WAIT_V(8); PG8_WAIT_L(0); PG8_BAR; PG8_MMA(0, 0, At, B0); PG8_MMA(0, 1, At, B1); PG8_BAR; PG8_SCHED;
;     ...
; #pragma unroll
;         for (int a = 0; a < 2; ++a)
; #pragma unroll
;             for (int b = 0; b < 2; ++b)
; #pragma unroll
;                 for (int m = 0; m < 4; ++m)
; #pragma unroll
;                     for (int n = 0; n < 2; ++n) acc[a][b][m][n] = (f32x4){0.f, 0.f, 0.f, 0.f};
;         cur = nxt; cA = nA; cB = nB; ++ui;
.LBB0_1187:
	s_ashr_i32 s13, s12, 31
	s_lshl_b64 s[14:15], s[12:13], 20
	v_readlane_b32 s16, v253, 46
	v_readlane_b32 s17, v253, 47
	s_add_u32 s16, s16, s14
	s_addc_u32 s17, s17, s15
	s_and_b64 s[14:15], s[0:1], exec
	s_cselect_b32 s13, s17, s21
	s_cselect_b32 s50, s16, s20
	s_ashr_i32 s11, s10, 31
	s_lshl_b64 s[14:15], s[10:11], 20
	v_readlane_b32 s11, v253, 15
	s_add_u32 s18, s11, s14
	v_readlane_b32 s11, v253, 16
	s_addc_u32 s19, s11, s15
	s_and_b64 s[14:15], s[0:1], exec
	s_cselect_b32 s11, s19, s23
	s_cselect_b32 s51, s18, s22
	s_add_u32 s20, s20, 0x80080
	s_addc_u32 s21, s21, 0
	s_add_u32 s52, s22, 0x100
	v_mov_b32_e32 v2, 0
	s_addc_u32 s53, s23, 0
	s_mov_b32 s54, -2
	v_mov_b32_e32 v3, v2
	v_mov_b32_e32 v4, v2
	v_mov_b32_e32 v5, v2
	v_mov_b32_e32 v10, v2
	v_mov_b32_e32 v11, v2
	v_mov_b32_e32 v12, v2
	v_mov_b32_e32 v13, v2
	v_mov_b32_e32 v18, v2
	v_mov_b32_e32 v19, v2
	v_mov_b32_e32 v20, v2
	v_mov_b32_e32 v21, v2
	v_mov_b32_e32 v26, v2
	v_mov_b32_e32 v27, v2
	v_mov_b32_e32 v28, v2
	v_mov_b32_e32 v29, v2
	v_mov_b32_e32 v34, v2
	v_mov_b32_e32 v35, v2
	v_mov_b32_e32 v36, v2
	v_mov_b32_e32 v37, v2
	v_mov_b32_e32 v42, v2
	v_mov_b32_e32 v43, v2
	v_mov_b32_e32 v44, v2
	v_mov_b32_e32 v45, v2
	v_mov_b32_e32 v50, v2
	v_mov_b32_e32 v51, v2
	v_mov_b32_e32 v52, v2
	v_mov_b32_e32 v53, v2
	v_mov_b32_e32 v58, v2
	v_mov_b32_e32 v59, v2
	v_mov_b32_e32 v60, v2
	v_mov_b32_e32 v61, v2
	v_mov_b32_e32 v6, v2
	v_mov_b32_e32 v7, v2
	v_mov_b32_e32 v8, v2
	v_mov_b32_e32 v9, v2
	v_mov_b32_e32 v14, v2
	v_mov_b32_e32 v15, v2
	v_mov_b32_e32 v16, v2
	v_mov_b32_e32 v17, v2
	v_mov_b32_e32 v22, v2
	v_mov_b32_e32 v23, v2
	v_mov_b32_e32 v24, v2
	v_mov_b32_e32 v25, v2
	v_mov_b32_e32 v30, v2
	v_mov_b32_e32 v31, v2
	v_mov_b32_e32 v32, v2
	v_mov_b32_e32 v33, v2
	v_mov_b32_e32 v38, v2
	v_mov_b32_e32 v39, v2
	v_mov_b32_e32 v40, v2
	v_mov_b32_e32 v41, v2
	v_mov_b32_e32 v46, v2
	v_mov_b32_e32 v47, v2
	v_mov_b32_e32 v48, v2
	v_mov_b32_e32 v49, v2
	v_mov_b32_e32 v54, v2
	v_mov_b32_e32 v55, v2
	v_mov_b32_e32 v56, v2
	v_mov_b32_e32 v57, v2
	v_mov_b32_e32 v62, v2
	v_mov_b32_e32 v63, v2
	v_mov_b32_e32 v64, v2
	v_mov_b32_e32 v65, v2
	v_mov_b32_e32 v66, v2
	v_mov_b32_e32 v67, v2
	v_mov_b32_e32 v68, v2
	v_mov_b32_e32 v69, v2
	v_mov_b32_e32 v74, v2
	v_mov_b32_e32 v75, v2
	v_mov_b32_e32 v76, v2
	v_mov_b32_e32 v77, v2
	v_mov_b32_e32 v82, v2
	v_mov_b32_e32 v83, v2
	v_mov_b32_e32 v84, v2
	v_mov_b32_e32 v85, v2
	v_mov_b32_e32 v90, v2
	v_mov_b32_e32 v91, v2
	v_mov_b32_e32 v92, v2
	v_mov_b32_e32 v93, v2
	v_mov_b32_e32 v98, v2
	v_mov_b32_e32 v99, v2
	v_mov_b32_e32 v100, v2
	v_mov_b32_e32 v101, v2
	v_mov_b32_e32 v106, v2
	v_mov_b32_e32 v107, v2
	v_mov_b32_e32 v108, v2
	v_mov_b32_e32 v109, v2
	v_mov_b32_e32 v114, v2
	v_mov_b32_e32 v115, v2
	v_mov_b32_e32 v116, v2
	v_mov_b32_e32 v117, v2
	v_mov_b32_e32 v122, v2
	v_mov_b32_e32 v123, v2
	v_mov_b32_e32 v124, v2
	v_mov_b32_e32 v125, v2
	v_mov_b32_e32 v70, v2
	v_mov_b32_e32 v71, v2
	v_mov_b32_e32 v72, v2
	v_mov_b32_e32 v73, v2
	v_mov_b32_e32 v78, v2
	v_mov_b32_e32 v79, v2
	v_mov_b32_e32 v80, v2
	v_mov_b32_e32 v81, v2
	v_mov_b32_e32 v86, v2
	v_mov_b32_e32 v87, v2
	v_mov_b32_e32 v88, v2
	v_mov_b32_e32 v89, v2
	v_mov_b32_e32 v94, v2
	v_mov_b32_e32 v95, v2
	v_mov_b32_e32 v96, v2
	v_mov_b32_e32 v97, v2
	v_mov_b32_e32 v102, v2
	v_mov_b32_e32 v103, v2
	v_mov_b32_e32 v104, v2
	v_mov_b32_e32 v105, v2
	v_mov_b32_e32 v110, v2
	v_mov_b32_e32 v111, v2
	v_mov_b32_e32 v112, v2
	v_mov_b32_e32 v113, v2
	v_mov_b32_e32 v118, v2
	v_mov_b32_e32 v119, v2
	v_mov_b32_e32 v120, v2
	v_mov_b32_e32 v121, v2
	v_mov_b32_e32 v126, v2
	v_mov_b32_e32 v127, v2
	v_mov_b32_e32 v128, v2
	v_mov_b32_e32 v129, v2
	s_cmp_eq_u32 s47, 1
	s_cbranch_scc1 .LBB0_1188
	s_add_u32 s14, s20, 0xfff80080
	s_addc_u32 s15, s21, -1
	s_add_i32 s55, 0, 0x10000
	s_cmp_eq_u32 s54, 28
	s_cselect_b32 s41, s13, s15
	s_cselect_b32 s40, s50, s14
	v_add_u32_e32 v140, s55, v1
	s_cselect_b32 s23, s11, s53
	s_cselect_b32 s22, s51, s52
	s_add_i32 s56, 0, 0x14000
	ds_read_b128 v[146:149], v140
	ds_read_b128 v[150:153], v140 offset:1024
	ds_read_b128 v[154:157], v140 offset:2048
	ds_read_b128 v[158:161], v140 offset:3072
	v_add_u32_e32 v140, s56, v1
	ds_read_b128 v[162:165], v140
	ds_read_b128 v[166:169], v140 offset:1024
	ds_read_b128 v[170:173], v140 offset:2048
	ds_read_b128 v[174:177], v140 offset:3072
	v_lshl_add_u64 v[140:141], s[20:21], 0, v[136:137]
	s_add_i32 m0, s31, 0xc000
	ds_read_b128 v[178:181], v144
	ds_read_b128 v[182:185], v144 offset:1024
	ds_read_b128 v[200:203], v144 offset:2048
	ds_read_b128 v[204:207], v144 offset:3072
	ds_read_b128 v[208:211], v144 offset:4096
	ds_read_b128 v[212:215], v144 offset:5120
	ds_read_b128 v[216:219], v144 offset:6144
	ds_read_b128 v[220:223], v144 offset:7168
	global_load_lds_dwordx4 v[140:141], off
	v_lshl_add_u64 v[140:141], s[20:21], 0, v[138:139]
	s_add_i32 m0, s31, 0xe000
	s_nop 0
	global_load_lds_dwordx4 v[140:141], off
	s_waitcnt vmcnt(16)
	s_waitcnt lgkmcnt(0)
	s_barrier
; #define PG8_STAGE(bufoff, gbase, voff) do { _Pragma("unroll") for (int _i = 0; _i < 2; ++_i) \
;         __builtin_amdgcn_global_load_lds((const unsigned*)((const char*)(gbase) + (voff)[_i]), (LAS unsigned*)(lds + (bufoff) + ldsw + _i * 8192), 16, 0, 0); } while (0)
; #define PG8_LDA(dst, b, h) do { _Pragma("unroll") for (int m = 0; m < 4; ++m) _Pragma("unroll") for (int k = 0; k < 2; ++k) dst[m][k] = *(const LAS bf16x8*)(lds + PG8_SA(b, h) + aoff + m * 2048 + k * 1024); } while (0)
; #define PG8_MMA(ai, bj, At, Bt) do { __builtin_amdgcn_s_setprio(1); _Pragma("unroll") for (int m = 0; m < 4; ++m) _Pragma("unroll") for (int n = 0; n < 2; ++n) _Pragma("unroll") for (int k = 0; k < 2; ++k) \
;         acc[ai][bj][m][n] = __builtin_amdgcn_mfma_f32_16x16x32_bf16(Bt[n][k], At[m][k], acc[ai][bj][m][n], 0, 0, 0); __builtin_amdgcn_s_setprio(0); } while (0)
; #define PG8_WAIT_V(n) asm volatile("s_waitcnt vmcnt(" #n ")" ::: "memory")
; #define PG8_WAIT_L(n) asm volatile("s_waitcnt lgkmcnt(" #n ")" ::: "memory")
; #define PG8_BAR __builtin_amdgcn_s_barrier()
; #define PG8_SCHED __builtin_amdgcn_sched_barrier(0)
; template <class Epi, class Sched>
; __device__ __forceinline__ void gemm_phase(LAS unsigned char* lds, const Gemm g, const Sched& S, const Epi& E, const int tid, unsigned* last_sig = nullptr) {
;     ...
;             PG8_WAIT_V(8); PG8_WAIT_L(0); PG8_BAR; PG8_MMA(0, 0, At, B0); PG8_MMA(0, 1, At, B1); PG8_BAR; PG8_SCHED;
;             PG8_LDA(At, 0, 1); PG8_STAGE(PG8_SB(0, 0), b2, voffB); PG8_STAGE(PG8_SB(0, 1), b2 + hstep, voffB); PG8_STAGE(PG8_SA(0, 0), a2, voffA);
;             PG8_WAIT_V(8); PG8_WAIT_L(0); PG8_BAR; PG8_MMA(1, 0, At, B0); PG8_MMA(1, 1, At, B1); PG8_BAR; PG8_SCHED;
	s_setprio 1
	s_waitcnt lgkmcnt(0)
	v_mfma_f32_16x16x32_bf16 v[126:129], v[146:149], v[178:181], v[126:129]
	v_mfma_f32_16x16x32_bf16 v[118:121], v[154:157], v[178:181], v[118:121]
	v_mfma_f32_16x16x32_bf16 v[110:113], v[146:149], v[200:203], v[110:113]
	v_mfma_f32_16x16x32_bf16 v[102:105], v[154:157], v[200:203], v[102:105]
	v_mfma_f32_16x16x32_bf16 v[94:97], v[146:149], v[208:211], v[94:97]
	v_mfma_f32_16x16x32_bf16 v[86:89], v[154:157], v[208:211], v[86:89]
	v_mfma_f32_16x16x32_bf16 v[78:81], v[146:149], v[216:219], v[78:81]
	v_mfma_f32_16x16x32_bf16 v[70:73], v[154:157], v[216:219], v[70:73]
	v_mfma_f32_16x16x32_bf16 v[126:129], v[150:153], v[182:185], v[126:129]
	v_mfma_f32_16x16x32_bf16 v[118:121], v[158:161], v[182:185], v[118:121]
	v_mfma_f32_16x16x32_bf16 v[110:113], v[150:153], v[204:207], v[110:113]
	v_mfma_f32_16x16x32_bf16 v[102:105], v[158:161], v[204:207], v[102:105]
	v_mfma_f32_16x16x32_bf16 v[94:97], v[150:153], v[212:215], v[94:97]
	v_mfma_f32_16x16x32_bf16 v[86:89], v[158:161], v[212:215], v[86:89]
	v_mfma_f32_16x16x32_bf16 v[78:81], v[150:153], v[220:223], v[78:81]
	v_mfma_f32_16x16x32_bf16 v[70:73], v[158:161], v[220:223], v[70:73]
	s_setprio 0
	s_setprio 1
	v_mfma_f32_16x16x32_bf16 v[122:125], v[162:165], v[178:181], v[122:125]
	v_mfma_f32_16x16x32_bf16 v[114:117], v[170:173], v[178:181], v[114:117]
	v_mfma_f32_16x16x32_bf16 v[106:109], v[162:165], v[200:203], v[106:109]
	v_mfma_f32_16x16x32_bf16 v[98:101], v[170:173], v[200:203], v[98:101]
	v_mfma_f32_16x16x32_bf16 v[90:93], v[162:165], v[208:211], v[90:93]
	v_mfma_f32_16x16x32_bf16 v[82:85], v[170:173], v[208:211], v[82:85]
	v_mfma_f32_16x16x32_bf16 v[74:77], v[162:165], v[216:219], v[74:77]
	v_mfma_f32_16x16x32_bf16 v[66:69], v[170:173], v[216:219], v[66:69]
	v_mfma_f32_16x16x32_bf16 v[122:125], v[166:169], v[182:185], v[122:125]
	v_mfma_f32_16x16x32_bf16 v[114:117], v[174:177], v[182:185], v[114:117]
	v_mfma_f32_16x16x32_bf16 v[106:109], v[166:169], v[204:207], v[106:109]
	v_mfma_f32_16x16x32_bf16 v[98:101], v[174:177], v[204:207], v[98:101]
	v_mfma_f32_16x16x32_bf16 v[90:93], v[166:169], v[212:215], v[90:93]
	v_mfma_f32_16x16x32_bf16 v[82:85], v[174:177], v[212:215], v[82:85]
	v_mfma_f32_16x16x32_bf16 v[74:77], v[166:169], v[220:223], v[74:77]
	v_mfma_f32_16x16x32_bf16 v[66:69], v[174:177], v[220:223], v[66:69]
	s_setprio 0
	s_barrier
	s_add_i32 s14, s55, s28
	v_lshl_add_u64 v[140:141], s[22:23], 0, v[186:187]
	s_mov_b32 m0, s14
	ds_read_b128 v[178:181], v144 offset:16384
	ds_read_b128 v[182:185], v144 offset:17408
	ds_read_b128 v[200:203], v144 offset:18432
	ds_read_b128 v[204:207], v144 offset:19456
	ds_read_b128 v[208:211], v144 offset:20480
	ds_read_b128 v[212:215], v144 offset:21504
	ds_read_b128 v[216:219], v144 offset:22528
	ds_read_b128 v[220:223], v144 offset:23552
	global_load_lds_dwordx4 v[140:141], off
	s_add_i32 m0, s14, 0x2000
	s_add_u32 s14, s22, 0x80000
	v_lshl_add_u64 v[232:233], s[22:23], 0, v[130:131]
	s_addc_u32 s15, s23, 0
	s_add_i32 s55, s56, s28
	global_load_lds_dwordx4 v[232:233], off
	v_lshl_add_u64 v[234:235], s[14:15], 0, v[186:187]
	s_mov_b32 m0, s55
	v_lshl_add_u64 v[236:237], s[40:41], 0, v[132:133]
	global_load_lds_dwordx4 v[234:235], off
	v_lshl_add_u64 v[234:235], s[14:15], 0, v[130:131]
	s_add_i32 m0, s55, 0x2000
	s_nop 0
	global_load_lds_dwordx4 v[234:235], off
	v_lshl_add_u64 v[234:235], s[40:41], 0, v[134:135]
	s_mov_b32 m0, s31
	s_nop 0
	global_load_lds_dwordx4 v[234:235], off
	s_mov_b32 m0, s42
	s_nop 0
	global_load_lds_dwordx4 v[236:237], off
	s_waitcnt vmcnt(16)
	s_waitcnt lgkmcnt(0)
	s_barrier
	s_setprio 1
	s_waitcnt lgkmcnt(0)
	v_mfma_f32_16x16x32_bf16 v[62:65], v[146:149], v[178:181], v[62:65]
	v_mfma_f32_16x16x32_bf16 v[54:57], v[154:157], v[178:181], v[54:57]
	v_mfma_f32_16x16x32_bf16 v[46:49], v[146:149], v[200:203], v[46:49]
	v_mfma_f32_16x16x32_bf16 v[38:41], v[154:157], v[200:203], v[38:41]
	v_mfma_f32_16x16x32_bf16 v[30:33], v[146:149], v[208:211], v[30:33]
	v_mfma_f32_16x16x32_bf16 v[22:25], v[154:157], v[208:211], v[22:25]
	v_mfma_f32_16x16x32_bf16 v[14:17], v[146:149], v[216:219], v[14:17]
	v_mfma_f32_16x16x32_bf16 v[6:9], v[154:157], v[216:219], v[6:9]
	v_mfma_f32_16x16x32_bf16 v[62:65], v[150:153], v[182:185], v[62:65]
	v_mfma_f32_16x16x32_bf16 v[54:57], v[158:161], v[182:185], v[54:57]
	v_mfma_f32_16x16x32_bf16 v[46:49], v[150:153], v[204:207], v[46:49]
	v_mfma_f32_16x16x32_bf16 v[38:41], v[158:161], v[204:207], v[38:41]
	v_mfma_f32_16x16x32_bf16 v[30:33], v[150:153], v[212:215], v[30:33]
	v_mfma_f32_16x16x32_bf16 v[22:25], v[158:161], v[212:215], v[22:25]
	v_mfma_f32_16x16x32_bf16 v[14:17], v[150:153], v[220:223], v[14:17]
	v_mfma_f32_16x16x32_bf16 v[6:9], v[158:161], v[220:223], v[6:9]
	s_setprio 0
	s_setprio 1
	v_mfma_f32_16x16x32_bf16 v[58:61], v[162:165], v[178:181], v[58:61]
	v_mfma_f32_16x16x32_bf16 v[50:53], v[170:173], v[178:181], v[50:53]
	v_mfma_f32_16x16x32_bf16 v[42:45], v[162:165], v[200:203], v[42:45]
	v_mfma_f32_16x16x32_bf16 v[34:37], v[170:173], v[200:203], v[34:37]
	v_mfma_f32_16x16x32_bf16 v[26:29], v[162:165], v[208:211], v[26:29]
	v_mfma_f32_16x16x32_bf16 v[18:21], v[170:173], v[208:211], v[18:21]
	v_mfma_f32_16x16x32_bf16 v[10:13], v[162:165], v[216:219], v[10:13]
	v_mfma_f32_16x16x32_bf16 v[2:5], v[170:173], v[216:219], v[2:5]
	v_mfma_f32_16x16x32_bf16 v[58:61], v[166:169], v[182:185], v[58:61]
	v_mfma_f32_16x16x32_bf16 v[50:53], v[174:177], v[182:185], v[50:53]
	v_mfma_f32_16x16x32_bf16 v[42:45], v[166:169], v[204:207], v[42:45]
	v_mfma_f32_16x16x32_bf16 v[34:37], v[174:177], v[204:207], v[34:37]
	v_mfma_f32_16x16x32_bf16 v[26:29], v[166:169], v[212:215], v[26:29]
	v_mfma_f32_16x16x32_bf16 v[18:21], v[174:177], v[212:215], v[18:21]
	v_mfma_f32_16x16x32_bf16 v[10:13], v[166:169], v[220:223], v[10:13]
	v_mfma_f32_16x16x32_bf16 v[2:5], v[174:177], v[220:223], v[2:5]
	s_setprio 0
	s_barrier
; #define PG8_STAGE(bufoff, gbase, voff) do { _Pragma("unroll") for (int _i = 0; _i < 2; ++_i) \
;         __builtin_amdgcn_global_load_lds((const unsigned*)((const char*)(gbase) + (voff)[_i]), (LAS unsigned*)(lds + (bufoff) + ldsw + _i * 8192), 16, 0, 0); } while (0)
; #define PG8_LDA(dst, b, h) do { _Pragma("unroll") for (int m = 0; m < 4; ++m) _Pragma("unroll") for (int k = 0; k < 2; ++k) dst[m][k] = *(const LAS bf16x8*)(lds + PG8_SA(b, h) + aoff + m * 2048 + k * 1024); } while (0)
; #define PG8_LDB(dst, b, h) do { _Pragma("unroll") for (int n = 0; n < 2; ++n) _Pragma("unroll") for (int k = 0; k < 2; ++k) dst[n][k] = *(const LAS bf16x8*)(lds + PG8_SB(b, h) + boff + n * 2048 + k * 1024); } while (0)
; #define PG8_MMA(ai, bj, At, Bt) do { __builtin_amdgcn_s_setprio(1); _Pragma("unroll") for (int m = 0; m < 4; ++m) _Pragma("unroll") for (int n = 0; n < 2; ++n) _Pragma("unroll") for (int k = 0; k < 2; ++k) \
;         acc[ai][bj][m][n] = __builtin_amdgcn_mfma_f32_16x16x32_bf16(Bt[n][k], At[m][k], acc[ai][bj][m][n], 0, 0, 0); __builtin_amdgcn_s_setprio(0); } while (0)
; #define PG8_WAIT_V(n) asm volatile("s_waitcnt vmcnt(" #n ")" ::: "memory")
; #define PG8_WAIT_L(n) asm volatile("s_waitcnt lgkmcnt(" #n ")" ::: "memory")
; #define PG8_BAR __builtin_amdgcn_s_barrier()
; #define PG8_SCHED __builtin_amdgcn_sched_barrier(0)
; template <class Epi, class Sched>
; __device__ __forceinline__ void gemm_phase(LAS unsigned char* lds, const Gemm g, const Sched& S, const Epi& E, const int tid, unsigned* last_sig = nullptr) {
;     ...
;             PG8_LDB(B0, 1, 0); PG8_LDB(B1, 1, 1); PG8_SCHED; PG8_LDA(At, 1, 0); PG8_STAGE(PG8_SA(0, 1), a2 + hstep, voffA);
;             PG8_WAIT_V(8); PG8_WAIT_L(0); PG8_BAR; PG8_MMA(0, 0, At, B0); PG8_MMA(0, 1, At, B1); PG8_BAR; PG8_SCHED;
	s_add_i32 s55, 0, 0x18000
	v_add_u32_e32 v145, s55, v1
	s_add_i32 s56, 0, 0x1c000
	ds_read_b128 v[146:149], v145
	ds_read_b128 v[150:153], v145 offset:1024
	ds_read_b128 v[154:157], v145 offset:2048
	ds_read_b128 v[158:161], v145 offset:3072
	v_add_u32_e32 v145, s56, v1
	ds_read_b128 v[162:165], v145
	ds_read_b128 v[166:169], v145 offset:1024
	ds_read_b128 v[170:173], v145 offset:2048
	ds_read_b128 v[174:177], v145 offset:3072
	s_add_u32 s14, s40, 0x80000
	s_addc_u32 s15, s41, 0
	s_mov_b32 m0, s43
	v_lshl_add_u64 v[238:239], s[14:15], 0, v[134:135]
	ds_read_b128 v[178:181], v144 offset:32768
	ds_read_b128 v[182:185], v144 offset:33792
	ds_read_b128 v[200:203], v144 offset:34816
	ds_read_b128 v[204:207], v144 offset:35840
	ds_read_b128 v[208:211], v144 offset:36864
	ds_read_b128 v[212:215], v144 offset:37888
	ds_read_b128 v[216:219], v144 offset:38912
	ds_read_b128 v[220:223], v144 offset:39936
	global_load_lds_dwordx4 v[238:239], off
	v_lshl_add_u64 v[238:239], s[14:15], 0, v[132:133]
	s_mov_b32 m0, s44
	s_nop 0
	global_load_lds_dwordx4 v[238:239], off
	s_waitcnt vmcnt(8)
	s_waitcnt lgkmcnt(0)
	s_barrier
	s_setprio 1
	s_waitcnt lgkmcnt(0)
	v_mfma_f32_16x16x32_bf16 v[126:129], v[146:149], v[178:181], v[126:129]
	v_mfma_f32_16x16x32_bf16 v[118:121], v[154:157], v[178:181], v[118:121]
	v_mfma_f32_16x16x32_bf16 v[110:113], v[146:149], v[200:203], v[110:113]
	v_mfma_f32_16x16x32_bf16 v[102:105], v[154:157], v[200:203], v[102:105]
	v_mfma_f32_16x16x32_bf16 v[94:97], v[146:149], v[208:211], v[94:97]
	v_mfma_f32_16x16x32_bf16 v[86:89], v[154:157], v[208:211], v[86:89]
	v_mfma_f32_16x16x32_bf16 v[78:81], v[146:149], v[216:219], v[78:81]
	v_mfma_f32_16x16x32_bf16 v[70:73], v[154:157], v[216:219], v[70:73]
	v_mfma_f32_16x16x32_bf16 v[126:129], v[150:153], v[182:185], v[126:129]
	v_mfma_f32_16x16x32_bf16 v[118:121], v[158:161], v[182:185], v[118:121]
	v_mfma_f32_16x16x32_bf16 v[110:113], v[150:153], v[204:207], v[110:113]
	v_mfma_f32_16x16x32_bf16 v[102:105], v[158:161], v[204:207], v[102:105]
	v_mfma_f32_16x16x32_bf16 v[94:97], v[150:153], v[212:215], v[94:97]
	v_mfma_f32_16x16x32_bf16 v[86:89], v[158:161], v[212:215], v[86:89]
	v_mfma_f32_16x16x32_bf16 v[78:81], v[150:153], v[220:223], v[78:81]
	v_mfma_f32_16x16x32_bf16 v[70:73], v[158:161], v[220:223], v[70:73]
	s_setprio 0
	s_setprio 1
	v_mfma_f32_16x16x32_bf16 v[122:125], v[162:165], v[178:181], v[122:125]
	v_mfma_f32_16x16x32_bf16 v[114:117], v[170:173], v[178:181], v[114:117]
	v_mfma_f32_16x16x32_bf16 v[106:109], v[162:165], v[200:203], v[106:109]
	v_mfma_f32_16x16x32_bf16 v[98:101], v[170:173], v[200:203], v[98:101]
	v_mfma_f32_16x16x32_bf16 v[90:93], v[162:165], v[208:211], v[90:93]
	v_mfma_f32_16x16x32_bf16 v[82:85], v[170:173], v[208:211], v[82:85]
	v_mfma_f32_16x16x32_bf16 v[74:77], v[162:165], v[216:219], v[74:77]
	v_mfma_f32_16x16x32_bf16 v[66:69], v[170:173], v[216:219], v[66:69]
	v_mfma_f32_16x16x32_bf16 v[122:125], v[166:169], v[182:185], v[122:125]
	v_mfma_f32_16x16x32_bf16 v[114:117], v[174:177], v[182:185], v[114:117]
	v_mfma_f32_16x16x32_bf16 v[106:109], v[166:169], v[204:207], v[106:109]
	v_mfma_f32_16x16x32_bf16 v[98:101], v[174:177], v[204:207], v[98:101]
	v_mfma_f32_16x16x32_bf16 v[90:93], v[166:169], v[212:215], v[90:93]
	v_mfma_f32_16x16x32_bf16 v[82:85], v[174:177], v[212:215], v[82:85]
	v_mfma_f32_16x16x32_bf16 v[74:77], v[166:169], v[220:223], v[74:77]
	v_mfma_f32_16x16x32_bf16 v[66:69], v[174:177], v[220:223], v[66:69]
	s_setprio 0
	s_barrier
; #define PG8_STAGE(bufoff, gbase, voff) do { _Pragma("unroll") for (int _i = 0; _i < 2; ++_i) \
;         __builtin_amdgcn_global_load_lds((const unsigned*)((const char*)(gbase) + (voff)[_i]), (LAS unsigned*)(lds + (bufoff) + ldsw + _i * 8192), 16, 0, 0); } while (0)
; #define PG8_LDA(dst, b, h) do { _Pragma("unroll") for (int m = 0; m < 4; ++m) _Pragma("unroll") for (int k = 0; k < 2; ++k) dst[m][k] = *(const LAS bf16x8*)(lds + PG8_SA(b, h) + aoff + m * 2048 + k * 1024); } while (0)
; #define PG8_MMA(ai, bj, At, Bt) do { __builtin_amdgcn_s_setprio(1); _Pragma("unroll") for (int m = 0; m < 4; ++m) _Pragma("unroll") for (int n = 0; n < 2; ++n) _Pragma("unroll") for (int k = 0; k < 2; ++k) \
;         acc[ai][bj][m][n] = __builtin_amdgcn_mfma_f32_16x16x32_bf16(Bt[n][k], At[m][k], acc[ai][bj][m][n], 0, 0, 0); __builtin_amdgcn_s_setprio(0); } while (0)
; #define PG8_WAIT_V(n) asm volatile("s_waitcnt vmcnt(" #n ")" ::: "memory")
; #define PG8_WAIT_L(n) asm volatile("s_waitcnt lgkmcnt(" #n ")" ::: "memory")
; #define PG8_BAR __builtin_amdgcn_s_barrier()
; #define PG8_SCHED __builtin_amdgcn_sched_barrier(0)
; template <class Epi, class Sched>
; __device__ __forceinline__ void gemm_phase(LAS unsigned char* lds, const Gemm g, const Sched& S, const Epi& E, const int tid, unsigned* last_sig = nullptr) {
;     ...
;             PG8_LDA(At, 1, 1); PG8_STAGE(PG8_SB(1, 0), b3, voffB); PG8_STAGE(PG8_SB(1, 1), b3 + hstep, voffB); PG8_STAGE(PG8_SA(1, 0), a3, voffA);
;             PG8_WAIT_V(8); PG8_WAIT_L(0); PG8_BAR; PG8_MMA(1, 0, At, B0); PG8_MMA(1, 1, At, B1); PG8_BAR; PG8_SCHED;
;         }
	s_add_i32 s14, s55, s28
	v_lshl_add_u64 v[140:141], v[140:141], 0, s[34:35]
	s_mov_b32 m0, s14
	ds_read_b128 v[178:181], v144 offset:49152
	ds_read_b128 v[182:185], v144 offset:50176
	ds_read_b128 v[200:203], v144 offset:51200
	ds_read_b128 v[204:207], v144 offset:52224
	ds_read_b128 v[208:211], v144 offset:53248
	ds_read_b128 v[212:215], v144 offset:54272
	ds_read_b128 v[216:219], v144 offset:55296
	ds_read_b128 v[220:223], v144 offset:56320
	global_load_lds_dwordx4 v[140:141], off
	s_add_i32 m0, s14, 0x2000
	s_add_u32 s14, s22, 0x80080
	v_lshl_add_u64 v[140:141], v[232:233], 0, s[34:35]
	s_addc_u32 s15, s23, 0
	s_add_i32 s22, s56, s28
	global_load_lds_dwordx4 v[140:141], off
	v_lshl_add_u64 v[140:141], s[14:15], 0, v[186:187]
	s_mov_b32 m0, s22
	s_nop 0
	global_load_lds_dwordx4 v[140:141], off
	v_lshl_add_u64 v[140:141], s[14:15], 0, v[130:131]
	s_add_i32 m0, s22, 0x2000
	s_nop 0
	global_load_lds_dwordx4 v[140:141], off
	v_lshl_add_u64 v[140:141], v[234:235], 0, s[34:35]
	s_mov_b32 m0, s45
	s_nop 0
	global_load_lds_dwordx4 v[140:141], off
	v_lshl_add_u64 v[140:141], v[236:237], 0, s[34:35]
	s_mov_b32 m0, s46
	s_nop 0
	global_load_lds_dwordx4 v[140:141], off
	s_waitcnt vmcnt(8)
	s_waitcnt lgkmcnt(0)
	s_barrier
	s_setprio 1
	s_waitcnt lgkmcnt(0)
	v_mfma_f32_16x16x32_bf16 v[62:65], v[146:149], v[178:181], v[62:65]
	v_mfma_f32_16x16x32_bf16 v[54:57], v[154:157], v[178:181], v[54:57]
	v_mfma_f32_16x16x32_bf16 v[46:49], v[146:149], v[200:203], v[46:49]
	v_mfma_f32_16x16x32_bf16 v[38:41], v[154:157], v[200:203], v[38:41]
	v_mfma_f32_16x16x32_bf16 v[30:33], v[146:149], v[208:211], v[30:33]
	v_mfma_f32_16x16x32_bf16 v[22:25], v[154:157], v[208:211], v[22:25]
	v_mfma_f32_16x16x32_bf16 v[14:17], v[146:149], v[216:219], v[14:17]
	v_mfma_f32_16x16x32_bf16 v[6:9], v[154:157], v[216:219], v[6:9]
	v_mfma_f32_16x16x32_bf16 v[62:65], v[150:153], v[182:185], v[62:65]
	v_mfma_f32_16x16x32_bf16 v[54:57], v[158:161], v[182:185], v[54:57]
	v_mfma_f32_16x16x32_bf16 v[46:49], v[150:153], v[204:207], v[46:49]
	v_mfma_f32_16x16x32_bf16 v[38:41], v[158:161], v[204:207], v[38:41]
	v_mfma_f32_16x16x32_bf16 v[30:33], v[150:153], v[212:215], v[30:33]
	v_mfma_f32_16x16x32_bf16 v[22:25], v[158:161], v[212:215], v[22:25]
	v_mfma_f32_16x16x32_bf16 v[14:17], v[150:153], v[220:223], v[14:17]
	v_mfma_f32_16x16x32_bf16 v[6:9], v[158:161], v[220:223], v[6:9]
	s_setprio 0
	s_setprio 1
	v_mfma_f32_16x16x32_bf16 v[58:61], v[162:165], v[178:181], v[58:61]
	v_mfma_f32_16x16x32_bf16 v[50:53], v[170:173], v[178:181], v[50:53]
	v_mfma_f32_16x16x32_bf16 v[42:45], v[162:165], v[200:203], v[42:45]
	v_mfma_f32_16x16x32_bf16 v[34:37], v[170:173], v[200:203], v[34:37]
	v_mfma_f32_16x16x32_bf16 v[26:29], v[162:165], v[208:211], v[26:29]
	v_mfma_f32_16x16x32_bf16 v[18:21], v[170:173], v[208:211], v[18:21]
	v_mfma_f32_16x16x32_bf16 v[10:13], v[162:165], v[216:219], v[10:13]
	v_mfma_f32_16x16x32_bf16 v[2:5], v[170:173], v[216:219], v[2:5]
	v_mfma_f32_16x16x32_bf16 v[58:61], v[166:169], v[182:185], v[58:61]
	v_mfma_f32_16x16x32_bf16 v[50:53], v[174:177], v[182:185], v[50:53]
	v_mfma_f32_16x16x32_bf16 v[42:45], v[166:169], v[204:207], v[42:45]
	v_mfma_f32_16x16x32_bf16 v[34:37], v[174:177], v[204:207], v[34:37]
	v_mfma_f32_16x16x32_bf16 v[26:29], v[166:169], v[212:215], v[26:29]
	v_mfma_f32_16x16x32_bf16 v[18:21], v[174:177], v[212:215], v[18:21]
	v_mfma_f32_16x16x32_bf16 v[10:13], v[166:169], v[220:223], v[10:13]
	v_mfma_f32_16x16x32_bf16 v[2:5], v[174:177], v[220:223], v[2:5]
	s_setprio 0
	s_barrier
	s_add_i32 s54, s54, 2
	s_add_u32 s20, s20, 0x100
	s_addc_u32 s21, s21, 0
	s_add_u32 s52, s52, 0x100
	s_addc_u32 s53, s53, 0
	s_cmp_gt_u32 s54, 29
	s_cbranch_scc1 .Lkpeel_exit_5

; #define PG8_STAGE(bufoff, gbase, voff) do { _Pragma("unroll") for (int _i = 0; _i < 2; ++_i) \
;         __builtin_amdgcn_global_load_lds((const unsigned*)((const char*)(gbase) + (voff)[_i]), (LAS unsigned*)(lds + (bufoff) + ldsw + _i * 8192), 16, 0, 0); } while (0)
; #define PG8_LDA(dst, b, h) do { _Pragma("unroll") for (int m = 0; m < 4; ++m) _Pragma("unroll") for (int k = 0; k < 2; ++k) dst[m][k] = *(const LAS bf16x8*)(lds + PG8_SA(b, h) + aoff + m * 2048 + k * 1024); } while (0)
; #define PG8_LDB(dst, b, h) do { _Pragma("unroll") for (int n = 0; n < 2; ++n) _Pragma("unroll") for (int k = 0; k < 2; ++k) dst[n][k] = *(const LAS bf16x8*)(lds + PG8_SB(b, h) + boff + n * 2048 + k * 1024); } while (0)
; #define PG8_WAIT_V(n) asm volatile("s_waitcnt vmcnt(" #n ")" ::: "memory")
; #define PG8_WAIT_L(n) asm volatile("s_waitcnt lgkmcnt(" #n ")" ::: "memory")
; #define PG8_BAR __builtin_amdgcn_s_barrier()
; #define PG8_SCHED __builtin_amdgcn_sched_barrier(0)
; template <class Epi, class Sched>
; __device__ __forceinline__ void gemm_phase(LAS unsigned char* lds, const Gemm g, const Sched& S, const Epi& E, const int tid, unsigned* last_sig = nullptr) {
;     ...
;         for (int t = 0; t < nt; t += 2) {
;             const bool last = (t == nt - 2);
;             const char* a1 = cA + (size_t)(t + 1) * kstep;
;             const char* a2 = last ? nA : cA + (size_t)(t + 2) * kstep; const char* b2 = last ? nB : cB + (size_t)(t + 2) * kstep;
;             const char* a3 = a2 + kstep; const char* b3 = b2 + kstep;
;             PG8_LDB(B0, 0, 0); PG8_LDB(B1, 0, 1); PG8_SCHED; PG8_LDA(At, 0, 0); PG8_STAGE(PG8_SA(1, 1), a1 + hstep, voffA);
;             PG8_WAIT_V(8); PG8_WAIT_L(0); PG8_BAR; PG8_MMA(0, 0, At, B0); PG8_MMA(0, 1, At, B1); PG8_BAR; PG8_SCHED;
;             PG8_LDA(At, 0, 1); PG8_STAGE(PG8_SB(0, 0), b2, voffB); PG8_STAGE(PG8_SB(0, 1), b2 + hstep, voffB); PG8_STAGE(PG8_SA(0, 0), a2, voffA);
;             PG8_WAIT_V(8); PG8_WAIT_L(0); PG8_BAR; PG8_MMA(1, 0, At, B0); PG8_MMA(1, 1, At, B1); PG8_BAR; PG8_SCHED;
;     ...
; #pragma unroll
;         for (int a = 0; a < 2; ++a)
; #pragma unroll
;             for (int b = 0; b < 2; ++b)
; #pragma unroll
;                 for (int m = 0; m < 4; ++m)
; #pragma unroll
;                     for (int n = 0; n < 2; ++n) acc[a][b][m][n] = (f32x4){0.f, 0.f, 0.f, 0.f};
;         cur = nxt; cA = nA; cB = nB; ++ui;
.LBB0_1261:
	s_add_u32 s54, s18, 0x100
	v_mov_b32_e32 v2, 0
	s_addc_u32 s55, s19, 0
	s_mov_b32 s56, -2
	v_mov_b32_e32 v3, v2
	v_mov_b32_e32 v4, v2
	v_mov_b32_e32 v5, v2
	v_mov_b32_e32 v6, v2
	v_mov_b32_e32 v7, v2
	v_mov_b32_e32 v8, v2
	v_mov_b32_e32 v9, v2
	v_mov_b32_e32 v10, v2
	v_mov_b32_e32 v11, v2
	v_mov_b32_e32 v12, v2
	v_mov_b32_e32 v13, v2
	v_mov_b32_e32 v14, v2
	v_mov_b32_e32 v15, v2
	v_mov_b32_e32 v16, v2
	v_mov_b32_e32 v17, v2
	v_mov_b32_e32 v26, v2
	v_mov_b32_e32 v27, v2
	v_mov_b32_e32 v28, v2
	v_mov_b32_e32 v29, v2
	v_mov_b32_e32 v30, v2
	v_mov_b32_e32 v31, v2
	v_mov_b32_e32 v32, v2
	v_mov_b32_e32 v33, v2
	v_mov_b32_e32 v42, v2
	v_mov_b32_e32 v43, v2
	v_mov_b32_e32 v44, v2
	v_mov_b32_e32 v45, v2
	v_mov_b32_e32 v46, v2
	v_mov_b32_e32 v47, v2
	v_mov_b32_e32 v48, v2
	v_mov_b32_e32 v49, v2
	v_mov_b32_e32 v18, v2
	v_mov_b32_e32 v19, v2
	v_mov_b32_e32 v20, v2
	v_mov_b32_e32 v21, v2
	v_mov_b32_e32 v22, v2
	v_mov_b32_e32 v23, v2
	v_mov_b32_e32 v24, v2
	v_mov_b32_e32 v25, v2
	v_mov_b32_e32 v34, v2
	v_mov_b32_e32 v35, v2
	v_mov_b32_e32 v36, v2
	v_mov_b32_e32 v37, v2
	v_mov_b32_e32 v38, v2
	v_mov_b32_e32 v39, v2
	v_mov_b32_e32 v40, v2
	v_mov_b32_e32 v41, v2
	v_mov_b32_e32 v50, v2
	v_mov_b32_e32 v51, v2
	v_mov_b32_e32 v52, v2
	v_mov_b32_e32 v53, v2
	v_mov_b32_e32 v54, v2
	v_mov_b32_e32 v55, v2
	v_mov_b32_e32 v56, v2
	v_mov_b32_e32 v57, v2
	v_mov_b32_e32 v58, v2
	v_mov_b32_e32 v59, v2
	v_mov_b32_e32 v60, v2
	v_mov_b32_e32 v61, v2
	v_mov_b32_e32 v62, v2
	v_mov_b32_e32 v63, v2
	v_mov_b32_e32 v64, v2
	v_mov_b32_e32 v65, v2
	v_mov_b32_e32 v66, v2
	v_mov_b32_e32 v67, v2
	v_mov_b32_e32 v68, v2
	v_mov_b32_e32 v69, v2
	v_mov_b32_e32 v70, v2
	v_mov_b32_e32 v71, v2
	v_mov_b32_e32 v72, v2
	v_mov_b32_e32 v73, v2
	v_mov_b32_e32 v74, v2
	v_mov_b32_e32 v75, v2
	v_mov_b32_e32 v76, v2
	v_mov_b32_e32 v77, v2
	v_mov_b32_e32 v78, v2
	v_mov_b32_e32 v79, v2
	v_mov_b32_e32 v80, v2
	v_mov_b32_e32 v81, v2
	v_mov_b32_e32 v90, v2
	v_mov_b32_e32 v91, v2
	v_mov_b32_e32 v92, v2
	v_mov_b32_e32 v93, v2
	v_mov_b32_e32 v94, v2
	v_mov_b32_e32 v95, v2
	v_mov_b32_e32 v96, v2
	v_mov_b32_e32 v97, v2
	v_mov_b32_e32 v106, v2
	v_mov_b32_e32 v107, v2
	v_mov_b32_e32 v108, v2
	v_mov_b32_e32 v109, v2
	v_mov_b32_e32 v110, v2
	v_mov_b32_e32 v111, v2
	v_mov_b32_e32 v112, v2
	v_mov_b32_e32 v113, v2
	v_mov_b32_e32 v82, v2
	v_mov_b32_e32 v83, v2
	v_mov_b32_e32 v84, v2
	v_mov_b32_e32 v85, v2
	v_mov_b32_e32 v86, v2
	v_mov_b32_e32 v87, v2
	v_mov_b32_e32 v88, v2
	v_mov_b32_e32 v89, v2
	v_mov_b32_e32 v98, v2
	v_mov_b32_e32 v99, v2
	v_mov_b32_e32 v100, v2
	v_mov_b32_e32 v101, v2
	v_mov_b32_e32 v102, v2
	v_mov_b32_e32 v103, v2
	v_mov_b32_e32 v104, v2
	v_mov_b32_e32 v105, v2
	v_mov_b32_e32 v114, v2
	v_mov_b32_e32 v115, v2
	v_mov_b32_e32 v116, v2
	v_mov_b32_e32 v117, v2
	v_mov_b32_e32 v118, v2
	v_mov_b32_e32 v119, v2
	v_mov_b32_e32 v120, v2
	v_mov_b32_e32 v121, v2
	v_mov_b32_e32 v122, v2
	v_mov_b32_e32 v123, v2
	v_mov_b32_e32 v124, v2
	v_mov_b32_e32 v125, v2
	v_mov_b32_e32 v126, v2
	v_mov_b32_e32 v127, v2
	v_mov_b32_e32 v128, v2
	v_mov_b32_e32 v129, v2
	s_cmp_eq_u32 s50, 1
	s_cbranch_scc1 .LBB0_1262
	s_add_u32 s18, s16, 0x100
	s_addc_u32 s19, s17, 0
	s_add_i32 s14, 0, 0x10000
	s_cmp_eq_u32 s56, 52
	s_cselect_b32 s23, s5, s19
	s_cselect_b32 s22, s4, s18
	s_cselect_b32 s21, s13, s55
	s_cselect_b32 s20, s12, s54
	s_add_i32 s57, 0, 0x14000
	v_add_u32_e32 v156, s14, v141
	v_add_u32_e32 v172, s57, v141
	ds_read_b128 v[144:147], v156
	ds_read_b128 v[148:151], v156 offset:1024
	ds_read_b128 v[152:155], v156 offset:2048
	ds_read_b128 v[156:159], v156 offset:3072
	ds_read_b128 v[160:163], v172
	ds_read_b128 v[164:167], v172 offset:1024
	ds_read_b128 v[168:171], v172 offset:2048
	ds_read_b128 v[172:175], v172 offset:3072
	v_lshl_add_u64 v[184:185], s[16:17], 0, v[136:137]
	s_add_i32 m0, s42, 0xc000
	ds_read_b128 v[176:179], v143
	ds_read_b128 v[180:183], v143 offset:1024
	ds_read_b128 v[200:203], v143 offset:2048
	ds_read_b128 v[204:207], v143 offset:3072
	ds_read_b128 v[208:211], v143 offset:4096
	ds_read_b128 v[212:215], v143 offset:5120
	ds_read_b128 v[216:219], v143 offset:6144
	ds_read_b128 v[220:223], v143 offset:7168
	global_load_lds_dwordx4 v[184:185], off
	v_lshl_add_u64 v[184:185], s[16:17], 0, v[138:139]
	s_add_i32 m0, s42, 0xe000
	s_nop 0
	global_load_lds_dwordx4 v[184:185], off
	s_waitcnt vmcnt(24)
	s_waitcnt lgkmcnt(0)
	s_barrier
	s_setprio 1
	s_waitcnt lgkmcnt(0)
	v_mfma_f32_16x16x32_bf16 v[126:129], v[144:147], v[176:179], v[126:129]
	v_mfma_f32_16x16x32_bf16 v[122:125], v[152:155], v[176:179], v[122:125]
	v_mfma_f32_16x16x32_bf16 v[118:121], v[144:147], v[200:203], v[118:121]
	v_mfma_f32_16x16x32_bf16 v[114:117], v[152:155], v[200:203], v[114:117]
	v_mfma_f32_16x16x32_bf16 v[102:105], v[144:147], v[208:211], v[102:105]
	v_mfma_f32_16x16x32_bf16 v[98:101], v[152:155], v[208:211], v[98:101]
	v_mfma_f32_16x16x32_bf16 v[86:89], v[144:147], v[216:219], v[86:89]
	v_mfma_f32_16x16x32_bf16 v[82:85], v[152:155], v[216:219], v[82:85]
	v_mfma_f32_16x16x32_bf16 v[126:129], v[148:151], v[180:183], v[126:129]
	v_mfma_f32_16x16x32_bf16 v[122:125], v[156:159], v[180:183], v[122:125]
	v_mfma_f32_16x16x32_bf16 v[118:121], v[148:151], v[204:207], v[118:121]
	v_mfma_f32_16x16x32_bf16 v[114:117], v[156:159], v[204:207], v[114:117]
	v_mfma_f32_16x16x32_bf16 v[102:105], v[148:151], v[212:215], v[102:105]
	v_mfma_f32_16x16x32_bf16 v[98:101], v[156:159], v[212:215], v[98:101]
	v_mfma_f32_16x16x32_bf16 v[86:89], v[148:151], v[220:223], v[86:89]
	v_mfma_f32_16x16x32_bf16 v[82:85], v[156:159], v[220:223], v[82:85]
	s_setprio 0
	s_setprio 1
	v_mfma_f32_16x16x32_bf16 v[110:113], v[160:163], v[176:179], v[110:113]
	v_mfma_f32_16x16x32_bf16 v[106:109], v[168:171], v[176:179], v[106:109]
	v_mfma_f32_16x16x32_bf16 v[94:97], v[160:163], v[200:203], v[94:97]
	v_mfma_f32_16x16x32_bf16 v[90:93], v[168:171], v[200:203], v[90:93]
	v_mfma_f32_16x16x32_bf16 v[78:81], v[160:163], v[208:211], v[78:81]
	v_mfma_f32_16x16x32_bf16 v[74:77], v[168:171], v[208:211], v[74:77]
	v_mfma_f32_16x16x32_bf16 v[70:73], v[160:163], v[216:219], v[70:73]
	v_mfma_f32_16x16x32_bf16 v[66:69], v[168:171], v[216:219], v[66:69]
	v_mfma_f32_16x16x32_bf16 v[110:113], v[164:167], v[180:183], v[110:113]
	v_mfma_f32_16x16x32_bf16 v[106:109], v[172:175], v[180:183], v[106:109]
	v_mfma_f32_16x16x32_bf16 v[94:97], v[164:167], v[204:207], v[94:97]
	v_mfma_f32_16x16x32_bf16 v[90:93], v[172:175], v[204:207], v[90:93]
	v_mfma_f32_16x16x32_bf16 v[78:81], v[164:167], v[212:215], v[78:81]
	v_mfma_f32_16x16x32_bf16 v[74:77], v[172:175], v[212:215], v[74:77]
	v_mfma_f32_16x16x32_bf16 v[70:73], v[164:167], v[220:223], v[70:73]
	v_mfma_f32_16x16x32_bf16 v[66:69], v[172:175], v[220:223], v[66:69]
	s_setprio 0
	s_barrier
; #define PG8_STAGE(bufoff, gbase, voff) do { _Pragma("unroll") for (int _i = 0; _i < 2; ++_i) \
;         __builtin_amdgcn_global_load_lds((const unsigned*)((const char*)(gbase) + (voff)[_i]), (LAS unsigned*)(lds + (bufoff) + ldsw + _i * 8192), 16, 0, 0); } while (0)
; #define PG8_LDA(dst, b, h) do { _Pragma("unroll") for (int m = 0; m < 4; ++m) _Pragma("unroll") for (int k = 0; k < 2; ++k) dst[m][k] = *(const LAS bf16x8*)(lds + PG8_SA(b, h) + aoff + m * 2048 + k * 1024); } while (0)
; #define PG8_LDB(dst, b, h) do { _Pragma("unroll") for (int n = 0; n < 2; ++n) _Pragma("unroll") for (int k = 0; k < 2; ++k) dst[n][k] = *(const LAS bf16x8*)(lds + PG8_SB(b, h) + boff + n * 2048 + k * 1024); } while (0)
; #define PG8_MMA(ai, bj, At, Bt) do { __builtin_amdgcn_s_setprio(1); _Pragma("unroll") for (int m = 0; m < 4; ++m) _Pragma("unroll") for (int n = 0; n < 2; ++n) _Pragma("unroll") for (int k = 0; k < 2; ++k) \
;         acc[ai][bj][m][n] = __builtin_amdgcn_mfma_f32_16x16x32_bf16(Bt[n][k], At[m][k], acc[ai][bj][m][n], 0, 0, 0); __builtin_amdgcn_s_setprio(0); } while (0)
; #define PG8_WAIT_V(n) asm volatile("s_waitcnt vmcnt(" #n ")" ::: "memory")
; #define PG8_WAIT_L(n) asm volatile("s_waitcnt lgkmcnt(" #n ")" ::: "memory")
; #define PG8_BAR __builtin_amdgcn_s_barrier()
; #define PG8_SCHED __builtin_amdgcn_sched_barrier(0)
; template <class Epi, class Sched>
; __device__ __forceinline__ void gemm_phase(LAS unsigned char* lds, const Gemm g, const Sched& S, const Epi& E, const int tid, unsigned* last_sig = nullptr) {
;     ...
;             PG8_LDA(At, 0, 1); PG8_STAGE(PG8_SB(0, 0), b2, voffB); PG8_STAGE(PG8_SB(0, 1), b2 + hstep, voffB); PG8_STAGE(PG8_SA(0, 0), a2, voffA);
;             PG8_WAIT_V(8); PG8_WAIT_L(0); PG8_BAR; PG8_MMA(1, 0, At, B0); PG8_MMA(1, 1, At, B1); PG8_BAR; PG8_SCHED;
;             PG8_LDB(B0, 1, 0); PG8_LDB(B1, 1, 1); PG8_SCHED; PG8_LDA(At, 1, 0); PG8_STAGE(PG8_SA(0, 1), a2 + hstep, voffA);
;             PG8_WAIT_V(8); PG8_WAIT_L(0); PG8_BAR; PG8_MMA(0, 0, At, B0); PG8_MMA(0, 1, At, B1); PG8_BAR; PG8_SCHED;
	s_add_i32 s14, s14, s40
	v_lshl_add_u64 v[184:185], s[20:21], 0, v[186:187]
	s_mov_b32 m0, s14
	ds_read_b128 v[176:179], v143 offset:16384
	ds_read_b128 v[180:183], v143 offset:17408
	ds_read_b128 v[200:203], v143 offset:18432
	ds_read_b128 v[204:207], v143 offset:19456
	ds_read_b128 v[208:211], v143 offset:20480
	ds_read_b128 v[212:215], v143 offset:21504
	ds_read_b128 v[216:219], v143 offset:22528
	ds_read_b128 v[220:223], v143 offset:23552
	global_load_lds_dwordx4 v[184:185], off
	s_add_i32 m0, s14, 0x2000
	s_add_u32 s14, s20, 0xe0000
	v_lshl_add_u64 v[232:233], s[20:21], 0, v[134:135]
	s_addc_u32 s15, s21, 0
	s_add_i32 s16, s57, s40
	global_load_lds_dwordx4 v[232:233], off
	v_lshl_add_u64 v[234:235], s[14:15], 0, v[186:187]
	s_mov_b32 m0, s16
	v_lshl_add_u64 v[236:237], s[22:23], 0, v[132:133]
	global_load_lds_dwordx4 v[234:235], off
	v_lshl_add_u64 v[234:235], s[14:15], 0, v[134:135]
	s_add_i32 m0, s16, 0x2000
	s_nop 0
	global_load_lds_dwordx4 v[234:235], off
	v_lshl_add_u64 v[234:235], s[22:23], 0, v[130:131]
	s_mov_b32 m0, s42
	s_nop 0
	global_load_lds_dwordx4 v[234:235], off
	s_mov_b32 m0, s43
	s_nop 0
	global_load_lds_dwordx4 v[236:237], off
	s_waitcnt vmcnt(24)
	s_waitcnt lgkmcnt(0)
	s_barrier
	s_setprio 1
	s_waitcnt lgkmcnt(0)
	v_mfma_f32_16x16x32_bf16 v[62:65], v[144:147], v[176:179], v[62:65]
	v_mfma_f32_16x16x32_bf16 v[58:61], v[152:155], v[176:179], v[58:61]
	v_mfma_f32_16x16x32_bf16 v[54:57], v[144:147], v[200:203], v[54:57]
	v_mfma_f32_16x16x32_bf16 v[50:53], v[152:155], v[200:203], v[50:53]
	v_mfma_f32_16x16x32_bf16 v[38:41], v[144:147], v[208:211], v[38:41]
	v_mfma_f32_16x16x32_bf16 v[34:37], v[152:155], v[208:211], v[34:37]
	v_mfma_f32_16x16x32_bf16 v[22:25], v[144:147], v[216:219], v[22:25]
	v_mfma_f32_16x16x32_bf16 v[18:21], v[152:155], v[216:219], v[18:21]
	v_mfma_f32_16x16x32_bf16 v[62:65], v[148:151], v[180:183], v[62:65]
	v_mfma_f32_16x16x32_bf16 v[58:61], v[156:159], v[180:183], v[58:61]
	v_mfma_f32_16x16x32_bf16 v[54:57], v[148:151], v[204:207], v[54:57]
	v_mfma_f32_16x16x32_bf16 v[50:53], v[156:159], v[204:207], v[50:53]
	v_mfma_f32_16x16x32_bf16 v[38:41], v[148:151], v[212:215], v[38:41]
	v_mfma_f32_16x16x32_bf16 v[34:37], v[156:159], v[212:215], v[34:37]
	v_mfma_f32_16x16x32_bf16 v[22:25], v[148:151], v[220:223], v[22:25]
	v_mfma_f32_16x16x32_bf16 v[18:21], v[156:159], v[220:223], v[18:21]
	s_setprio 0
	s_setprio 1
	v_mfma_f32_16x16x32_bf16 v[46:49], v[160:163], v[176:179], v[46:49]
	v_mfma_f32_16x16x32_bf16 v[42:45], v[168:171], v[176:179], v[42:45]
	v_mfma_f32_16x16x32_bf16 v[30:33], v[160:163], v[200:203], v[30:33]
	v_mfma_f32_16x16x32_bf16 v[26:29], v[168:171], v[200:203], v[26:29]
	v_mfma_f32_16x16x32_bf16 v[14:17], v[160:163], v[208:211], v[14:17]
	v_mfma_f32_16x16x32_bf16 v[10:13], v[168:171], v[208:211], v[10:13]
	v_mfma_f32_16x16x32_bf16 v[6:9], v[160:163], v[216:219], v[6:9]
	v_mfma_f32_16x16x32_bf16 v[2:5], v[168:171], v[216:219], v[2:5]
	v_mfma_f32_16x16x32_bf16 v[46:49], v[164:167], v[180:183], v[46:49]
	v_mfma_f32_16x16x32_bf16 v[42:45], v[172:175], v[180:183], v[42:45]
	v_mfma_f32_16x16x32_bf16 v[30:33], v[164:167], v[204:207], v[30:33]
	v_mfma_f32_16x16x32_bf16 v[26:29], v[172:175], v[204:207], v[26:29]
	v_mfma_f32_16x16x32_bf16 v[14:17], v[164:167], v[212:215], v[14:17]
	v_mfma_f32_16x16x32_bf16 v[10:13], v[172:175], v[212:215], v[10:13]
	v_mfma_f32_16x16x32_bf16 v[6:9], v[164:167], v[220:223], v[6:9]
	v_mfma_f32_16x16x32_bf16 v[2:5], v[172:175], v[220:223], v[2:5]
	s_setprio 0
	s_barrier
	s_add_i32 s16, 0, 0x18000
	s_add_i32 s17, 0, 0x1c000
	v_add_u32_e32 v156, s16, v141
	v_add_u32_e32 v172, s17, v141
	ds_read_b128 v[144:147], v156
	ds_read_b128 v[148:151], v156 offset:1024
	ds_read_b128 v[152:155], v156 offset:2048
	ds_read_b128 v[156:159], v156 offset:3072
	ds_read_b128 v[160:163], v172
	ds_read_b128 v[164:167], v172 offset:1024
	ds_read_b128 v[168:171], v172 offset:2048
	ds_read_b128 v[172:175], v172 offset:3072
	s_add_u32 s14, s22, 0xe0000
	s_addc_u32 s15, s23, 0
	s_mov_b32 m0, s44
	v_lshl_add_u64 v[238:239], s[14:15], 0, v[130:131]
	ds_read_b128 v[176:179], v143 offset:32768
	ds_read_b128 v[180:183], v143 offset:33792
	ds_read_b128 v[200:203], v143 offset:34816
	ds_read_b128 v[204:207], v143 offset:35840
	ds_read_b128 v[208:211], v143 offset:36864
	ds_read_b128 v[212:215], v143 offset:37888
	ds_read_b128 v[216:219], v143 offset:38912
	ds_read_b128 v[220:223], v143 offset:39936
	global_load_lds_dwordx4 v[238:239], off
	v_lshl_add_u64 v[238:239], s[14:15], 0, v[132:133]
	s_mov_b32 m0, s45
	s_nop 0
	global_load_lds_dwordx4 v[238:239], off
	s_waitcnt vmcnt(8)
	s_waitcnt lgkmcnt(0)
	s_barrier
; #define PG8_STAGE(bufoff, gbase, voff) do { _Pragma("unroll") for (int _i = 0; _i < 2; ++_i) \
;         __builtin_amdgcn_global_load_lds((const unsigned*)((const char*)(gbase) + (voff)[_i]), (LAS unsigned*)(lds + (bufoff) + ldsw + _i * 8192), 16, 0, 0); } while (0)
; #define PG8_LDA(dst, b, h) do { _Pragma("unroll") for (int m = 0; m < 4; ++m) _Pragma("unroll") for (int k = 0; k < 2; ++k) dst[m][k] = *(const LAS bf16x8*)(lds + PG8_SA(b, h) + aoff + m * 2048 + k * 1024); } while (0)
; #define PG8_MMA(ai, bj, At, Bt) do { __builtin_amdgcn_s_setprio(1); _Pragma("unroll") for (int m = 0; m < 4; ++m) _Pragma("unroll") for (int n = 0; n < 2; ++n) _Pragma("unroll") for (int k = 0; k < 2; ++k) \
;         acc[ai][bj][m][n] = __builtin_amdgcn_mfma_f32_16x16x32_bf16(Bt[n][k], At[m][k], acc[ai][bj][m][n], 0, 0, 0); __builtin_amdgcn_s_setprio(0); } while (0)
; #define PG8_WAIT_V(n) asm volatile("s_waitcnt vmcnt(" #n ")" ::: "memory")
; #define PG8_WAIT_L(n) asm volatile("s_waitcnt lgkmcnt(" #n ")" ::: "memory")
; #define PG8_BAR __builtin_amdgcn_s_barrier()
; #define PG8_SCHED __builtin_amdgcn_sched_barrier(0)
; template <class Epi, class Sched>
; __device__ __forceinline__ void gemm_phase(LAS unsigned char* lds, const Gemm g, const Sched& S, const Epi& E, const int tid, unsigned* last_sig = nullptr) {
;     ...
;             PG8_WAIT_V(8); PG8_WAIT_L(0); PG8_BAR; PG8_MMA(0, 0, At, B0); PG8_MMA(0, 1, At, B1); PG8_BAR; PG8_SCHED;
;             PG8_LDA(At, 1, 1); PG8_STAGE(PG8_SB(1, 0), b3, voffB); PG8_STAGE(PG8_SB(1, 1), b3 + hstep, voffB); PG8_STAGE(PG8_SA(1, 0), a3, voffA);
;             PG8_WAIT_V(8); PG8_WAIT_L(0); PG8_BAR; PG8_MMA(1, 0, At, B0); PG8_MMA(1, 1, At, B1); PG8_BAR; PG8_SCHED;
;         }
	s_setprio 1
	s_waitcnt lgkmcnt(0)
	v_mfma_f32_16x16x32_bf16 v[126:129], v[144:147], v[176:179], v[126:129]
	v_mfma_f32_16x16x32_bf16 v[122:125], v[152:155], v[176:179], v[122:125]
	v_mfma_f32_16x16x32_bf16 v[118:121], v[144:147], v[200:203], v[118:121]
	v_mfma_f32_16x16x32_bf16 v[114:117], v[152:155], v[200:203], v[114:117]
	v_mfma_f32_16x16x32_bf16 v[102:105], v[144:147], v[208:211], v[102:105]
	v_mfma_f32_16x16x32_bf16 v[98:101], v[152:155], v[208:211], v[98:101]
	v_mfma_f32_16x16x32_bf16 v[86:89], v[144:147], v[216:219], v[86:89]
	v_mfma_f32_16x16x32_bf16 v[82:85], v[152:155], v[216:219], v[82:85]
	v_mfma_f32_16x16x32_bf16 v[126:129], v[148:151], v[180:183], v[126:129]
	v_mfma_f32_16x16x32_bf16 v[122:125], v[156:159], v[180:183], v[122:125]
	v_mfma_f32_16x16x32_bf16 v[118:121], v[148:151], v[204:207], v[118:121]
	v_mfma_f32_16x16x32_bf16 v[114:117], v[156:159], v[204:207], v[114:117]
	v_mfma_f32_16x16x32_bf16 v[102:105], v[148:151], v[212:215], v[102:105]
	v_mfma_f32_16x16x32_bf16 v[98:101], v[156:159], v[212:215], v[98:101]
	v_mfma_f32_16x16x32_bf16 v[86:89], v[148:151], v[220:223], v[86:89]
	v_mfma_f32_16x16x32_bf16 v[82:85], v[156:159], v[220:223], v[82:85]
	s_setprio 0
	s_setprio 1
	v_mfma_f32_16x16x32_bf16 v[110:113], v[160:163], v[176:179], v[110:113]
	v_mfma_f32_16x16x32_bf16 v[106:109], v[168:171], v[176:179], v[106:109]
	v_mfma_f32_16x16x32_bf16 v[94:97], v[160:163], v[200:203], v[94:97]
	v_mfma_f32_16x16x32_bf16 v[90:93], v[168:171], v[200:203], v[90:93]
	v_mfma_f32_16x16x32_bf16 v[78:81], v[160:163], v[208:211], v[78:81]
	v_mfma_f32_16x16x32_bf16 v[74:77], v[168:171], v[208:211], v[74:77]
	v_mfma_f32_16x16x32_bf16 v[70:73], v[160:163], v[216:219], v[70:73]
	v_mfma_f32_16x16x32_bf16 v[66:69], v[168:171], v[216:219], v[66:69]
	v_mfma_f32_16x16x32_bf16 v[110:113], v[164:167], v[180:183], v[110:113]
	v_mfma_f32_16x16x32_bf16 v[106:109], v[172:175], v[180:183], v[106:109]
	v_mfma_f32_16x16x32_bf16 v[94:97], v[164:167], v[204:207], v[94:97]
	v_mfma_f32_16x16x32_bf16 v[90:93], v[172:175], v[204:207], v[90:93]
	v_mfma_f32_16x16x32_bf16 v[78:81], v[164:167], v[212:215], v[78:81]
	v_mfma_f32_16x16x32_bf16 v[74:77], v[172:175], v[212:215], v[74:77]
	v_mfma_f32_16x16x32_bf16 v[70:73], v[164:167], v[220:223], v[70:73]
	v_mfma_f32_16x16x32_bf16 v[66:69], v[172:175], v[220:223], v[66:69]
	s_setprio 0
	s_barrier
	s_add_i32 s14, s16, s40
	v_lshl_add_u64 v[184:185], v[184:185], 0, s[34:35]
	s_mov_b32 m0, s14
	ds_read_b128 v[176:179], v143 offset:49152
	ds_read_b128 v[180:183], v143 offset:50176
	ds_read_b128 v[200:203], v143 offset:51200
	ds_read_b128 v[204:207], v143 offset:52224
	ds_read_b128 v[208:211], v143 offset:53248
	ds_read_b128 v[212:215], v143 offset:54272
	ds_read_b128 v[216:219], v143 offset:55296
	ds_read_b128 v[220:223], v143 offset:56320
	global_load_lds_dwordx4 v[184:185], off
	s_add_i32 m0, s14, 0x2000
	s_add_u32 s14, s20, 0xe0080
	v_lshl_add_u64 v[184:185], v[232:233], 0, s[34:35]
	s_addc_u32 s15, s21, 0
	s_add_i32 s16, s17, s40
	global_load_lds_dwordx4 v[184:185], off
	v_lshl_add_u64 v[184:185], s[14:15], 0, v[186:187]
	s_mov_b32 m0, s16
	s_nop 0
	global_load_lds_dwordx4 v[184:185], off
	v_lshl_add_u64 v[184:185], s[14:15], 0, v[134:135]
	s_add_i32 m0, s16, 0x2000
	s_nop 0
	global_load_lds_dwordx4 v[184:185], off
	v_lshl_add_u64 v[184:185], v[234:235], 0, s[34:35]
	s_mov_b32 m0, s47
	s_nop 0
	global_load_lds_dwordx4 v[184:185], off
	v_lshl_add_u64 v[184:185], v[236:237], 0, s[34:35]
	s_mov_b32 m0, s49
	s_nop 0
	global_load_lds_dwordx4 v[184:185], off
	s_waitcnt vmcnt(8)
	s_waitcnt lgkmcnt(0)
	s_barrier
	s_setprio 1
	s_waitcnt lgkmcnt(0)
	v_mfma_f32_16x16x32_bf16 v[62:65], v[144:147], v[176:179], v[62:65]
	v_mfma_f32_16x16x32_bf16 v[58:61], v[152:155], v[176:179], v[58:61]
	v_mfma_f32_16x16x32_bf16 v[54:57], v[144:147], v[200:203], v[54:57]
	v_mfma_f32_16x16x32_bf16 v[50:53], v[152:155], v[200:203], v[50:53]
	v_mfma_f32_16x16x32_bf16 v[38:41], v[144:147], v[208:211], v[38:41]
	v_mfma_f32_16x16x32_bf16 v[34:37], v[152:155], v[208:211], v[34:37]
	v_mfma_f32_16x16x32_bf16 v[22:25], v[144:147], v[216:219], v[22:25]
	v_mfma_f32_16x16x32_bf16 v[18:21], v[152:155], v[216:219], v[18:21]
	v_mfma_f32_16x16x32_bf16 v[62:65], v[148:151], v[180:183], v[62:65]
	v_mfma_f32_16x16x32_bf16 v[58:61], v[156:159], v[180:183], v[58:61]
	v_mfma_f32_16x16x32_bf16 v[54:57], v[148:151], v[204:207], v[54:57]
	v_mfma_f32_16x16x32_bf16 v[50:53], v[156:159], v[204:207], v[50:53]
	v_mfma_f32_16x16x32_bf16 v[38:41], v[148:151], v[212:215], v[38:41]
	v_mfma_f32_16x16x32_bf16 v[34:37], v[156:159], v[212:215], v[34:37]
	v_mfma_f32_16x16x32_bf16 v[22:25], v[148:151], v[220:223], v[22:25]
	v_mfma_f32_16x16x32_bf16 v[18:21], v[156:159], v[220:223], v[18:21]
	s_setprio 0
	s_setprio 1
	v_mfma_f32_16x16x32_bf16 v[46:49], v[160:163], v[176:179], v[46:49]
	v_mfma_f32_16x16x32_bf16 v[42:45], v[168:171], v[176:179], v[42:45]
	v_mfma_f32_16x16x32_bf16 v[30:33], v[160:163], v[200:203], v[30:33]
	v_mfma_f32_16x16x32_bf16 v[26:29], v[168:171], v[200:203], v[26:29]
	v_mfma_f32_16x16x32_bf16 v[14:17], v[160:163], v[208:211], v[14:17]
	v_mfma_f32_16x16x32_bf16 v[10:13], v[168:171], v[208:211], v[10:13]
	v_mfma_f32_16x16x32_bf16 v[6:9], v[160:163], v[216:219], v[6:9]
	v_mfma_f32_16x16x32_bf16 v[2:5], v[168:171], v[216:219], v[2:5]
	v_mfma_f32_16x16x32_bf16 v[46:49], v[164:167], v[180:183], v[46:49]
	v_mfma_f32_16x16x32_bf16 v[42:45], v[172:175], v[180:183], v[42:45]
	v_mfma_f32_16x16x32_bf16 v[30:33], v[164:167], v[204:207], v[30:33]
	v_mfma_f32_16x16x32_bf16 v[26:29], v[172:175], v[204:207], v[26:29]
	v_mfma_f32_16x16x32_bf16 v[14:17], v[164:167], v[212:215], v[14:17]
	v_mfma_f32_16x16x32_bf16 v[10:13], v[172:175], v[212:215], v[10:13]
	v_mfma_f32_16x16x32_bf16 v[6:9], v[164:167], v[220:223], v[6:9]
	v_mfma_f32_16x16x32_bf16 v[2:5], v[172:175], v[220:223], v[2:5]
	s_setprio 0
	s_barrier
	s_add_i32 s56, s56, 2
	s_add_u32 s54, s54, 0x100
	s_addc_u32 s55, s55, 0
	s_cmp_gt_u32 s56, 53
	s_mov_b64 s[16:17], s[18:19]
	s_cbranch_scc1 .Lkpeel_exit_6

; #define PG8_BAR __builtin_amdgcn_s_barrier()
; template <class Epi, class Sched>
; __device__ __forceinline__ void gemm_phase(LAS unsigned char* lds, const Gemm g, const Sched& S, const Epi& E, const int tid, unsigned* last_sig = nullptr) {
;     ...
;         if (wr == 0) PG8_BAR;
.Lkpeel_exit_6:
	s_and_b64 vcc, exec, s[10:11]
	s_cbranch_vccz .LBB0_1265
	s_barrier

; #define PG8_STAGE(bufoff, gbase, voff) do { _Pragma("unroll") for (int _i = 0; _i < 2; ++_i) \
;         __builtin_amdgcn_global_load_lds((const unsigned*)((const char*)(gbase) + (voff)[_i]), (LAS unsigned*)(lds + (bufoff) + ldsw + _i * 8192), 16, 0, 0); } while (0)
; #define PG8_LDA(dst, b, h) do { _Pragma("unroll") for (int m = 0; m < 4; ++m) _Pragma("unroll") for (int k = 0; k < 2; ++k) dst[m][k] = *(const LAS bf16x8*)(lds + PG8_SA(b, h) + aoff + m * 2048 + k * 1024); } while (0)
; #define PG8_LDB(dst, b, h) do { _Pragma("unroll") for (int n = 0; n < 2; ++n) _Pragma("unroll") for (int k = 0; k < 2; ++k) dst[n][k] = *(const LAS bf16x8*)(lds + PG8_SB(b, h) + boff + n * 2048 + k * 1024); } while (0)
; #define PG8_MMA(ai, bj, At, Bt) do { __builtin_amdgcn_s_setprio(1); _Pragma("unroll") for (int m = 0; m < 4; ++m) _Pragma("unroll") for (int n = 0; n < 2; ++n) _Pragma("unroll") for (int k = 0; k < 2; ++k) \
;         acc[ai][bj][m][n] = __builtin_amdgcn_mfma_f32_16x16x32_bf16(Bt[n][k], At[m][k], acc[ai][bj][m][n], 0, 0, 0); __builtin_amdgcn_s_setprio(0); } while (0)
; #define PG8_WAIT_V(n) asm volatile("s_waitcnt vmcnt(" #n ")" ::: "memory")
; #define PG8_WAIT_L(n) asm volatile("s_waitcnt lgkmcnt(" #n ")" ::: "memory")
; template <class Epi, class Sched>
; __device__ __forceinline__ void gemm_phase(LAS unsigned char* lds, const Gemm g, const Sched& S, const Epi& E, const int tid, unsigned* last_sig = nullptr) {
;     ...
;         for (int t = 0; t < nt; t += 2) {
;             const bool last = (t == nt - 2);
;             const char* a1 = cA + (size_t)(t + 1) * kstep;
;             const char* a2 = last ? nA : cA + (size_t)(t + 2) * kstep; const char* b2 = last ? nB : cB + (size_t)(t + 2) * kstep;
;             const char* a3 = a2 + kstep; const char* b3 = b2 + kstep;
;             PG8_LDB(B0, 0, 0); PG8_LDB(B1, 0, 1); PG8_SCHED; PG8_LDA(At, 0, 0); PG8_STAGE(PG8_SA(1, 1), a1 + hstep, voffA);
;             PG8_WAIT_V(8); PG8_WAIT_L(0); PG8_BAR; PG8_MMA(0, 0, At, B0); PG8_MMA(0, 1, At, B1); PG8_BAR; PG8_SCHED;
;     ...
; #pragma unroll
;         for (int a = 0; a < 2; ++a)
; #pragma unroll
;             for (int b = 0; b < 2; ++b)
; #pragma unroll
;                 for (int m = 0; m < 4; ++m)
; #pragma unroll
;                     for (int n = 0; n < 2; ++n) acc[a][b][m][n] = (f32x4){0.f, 0.f, 0.f, 0.f};
;         cur = nxt; cA = nA; cB = nB; ++ui;
.LBB0_1287:
	s_add_u32 s48, s16, 0x100
	v_mov_b32_e32 v2, 0
	s_addc_u32 s49, s17, 0
	s_mov_b32 s50, -2
	v_mov_b32_e32 v3, v2
	v_mov_b32_e32 v4, v2
	v_mov_b32_e32 v5, v2
	v_mov_b32_e32 v6, v2
	v_mov_b32_e32 v7, v2
	v_mov_b32_e32 v8, v2
	v_mov_b32_e32 v9, v2
	v_mov_b32_e32 v10, v2
	v_mov_b32_e32 v11, v2
	v_mov_b32_e32 v12, v2
	v_mov_b32_e32 v13, v2
	v_mov_b32_e32 v18, v2
	v_mov_b32_e32 v19, v2
	v_mov_b32_e32 v20, v2
	v_mov_b32_e32 v21, v2
	v_mov_b32_e32 v26, v2
	v_mov_b32_e32 v27, v2
	v_mov_b32_e32 v28, v2
	v_mov_b32_e32 v29, v2
	v_mov_b32_e32 v34, v2
	v_mov_b32_e32 v35, v2
	v_mov_b32_e32 v36, v2
	v_mov_b32_e32 v37, v2
	v_mov_b32_e32 v42, v2
	v_mov_b32_e32 v43, v2
	v_mov_b32_e32 v44, v2
	v_mov_b32_e32 v45, v2
	v_mov_b32_e32 v50, v2
	v_mov_b32_e32 v51, v2
	v_mov_b32_e32 v52, v2
	v_mov_b32_e32 v53, v2
	v_mov_b32_e32 v14, v2
	v_mov_b32_e32 v15, v2
	v_mov_b32_e32 v16, v2
	v_mov_b32_e32 v17, v2
	v_mov_b32_e32 v22, v2
	v_mov_b32_e32 v23, v2
	v_mov_b32_e32 v24, v2
	v_mov_b32_e32 v25, v2
	v_mov_b32_e32 v30, v2
	v_mov_b32_e32 v31, v2
	v_mov_b32_e32 v32, v2
	v_mov_b32_e32 v33, v2
	v_mov_b32_e32 v38, v2
	v_mov_b32_e32 v39, v2
	v_mov_b32_e32 v40, v2
	v_mov_b32_e32 v41, v2
	v_mov_b32_e32 v46, v2
	v_mov_b32_e32 v47, v2
	v_mov_b32_e32 v48, v2
	v_mov_b32_e32 v49, v2
	v_mov_b32_e32 v54, v2
	v_mov_b32_e32 v55, v2
	v_mov_b32_e32 v56, v2
	v_mov_b32_e32 v57, v2
	v_mov_b32_e32 v58, v2
	v_mov_b32_e32 v59, v2
	v_mov_b32_e32 v60, v2
	v_mov_b32_e32 v61, v2
	v_mov_b32_e32 v62, v2
	v_mov_b32_e32 v63, v2
	v_mov_b32_e32 v64, v2
	v_mov_b32_e32 v65, v2
	v_mov_b32_e32 v66, v2
	v_mov_b32_e32 v67, v2
	v_mov_b32_e32 v68, v2
	v_mov_b32_e32 v69, v2
	v_mov_b32_e32 v70, v2
	v_mov_b32_e32 v71, v2
	v_mov_b32_e32 v72, v2
	v_mov_b32_e32 v73, v2
	v_mov_b32_e32 v74, v2
	v_mov_b32_e32 v75, v2
	v_mov_b32_e32 v76, v2
	v_mov_b32_e32 v77, v2
	v_mov_b32_e32 v78, v2
	v_mov_b32_e32 v79, v2
	v_mov_b32_e32 v80, v2
	v_mov_b32_e32 v81, v2
	v_mov_b32_e32 v86, v2
	v_mov_b32_e32 v87, v2
	v_mov_b32_e32 v88, v2
	v_mov_b32_e32 v89, v2
	v_mov_b32_e32 v94, v2
	v_mov_b32_e32 v95, v2
	v_mov_b32_e32 v96, v2
	v_mov_b32_e32 v97, v2
	v_mov_b32_e32 v102, v2
	v_mov_b32_e32 v103, v2
	v_mov_b32_e32 v104, v2
	v_mov_b32_e32 v105, v2
	v_mov_b32_e32 v110, v2
	v_mov_b32_e32 v111, v2
	v_mov_b32_e32 v112, v2
	v_mov_b32_e32 v113, v2
	v_mov_b32_e32 v82, v2
	v_mov_b32_e32 v83, v2
	v_mov_b32_e32 v84, v2
	v_mov_b32_e32 v85, v2
	v_mov_b32_e32 v90, v2
	v_mov_b32_e32 v91, v2
	v_mov_b32_e32 v92, v2
	v_mov_b32_e32 v93, v2
	v_mov_b32_e32 v98, v2
	v_mov_b32_e32 v99, v2
	v_mov_b32_e32 v100, v2
	v_mov_b32_e32 v101, v2
	v_mov_b32_e32 v106, v2
	v_mov_b32_e32 v107, v2
	v_mov_b32_e32 v108, v2
	v_mov_b32_e32 v109, v2
	v_mov_b32_e32 v114, v2
	v_mov_b32_e32 v115, v2
	v_mov_b32_e32 v116, v2
	v_mov_b32_e32 v117, v2
	v_mov_b32_e32 v118, v2
	v_mov_b32_e32 v119, v2
	v_mov_b32_e32 v120, v2
	v_mov_b32_e32 v121, v2
	v_mov_b32_e32 v122, v2
	v_mov_b32_e32 v123, v2
	v_mov_b32_e32 v124, v2
	v_mov_b32_e32 v125, v2
	v_mov_b32_e32 v126, v2
	v_mov_b32_e32 v127, v2
	v_mov_b32_e32 v128, v2
	v_mov_b32_e32 v129, v2
	s_cmp_eq_u32 s43, 1
	s_cbranch_scc1 .LBB0_1288
	s_add_u32 s16, s12, 0x100
	s_addc_u32 s17, s13, 0
	s_add_i32 s14, 0, 0x10000
	s_cmpk_eq_i32 s50, 0x54
	s_cselect_b32 s21, s5, s17
	s_cselect_b32 s20, s4, s16
	v_add_u32_e32 v151, s14, v148
	s_cselect_b32 s19, s11, s49
	s_cselect_b32 s18, s10, s48
	s_add_i32 s15, 0, 0x14000
	ds_read_b128 v[136:139], v151
	ds_read_b128 v[140:143], v151 offset:1024
	ds_read_b128 v[144:147], v151 offset:2048
	ds_read_b128 v[152:155], v151 offset:3072
	v_add_u32_e32 v151, s15, v148
	ds_read_b128 v[156:159], v151
	ds_read_b128 v[160:163], v151 offset:1024
	ds_read_b128 v[164:167], v151 offset:2048
	ds_read_b128 v[168:171], v151 offset:3072
	v_lshl_add_u64 v[184:185], s[12:13], 0, v[132:133]
	s_add_i32 m0, s23, 0xc000
	ds_read_b128 v[172:175], v150
	ds_read_b128 v[176:179], v150 offset:1024
	ds_read_b128 v[180:183], v150 offset:2048
	ds_read_b128 v[200:203], v150 offset:3072
	ds_read_b128 v[204:207], v150 offset:4096
	ds_read_b128 v[208:211], v150 offset:5120
	ds_read_b128 v[212:215], v150 offset:6144
	ds_read_b128 v[216:219], v150 offset:7168
	global_load_lds_dwordx4 v[184:185], off
	v_lshl_add_u64 v[184:185], s[12:13], 0, v[134:135]
	s_add_i32 m0, s23, 0xe000
	s_nop 0
	global_load_lds_dwordx4 v[184:185], off
	s_waitcnt vmcnt(24)
	s_waitcnt lgkmcnt(0)
	s_barrier
	s_setprio 1
	s_waitcnt lgkmcnt(0)
	v_mfma_f32_16x16x32_bf16 v[126:129], v[136:139], v[172:175], v[126:129]
	v_mfma_f32_16x16x32_bf16 v[122:125], v[144:147], v[172:175], v[122:125]
	v_mfma_f32_16x16x32_bf16 v[118:121], v[136:139], v[180:183], v[118:121]
	v_mfma_f32_16x16x32_bf16 v[114:117], v[144:147], v[180:183], v[114:117]
	v_mfma_f32_16x16x32_bf16 v[106:109], v[136:139], v[204:207], v[106:109]
	v_mfma_f32_16x16x32_bf16 v[98:101], v[144:147], v[204:207], v[98:101]
	v_mfma_f32_16x16x32_bf16 v[90:93], v[136:139], v[212:215], v[90:93]
	v_mfma_f32_16x16x32_bf16 v[82:85], v[144:147], v[212:215], v[82:85]
	v_mfma_f32_16x16x32_bf16 v[126:129], v[140:143], v[176:179], v[126:129]
	v_mfma_f32_16x16x32_bf16 v[122:125], v[152:155], v[176:179], v[122:125]
	v_mfma_f32_16x16x32_bf16 v[118:121], v[140:143], v[200:203], v[118:121]
	v_mfma_f32_16x16x32_bf16 v[114:117], v[152:155], v[200:203], v[114:117]
	v_mfma_f32_16x16x32_bf16 v[106:109], v[140:143], v[208:211], v[106:109]
	v_mfma_f32_16x16x32_bf16 v[98:101], v[152:155], v[208:211], v[98:101]
	v_mfma_f32_16x16x32_bf16 v[90:93], v[140:143], v[216:219], v[90:93]
	v_mfma_f32_16x16x32_bf16 v[82:85], v[152:155], v[216:219], v[82:85]
	s_setprio 0
	s_setprio 1
	v_mfma_f32_16x16x32_bf16 v[110:113], v[156:159], v[172:175], v[110:113]
	v_mfma_f32_16x16x32_bf16 v[102:105], v[164:167], v[172:175], v[102:105]
	v_mfma_f32_16x16x32_bf16 v[94:97], v[156:159], v[180:183], v[94:97]
	v_mfma_f32_16x16x32_bf16 v[86:89], v[164:167], v[180:183], v[86:89]
	v_mfma_f32_16x16x32_bf16 v[78:81], v[156:159], v[204:207], v[78:81]
	v_mfma_f32_16x16x32_bf16 v[74:77], v[164:167], v[204:207], v[74:77]
	v_mfma_f32_16x16x32_bf16 v[70:73], v[156:159], v[212:215], v[70:73]
	v_mfma_f32_16x16x32_bf16 v[66:69], v[164:167], v[212:215], v[66:69]
	v_mfma_f32_16x16x32_bf16 v[110:113], v[160:163], v[176:179], v[110:113]
	v_mfma_f32_16x16x32_bf16 v[102:105], v[168:171], v[176:179], v[102:105]
	v_mfma_f32_16x16x32_bf16 v[94:97], v[160:163], v[200:203], v[94:97]
	v_mfma_f32_16x16x32_bf16 v[86:89], v[168:171], v[200:203], v[86:89]
	v_mfma_f32_16x16x32_bf16 v[78:81], v[160:163], v[208:211], v[78:81]
	v_mfma_f32_16x16x32_bf16 v[74:77], v[168:171], v[208:211], v[74:77]
	v_mfma_f32_16x16x32_bf16 v[70:73], v[160:163], v[216:219], v[70:73]
	v_mfma_f32_16x16x32_bf16 v[66:69], v[168:171], v[216:219], v[66:69]
	s_setprio 0
	s_barrier
; #define PG8_STAGE(bufoff, gbase, voff) do { _Pragma("unroll") for (int _i = 0; _i < 2; ++_i) \
;         __builtin_amdgcn_global_load_lds((const unsigned*)((const char*)(gbase) + (voff)[_i]), (LAS unsigned*)(lds + (bufoff) + ldsw + _i * 8192), 16, 0, 0); } while (0)
; #define PG8_LDA(dst, b, h) do { _Pragma("unroll") for (int m = 0; m < 4; ++m) _Pragma("unroll") for (int k = 0; k < 2; ++k) dst[m][k] = *(const LAS bf16x8*)(lds + PG8_SA(b, h) + aoff + m * 2048 + k * 1024); } while (0)
; #define PG8_LDB(dst, b, h) do { _Pragma("unroll") for (int n = 0; n < 2; ++n) _Pragma("unroll") for (int k = 0; k < 2; ++k) dst[n][k] = *(const LAS bf16x8*)(lds + PG8_SB(b, h) + boff + n * 2048 + k * 1024); } while (0)
; #define PG8_MMA(ai, bj, At, Bt) do { __builtin_amdgcn_s_setprio(1); _Pragma("unroll") for (int m = 0; m < 4; ++m) _Pragma("unroll") for (int n = 0; n < 2; ++n) _Pragma("unroll") for (int k = 0; k < 2; ++k) \
;         acc[ai][bj][m][n] = __builtin_amdgcn_mfma_f32_16x16x32_bf16(Bt[n][k], At[m][k], acc[ai][bj][m][n], 0, 0, 0); __builtin_amdgcn_s_setprio(0); } while (0)
; #define PG8_WAIT_V(n) asm volatile("s_waitcnt vmcnt(" #n ")" ::: "memory")
; #define PG8_WAIT_L(n) asm volatile("s_waitcnt lgkmcnt(" #n ")" ::: "memory")
; #define PG8_BAR __builtin_amdgcn_s_barrier()
; #define PG8_SCHED __builtin_amdgcn_sched_barrier(0)
; template <class Epi, class Sched>
; __device__ __forceinline__ void gemm_phase(LAS unsigned char* lds, const Gemm g, const Sched& S, const Epi& E, const int tid, unsigned* last_sig = nullptr) {
;     ...
;             PG8_LDA(At, 0, 1); PG8_STAGE(PG8_SB(0, 0), b2, voffB); PG8_STAGE(PG8_SB(0, 1), b2 + hstep, voffB); PG8_STAGE(PG8_SA(0, 0), a2, voffA);
;             PG8_WAIT_V(8); PG8_WAIT_L(0); PG8_BAR; PG8_MMA(1, 0, At, B0); PG8_MMA(1, 1, At, B1); PG8_BAR; PG8_SCHED;
;             PG8_LDB(B0, 1, 0); PG8_LDB(B1, 1, 1); PG8_SCHED; PG8_LDA(At, 1, 0); PG8_STAGE(PG8_SA(0, 1), a2 + hstep, voffA);
;             PG8_WAIT_V(8); PG8_WAIT_L(0); PG8_BAR; PG8_MMA(0, 0, At, B0); PG8_MMA(0, 1, At, B1); PG8_BAR; PG8_SCHED;
	s_add_i32 s12, s14, s22
	v_lshl_add_u64 v[184:185], s[18:19], 0, v[186:187]
	s_mov_b32 m0, s12
	ds_read_b128 v[172:175], v150 offset:16384
	ds_read_b128 v[176:179], v150 offset:17408
	ds_read_b128 v[180:183], v150 offset:18432
	ds_read_b128 v[200:203], v150 offset:19456
	ds_read_b128 v[204:207], v150 offset:20480
	ds_read_b128 v[208:211], v150 offset:21504
	ds_read_b128 v[212:215], v150 offset:22528
	ds_read_b128 v[216:219], v150 offset:23552
	global_load_lds_dwordx4 v[184:185], off
	s_add_i32 m0, s12, 0x2000
	s_add_u32 s12, s18, 0x160000
	v_lshl_add_u64 v[220:221], s[18:19], 0, v[130:131]
	s_addc_u32 s13, s19, 0
	s_add_i32 s14, s15, s22
	global_load_lds_dwordx4 v[220:221], off
	v_lshl_add_u64 v[222:223], s[12:13], 0, v[186:187]
	s_mov_b32 m0, s14
	v_lshl_add_u64 v[232:233], s[20:21], 0, v[130:131]
	global_load_lds_dwordx4 v[222:223], off
	v_lshl_add_u64 v[222:223], s[12:13], 0, v[130:131]
	s_add_i32 m0, s14, 0x2000
	s_nop 0
	global_load_lds_dwordx4 v[222:223], off
	v_lshl_add_u64 v[222:223], s[20:21], 0, v[186:187]
	s_mov_b32 m0, s23
	s_nop 0
	global_load_lds_dwordx4 v[222:223], off
	s_mov_b32 m0, s28
	s_nop 0
	global_load_lds_dwordx4 v[232:233], off
	s_waitcnt vmcnt(24)
	s_waitcnt lgkmcnt(0)
	s_barrier
	s_setprio 1
	s_waitcnt lgkmcnt(0)
	v_mfma_f32_16x16x32_bf16 v[62:65], v[136:139], v[172:175], v[62:65]
	v_mfma_f32_16x16x32_bf16 v[58:61], v[144:147], v[172:175], v[58:61]
	v_mfma_f32_16x16x32_bf16 v[54:57], v[136:139], v[180:183], v[54:57]
	v_mfma_f32_16x16x32_bf16 v[46:49], v[144:147], v[180:183], v[46:49]
	v_mfma_f32_16x16x32_bf16 v[38:41], v[136:139], v[204:207], v[38:41]
	v_mfma_f32_16x16x32_bf16 v[30:33], v[144:147], v[204:207], v[30:33]
	v_mfma_f32_16x16x32_bf16 v[22:25], v[136:139], v[212:215], v[22:25]
	v_mfma_f32_16x16x32_bf16 v[14:17], v[144:147], v[212:215], v[14:17]
	v_mfma_f32_16x16x32_bf16 v[62:65], v[140:143], v[176:179], v[62:65]
	v_mfma_f32_16x16x32_bf16 v[58:61], v[152:155], v[176:179], v[58:61]
	v_mfma_f32_16x16x32_bf16 v[54:57], v[140:143], v[200:203], v[54:57]
	v_mfma_f32_16x16x32_bf16 v[46:49], v[152:155], v[200:203], v[46:49]
	v_mfma_f32_16x16x32_bf16 v[38:41], v[140:143], v[208:211], v[38:41]
	v_mfma_f32_16x16x32_bf16 v[30:33], v[152:155], v[208:211], v[30:33]
	v_mfma_f32_16x16x32_bf16 v[22:25], v[140:143], v[216:219], v[22:25]
	v_mfma_f32_16x16x32_bf16 v[14:17], v[152:155], v[216:219], v[14:17]
	s_setprio 0
	s_setprio 1
	v_mfma_f32_16x16x32_bf16 v[50:53], v[156:159], v[172:175], v[50:53]
	v_mfma_f32_16x16x32_bf16 v[42:45], v[164:167], v[172:175], v[42:45]
	v_mfma_f32_16x16x32_bf16 v[34:37], v[156:159], v[180:183], v[34:37]
	v_mfma_f32_16x16x32_bf16 v[26:29], v[164:167], v[180:183], v[26:29]
	v_mfma_f32_16x16x32_bf16 v[18:21], v[156:159], v[204:207], v[18:21]
	v_mfma_f32_16x16x32_bf16 v[10:13], v[164:167], v[204:207], v[10:13]
	v_mfma_f32_16x16x32_bf16 v[6:9], v[156:159], v[212:215], v[6:9]
	v_mfma_f32_16x16x32_bf16 v[2:5], v[164:167], v[212:215], v[2:5]
	v_mfma_f32_16x16x32_bf16 v[50:53], v[160:163], v[176:179], v[50:53]
	v_mfma_f32_16x16x32_bf16 v[42:45], v[168:171], v[176:179], v[42:45]
	v_mfma_f32_16x16x32_bf16 v[34:37], v[160:163], v[200:203], v[34:37]
	v_mfma_f32_16x16x32_bf16 v[26:29], v[168:171], v[200:203], v[26:29]
	v_mfma_f32_16x16x32_bf16 v[18:21], v[160:163], v[208:211], v[18:21]
	v_mfma_f32_16x16x32_bf16 v[10:13], v[168:171], v[208:211], v[10:13]
	v_mfma_f32_16x16x32_bf16 v[6:9], v[160:163], v[216:219], v[6:9]
	v_mfma_f32_16x16x32_bf16 v[2:5], v[168:171], v[216:219], v[2:5]
	s_setprio 0
	s_barrier
	s_add_i32 s14, 0, 0x18000
	v_add_u32_e32 v151, s14, v148
	s_add_i32 s15, 0, 0x1c000
	ds_read_b128 v[136:139], v151
	ds_read_b128 v[140:143], v151 offset:1024
	ds_read_b128 v[144:147], v151 offset:2048
	ds_read_b128 v[152:155], v151 offset:3072
	v_add_u32_e32 v151, s15, v148
	ds_read_b128 v[156:159], v151
	ds_read_b128 v[160:163], v151 offset:1024
	ds_read_b128 v[164:167], v151 offset:2048
	ds_read_b128 v[168:171], v151 offset:3072
	s_add_u32 s12, s20, 0x160000
	s_addc_u32 s13, s21, 0
	s_mov_b32 m0, s31
	v_lshl_add_u64 v[234:235], s[12:13], 0, v[186:187]
	ds_read_b128 v[172:175], v150 offset:32768
	ds_read_b128 v[176:179], v150 offset:33792
	ds_read_b128 v[180:183], v150 offset:34816
	ds_read_b128 v[200:203], v150 offset:35840
	ds_read_b128 v[204:207], v150 offset:36864
	ds_read_b128 v[208:211], v150 offset:37888
	ds_read_b128 v[212:215], v150 offset:38912
	ds_read_b128 v[216:219], v150 offset:39936
	global_load_lds_dwordx4 v[234:235], off
	v_lshl_add_u64 v[234:235], s[12:13], 0, v[130:131]
	s_mov_b32 m0, s40
	s_nop 0
	global_load_lds_dwordx4 v[234:235], off
	s_waitcnt vmcnt(8)
	s_waitcnt lgkmcnt(0)
	s_barrier
; #define PG8_STAGE(bufoff, gbase, voff) do { _Pragma("unroll") for (int _i = 0; _i < 2; ++_i) \
;         __builtin_amdgcn_global_load_lds((const unsigned*)((const char*)(gbase) + (voff)[_i]), (LAS unsigned*)(lds + (bufoff) + ldsw + _i * 8192), 16, 0, 0); } while (0)
; #define PG8_LDA(dst, b, h) do { _Pragma("unroll") for (int m = 0; m < 4; ++m) _Pragma("unroll") for (int k = 0; k < 2; ++k) dst[m][k] = *(const LAS bf16x8*)(lds + PG8_SA(b, h) + aoff + m * 2048 + k * 1024); } while (0)
; #define PG8_MMA(ai, bj, At, Bt) do { __builtin_amdgcn_s_setprio(1); _Pragma("unroll") for (int m = 0; m < 4; ++m) _Pragma("unroll") for (int n = 0; n < 2; ++n) _Pragma("unroll") for (int k = 0; k < 2; ++k) \
;         acc[ai][bj][m][n] = __builtin_amdgcn_mfma_f32_16x16x32_bf16(Bt[n][k], At[m][k], acc[ai][bj][m][n], 0, 0, 0); __builtin_amdgcn_s_setprio(0); } while (0)
; #define PG8_WAIT_V(n) asm volatile("s_waitcnt vmcnt(" #n ")" ::: "memory")
; #define PG8_WAIT_L(n) asm volatile("s_waitcnt lgkmcnt(" #n ")" ::: "memory")
; #define PG8_BAR __builtin_amdgcn_s_barrier()
; #define PG8_SCHED __builtin_amdgcn_sched_barrier(0)
; template <class Epi, class Sched>
; __device__ __forceinline__ void gemm_phase(LAS unsigned char* lds, const Gemm g, const Sched& S, const Epi& E, const int tid, unsigned* last_sig = nullptr) {
;     ...
;             PG8_WAIT_V(8); PG8_WAIT_L(0); PG8_BAR; PG8_MMA(0, 0, At, B0); PG8_MMA(0, 1, At, B1); PG8_BAR; PG8_SCHED;
;             PG8_LDA(At, 1, 1); PG8_STAGE(PG8_SB(1, 0), b3, voffB); PG8_STAGE(PG8_SB(1, 1), b3 + hstep, voffB); PG8_STAGE(PG8_SA(1, 0), a3, voffA);
;             PG8_WAIT_V(8); PG8_WAIT_L(0); PG8_BAR; PG8_MMA(1, 0, At, B0); PG8_MMA(1, 1, At, B1); PG8_BAR; PG8_SCHED;
;         }
	s_setprio 1
	s_waitcnt lgkmcnt(0)
	v_mfma_f32_16x16x32_bf16 v[126:129], v[136:139], v[172:175], v[126:129]
	v_mfma_f32_16x16x32_bf16 v[122:125], v[144:147], v[172:175], v[122:125]
	v_mfma_f32_16x16x32_bf16 v[118:121], v[136:139], v[180:183], v[118:121]
	v_mfma_f32_16x16x32_bf16 v[114:117], v[144:147], v[180:183], v[114:117]
	v_mfma_f32_16x16x32_bf16 v[106:109], v[136:139], v[204:207], v[106:109]
	v_mfma_f32_16x16x32_bf16 v[98:101], v[144:147], v[204:207], v[98:101]
	v_mfma_f32_16x16x32_bf16 v[90:93], v[136:139], v[212:215], v[90:93]
	v_mfma_f32_16x16x32_bf16 v[82:85], v[144:147], v[212:215], v[82:85]
	v_mfma_f32_16x16x32_bf16 v[126:129], v[140:143], v[176:179], v[126:129]
	v_mfma_f32_16x16x32_bf16 v[122:125], v[152:155], v[176:179], v[122:125]
	v_mfma_f32_16x16x32_bf16 v[118:121], v[140:143], v[200:203], v[118:121]
	v_mfma_f32_16x16x32_bf16 v[114:117], v[152:155], v[200:203], v[114:117]
	v_mfma_f32_16x16x32_bf16 v[106:109], v[140:143], v[208:211], v[106:109]
	v_mfma_f32_16x16x32_bf16 v[98:101], v[152:155], v[208:211], v[98:101]
	v_mfma_f32_16x16x32_bf16 v[90:93], v[140:143], v[216:219], v[90:93]
	v_mfma_f32_16x16x32_bf16 v[82:85], v[152:155], v[216:219], v[82:85]
	s_setprio 0
	s_setprio 1
	v_mfma_f32_16x16x32_bf16 v[110:113], v[156:159], v[172:175], v[110:113]
	v_mfma_f32_16x16x32_bf16 v[102:105], v[164:167], v[172:175], v[102:105]
	v_mfma_f32_16x16x32_bf16 v[94:97], v[156:159], v[180:183], v[94:97]
	v_mfma_f32_16x16x32_bf16 v[86:89], v[164:167], v[180:183], v[86:89]
	v_mfma_f32_16x16x32_bf16 v[78:81], v[156:159], v[204:207], v[78:81]
	v_mfma_f32_16x16x32_bf16 v[74:77], v[164:167], v[204:207], v[74:77]
	v_mfma_f32_16x16x32_bf16 v[70:73], v[156:159], v[212:215], v[70:73]
	v_mfma_f32_16x16x32_bf16 v[66:69], v[164:167], v[212:215], v[66:69]
	v_mfma_f32_16x16x32_bf16 v[110:113], v[160:163], v[176:179], v[110:113]
	v_mfma_f32_16x16x32_bf16 v[102:105], v[168:171], v[176:179], v[102:105]
	v_mfma_f32_16x16x32_bf16 v[94:97], v[160:163], v[200:203], v[94:97]
	v_mfma_f32_16x16x32_bf16 v[86:89], v[168:171], v[200:203], v[86:89]
	v_mfma_f32_16x16x32_bf16 v[78:81], v[160:163], v[208:211], v[78:81]
	v_mfma_f32_16x16x32_bf16 v[74:77], v[168:171], v[208:211], v[74:77]
	v_mfma_f32_16x16x32_bf16 v[70:73], v[160:163], v[216:219], v[70:73]
	v_mfma_f32_16x16x32_bf16 v[66:69], v[168:171], v[216:219], v[66:69]
	s_setprio 0
	s_barrier
	s_add_i32 s12, s14, s22
	v_lshl_add_u64 v[184:185], v[184:185], 0, s[34:35]
	s_mov_b32 m0, s12
	ds_read_b128 v[172:175], v150 offset:49152
	ds_read_b128 v[176:179], v150 offset:50176
	ds_read_b128 v[180:183], v150 offset:51200
	ds_read_b128 v[200:203], v150 offset:52224
	ds_read_b128 v[204:207], v150 offset:53248
	ds_read_b128 v[208:211], v150 offset:54272
	ds_read_b128 v[212:215], v150 offset:55296
	ds_read_b128 v[216:219], v150 offset:56320
	global_load_lds_dwordx4 v[184:185], off
	s_add_i32 m0, s12, 0x2000
	s_add_u32 s12, s18, 0x160080
	v_lshl_add_u64 v[184:185], v[220:221], 0, s[34:35]
	s_addc_u32 s13, s19, 0
	s_add_i32 s14, s15, s22
	global_load_lds_dwordx4 v[184:185], off
	v_lshl_add_u64 v[184:185], s[12:13], 0, v[186:187]
	s_mov_b32 m0, s14
	s_nop 0
	global_load_lds_dwordx4 v[184:185], off
	v_lshl_add_u64 v[184:185], s[12:13], 0, v[130:131]
	s_add_i32 m0, s14, 0x2000
	s_nop 0
	global_load_lds_dwordx4 v[184:185], off
	v_lshl_add_u64 v[184:185], v[222:223], 0, s[34:35]
	s_mov_b32 m0, s41
	s_nop 0
	global_load_lds_dwordx4 v[184:185], off
	v_lshl_add_u64 v[184:185], v[232:233], 0, s[34:35]
	s_mov_b32 m0, s42
	s_nop 0
	global_load_lds_dwordx4 v[184:185], off
	s_waitcnt vmcnt(8)
	s_waitcnt lgkmcnt(0)
	s_barrier
	s_setprio 1
	s_waitcnt lgkmcnt(0)
	v_mfma_f32_16x16x32_bf16 v[62:65], v[136:139], v[172:175], v[62:65]
	v_mfma_f32_16x16x32_bf16 v[58:61], v[144:147], v[172:175], v[58:61]
	v_mfma_f32_16x16x32_bf16 v[54:57], v[136:139], v[180:183], v[54:57]
	v_mfma_f32_16x16x32_bf16 v[46:49], v[144:147], v[180:183], v[46:49]
	v_mfma_f32_16x16x32_bf16 v[38:41], v[136:139], v[204:207], v[38:41]
	v_mfma_f32_16x16x32_bf16 v[30:33], v[144:147], v[204:207], v[30:33]
	v_mfma_f32_16x16x32_bf16 v[22:25], v[136:139], v[212:215], v[22:25]
	v_mfma_f32_16x16x32_bf16 v[14:17], v[144:147], v[212:215], v[14:17]
	v_mfma_f32_16x16x32_bf16 v[62:65], v[140:143], v[176:179], v[62:65]
	v_mfma_f32_16x16x32_bf16 v[58:61], v[152:155], v[176:179], v[58:61]
	v_mfma_f32_16x16x32_bf16 v[54:57], v[140:143], v[200:203], v[54:57]
	v_mfma_f32_16x16x32_bf16 v[46:49], v[152:155], v[200:203], v[46:49]
	v_mfma_f32_16x16x32_bf16 v[38:41], v[140:143], v[208:211], v[38:41]
	v_mfma_f32_16x16x32_bf16 v[30:33], v[152:155], v[208:211], v[30:33]
	v_mfma_f32_16x16x32_bf16 v[22:25], v[140:143], v[216:219], v[22:25]
	v_mfma_f32_16x16x32_bf16 v[14:17], v[152:155], v[216:219], v[14:17]
	s_setprio 0
	s_setprio 1
	v_mfma_f32_16x16x32_bf16 v[50:53], v[156:159], v[172:175], v[50:53]
	v_mfma_f32_16x16x32_bf16 v[42:45], v[164:167], v[172:175], v[42:45]
	v_mfma_f32_16x16x32_bf16 v[34:37], v[156:159], v[180:183], v[34:37]
	v_mfma_f32_16x16x32_bf16 v[26:29], v[164:167], v[180:183], v[26:29]
	v_mfma_f32_16x16x32_bf16 v[18:21], v[156:159], v[204:207], v[18:21]
	v_mfma_f32_16x16x32_bf16 v[10:13], v[164:167], v[204:207], v[10:13]
	v_mfma_f32_16x16x32_bf16 v[6:9], v[156:159], v[212:215], v[6:9]
	v_mfma_f32_16x16x32_bf16 v[2:5], v[164:167], v[212:215], v[2:5]
	v_mfma_f32_16x16x32_bf16 v[50:53], v[160:163], v[176:179], v[50:53]
	v_mfma_f32_16x16x32_bf16 v[42:45], v[168:171], v[176:179], v[42:45]
	v_mfma_f32_16x16x32_bf16 v[34:37], v[160:163], v[200:203], v[34:37]
	v_mfma_f32_16x16x32_bf16 v[26:29], v[168:171], v[200:203], v[26:29]
	v_mfma_f32_16x16x32_bf16 v[18:21], v[160:163], v[208:211], v[18:21]
	v_mfma_f32_16x16x32_bf16 v[10:13], v[168:171], v[208:211], v[10:13]
	v_mfma_f32_16x16x32_bf16 v[6:9], v[160:163], v[216:219], v[6:9]
	v_mfma_f32_16x16x32_bf16 v[2:5], v[168:171], v[216:219], v[2:5]
	s_setprio 0
	s_barrier
	s_add_i32 s50, s50, 2
	s_add_u32 s48, s48, 0x100
	s_addc_u32 s49, s49, 0
	s_cmpk_gt_u32 s50, 0x55
	s_mov_b64 s[12:13], s[16:17]
	s_cbranch_scc1 .Lkpeel_exit_7
